# strategy 7.5 packed-vs-scalar f32: v44 (v32 minus GEMM setprio) with 368 v_pk_mul/add/fma_f32 in the attention phase split into scalar f32 pairs (bit-identical)
# baseline (speedup 1.0000x reference)
;     ...
;     float bfox, bdil, bmax;
;     { const int l64 = tid & 63;
;       float g0 = fabsf(a.in[I_QGF][layer * 64 + l64]), g1 = fabsf(a.in[I_KGF][layer * 64 + l64]), g2 = fabsf(a.in[I_QGD][layer * 64 + l64]), g3 = fabsf(a.in[I_KGD][layer * 64 + l64]);
;       float rbm = 0.f;
;       for (int i = l64; i < 32 * 6; i += 64) rbm = fmaxf(rbm, a.in[I_RELB][i]);
; #pragma unroll
;       for (int o2 = 1; o2 < 64; o2 <<= 1) { g0 = fmaxf(g0, __shfl_xor(g0, o2)); g1 = fmaxf(g1, __shfl_xor(g1, o2)); g2 = fmaxf(g2, __shfl_xor(g2, o2)); g3 = fmaxf(g3, __shfl_xor(g3, o2)); rbm = fmaxf(rbm, __shfl_xor(rbm, o2)); }
;       bfox = 8.f * g0 * g1 * LOG2E * 1.01f; bdil = 8.f * g2 * g3 * LOG2E * 1.01f; bmax = fmaxf(rbm, 0.f) * LOG2E; }
;     const float fox_thr = 152.f + 2.f * bfox;
;     const bool fox_fixed = bfox < 40.f, dil_fixed = (bdil + bmax) < 40.f;
;     const float m_dil = bdil + bmax;
;     const unsigned l0 = (unsigned)(uintptr_t)lds;
.LBB0_412:
	v_readlane_b32 s4, v255, 13
	v_readlane_b32 s5, v255, 14
	v_writelane_b32 v254, s44, 18
	s_andn2_b64 vcc, exec, s[4:5]
	s_mov_b64 s[90:91], s[62:63]
	v_writelane_b32 v254, s45, 19
	s_cbranch_vccnz .LBB0_526
	s_waitcnt lgkmcnt(4)
	v_max_f32_e32 v2, v14, v14
	v_max_f32_e32 v3, v6, v6
	v_max_f32_e32 v2, v3, v2
	s_waitcnt lgkmcnt(3)
	v_max_f32_e32 v3, v13, v13
	v_max_f32_e32 v4, v7, v7
	v_max_f32_e32 v3, v4, v3
	v_mul_f32_e32 v2, 0x41000000, v2
	s_waitcnt lgkmcnt(2)
	v_max_f32_e32 v4, v12, v12
	v_max_f32_e32 v5, v9, v9
	v_mul_f32_e32 v2, v3, v2
	v_max_f32_e32 v4, v5, v4
	s_waitcnt lgkmcnt(1)
	v_max_f32_e32 v5, v11, v11
	v_max_f32_e32 v6, v8, v8
	v_mul_f32_e32 v2, 0x3fb8aa3b, v2
	v_max_f32_e32 v5, v6, v5
	v_mul_f32_e32 v164, 0x3f8147ae, v2
	v_mul_f32_e32 v2, 0x41000000, v4
	v_mul_f32_e32 v2, v5, v2
	s_mov_b32 s4, 0x3fb8aa3b
	v_writelane_b32 v254, s34, 20
	s_lshl_b64 s[10:11], s[34:35], 2
	v_readlane_b32 s2, v255, 9
	v_mul_f32_e32 v3, 0x3fb8aa3b, v2
	s_waitcnt lgkmcnt(0)
	v_max3_f32 v2, v1, v10, 0
	s_mov_b32 s5, 0x3f8147ae
	s_add_u32 s58, s2, s10
	v_readlane_b32 s2, v255, 10
	v_mul_f32_e32 v2, s4, v2
	v_mul_f32_e32 v3, s5, v3
	s_addc_u32 s59, s2, s11
	s_lshl_b32 s4, s18, 2
	s_mov_b32 s5, 0x42200000
	v_add_f32_e32 v166, v2, v3
	s_add_i32 s40, s4, 0
	s_lshl_b32 s4, s18, 4
	v_cmp_gt_f32_e64 s[22:23], s5, v164
	v_cmp_ngt_f32_e64 s[6:7], s5, v164
	v_cmp_ngt_f32_e64 s[8:9], s5, v166
	v_writelane_b32 v254, s35, 21
	s_and_b32 s42, s4, 48
	v_cmp_gt_f32_e64 s[4:5], s5, v166
	v_subrev_u32_e32 v167, 64, v18
	s_ashr_i32 s33, s12, 7
	v_writelane_b32 v254, s4, 22
	s_lshl_b32 s41, s18, 3
	s_lshl_b32 s43, s18, 10
	v_writelane_b32 v254, s5, 23
	v_cndmask_b32_e64 v2, 0, -v166, s[4:5]
	s_movk_i32 s4, 0x100
	v_cmp_gt_i32_e64 s[4:5], s4, v18
	s_lshl_b32 s2, s18, 5
	s_and_b32 s26, s41, 0xffffffe0
	v_writelane_b32 v254, s4, 24
	s_add_i32 s24, s43, 0
	v_fmaak_f32 v165, 2.0, v164, 0x43180000
	v_writelane_b32 v254, s5, 25
	s_movk_i32 s4, 0x81
	v_cmp_gt_u32_e64 s[4:5], s4, v167
	v_cmp_eq_u32_e64 s[10:11], 0, v18
	s_add_i32 s40, s40, 0x21400
	v_writelane_b32 v254, s4, 26
	s_ashr_i32 s27, s26, 31
	s_add_i32 s44, s24, 0xc000
	v_writelane_b32 v254, s5, 27
	s_add_i32 s4, 0, 0x21600
	v_lshl_add_u32 v168, v18, 2, s4
	s_mul_i32 s4, s18, 0x1200
	s_add_i32 s49, s4, 0
	s_lshl_b32 s4, s18, 7
	s_lshl_b32 s5, s33, 8
	s_sub_i32 s4, s4, s5
	s_add_i32 s68, s4, 0
	s_add_i32 s4, s68, 0x21614
	v_writelane_b32 v254, s4, 28
	s_add_i32 s4, s33, 3
	s_add_i32 s43, s33, 2
	v_mov_b32_e32 v3, v2
	v_mov_b32_e32 v4, v2
	v_mov_b32_e32 v5, v2
	v_mov_b32_e32 v6, v2
	v_mov_b32_e32 v7, v2
	v_mov_b32_e32 v8, v2
	v_mov_b32_e32 v9, v2
	v_mov_b32_e32 v10, v2
	v_mov_b32_e32 v11, v2
	v_mov_b32_e32 v12, v2
	v_mov_b32_e32 v13, v2
	v_mov_b32_e32 v14, v2
	v_mov_b32_e32 v15, v2
	v_mov_b32_e32 v16, v2
	v_mov_b32_e32 v17, v2
	s_ashr_i32 s47, s2, 31
	s_add_i32 s48, s2, 0xf00
	s_add_i32 s49, s49, 0x18000
	s_lshl_b32 s69, s33, 13
	v_writelane_b32 v254, s4, 29
	s_mov_b64 s[20:21], 0
	v_readlane_b32 s73, v255, 49
	s_branch .LBB0_415

; #define LAS __attribute__((address_space(3)))
; #define SB_ISSUE(i) do { const int j_ = jhi - (i); dma_kv(lds, (i) & 3, Kb + (size_t)j_ * 4096, Vb + (size_t)j_ * 4096, 64, wid, lane); } while (0)
; __device__ __forceinline__ void qkt(f32x16& p0, f32x16& p1, const LAS unsigned char* Kb, const bf16x8 (&qr)[4], float cinit, int r32, int hi) {
;     const int sw = (r32 >> 1) & 7;
;     bf16x8 kf[8];
; #pragma unroll
;     for (int d0 = 0; d0 < 4; ++d0) {
;         unsigned ka = (unsigned)(uintptr_t)Kb + r32 * 128 + (((2 * d0 + hi) ^ sw) << 4); asm volatile("" : "+v"(ka));
;         kf[2 * d0] = *(const LAS bf16x8*)(uintptr_t)ka;
;         kf[2 * d0 + 1] = *(const LAS bf16x8*)(uintptr_t)(ka + 4096);
;     }
; #pragma unroll
;     for (int r = 0; r < 16; ++r) { p0[r] = cinit; p1[r] = cinit; }
;     __builtin_amdgcn_sched_barrier(0);
; #pragma unroll
;     for (int d0 = 0; d0 < 4; ++d0) {
;         p0 = __builtin_amdgcn_mfma_f32_32x32x16_bf16(kf[2 * d0], qr[d0], p0, 0, 0, 0);
;         p1 = __builtin_amdgcn_mfma_f32_32x32x16_bf16(kf[2 * d0 + 1], qr[d0], p1, 0, 0, 0);
;     }
;     ...
;             const int v2 = u - AT_NFOX - AT_NDIL, qb = 15 - v2 / 48, bh = v2 % 48, b = bh / 6, h = bh % 6, q0 = qb * 256;
;             const size_t rb = (size_t)b * S;
;             const bf16_t* Kb = proj + ((size_t)(40 + h) * NTOK + rb) * 64;
;             const bf16_t* Vb = proj + ((size_t)(46 + h) * NTOK + rb) * 64;
;             const int tw = q0 + 32 * wid, t = tw + r32;
;             const int jhi = (q0 + 254) >> 6, jhi_w = (tw + 30) >> 6, T = jhi + 1;
;             float P_run = 1.f; bool wdone = false;
;             int issued = 3; bool alldone = false;
;             for (int i = 0; i < T; ++i) {
;                 if (i > 0) {
;                     const int n = issued - 1 - i; AT_WAIT_BAR(2, n);
;                     int c = 0;
; #pragma unroll
;                     for (int k = 0; k < 8; ++k) c += flags[((i - 1) & 1) * 8 + k];
;                     alldone = (c == 8);
;                 }
;                 if (alldone) break;
;                 if (issued < T) { SB_ISSUE(issued); ++issued; }
;                 const int j = jhi - i, buf = i & 3;
;                 if (j <= jhi_w && !wdone) {
;                     f32x16 p0, p1;
;                     qkt(p0, p1, lds + L_K + buf * 8192, qr, 0.f, r32, hi);
.LBB0_423:
	s_or_b64 exec, exec, s[18:19]
	s_cmpk_gt_i32 s73, 0x1ff
	s_cselect_b64 s[28:29], -1, 0
	v_and_b32_e32 v169, 31, v148
	v_ashrrev_i32_e32 v116, 5, v148
	s_mov_b64 s[18:19], -1
	s_and_b64 vcc, exec, s[28:29]
	s_cbranch_vccz .LBB0_431
	s_cmpk_gt_u32 s73, 0xaff
	s_cbranch_scc0 .LBB0_483
	s_add_i32 s4, s73, 0xf500
	s_and_b32 s5, s4, 0xffff
	s_mul_i32 s5, s5, 0xaaab
	s_lshr_b32 s5, s5, 21
	s_mul_i32 s14, s5, 48
	s_sub_i32 s4, s4, s14
	s_mul_i32 s14, s4, 0xab
	s_bfe_u32 s14, s14, 0x6000a
	s_mul_i32 s15, s14, 6
	s_sub_i32 s4, s4, s15
	s_and_b32 s4, s4, 0xff
	s_lshl_b32 s39, s5, 8
	s_lshl_b32 s5, s14, 12
	s_lshl_b32 s4, s4, 15
	s_add_i32 s4, s4, s5
	v_ashrrev_i32_e32 v1, 3, v148
	s_lshl_b32 s4, s4, 7
	v_add_u32_e32 v18, s41, v1
	s_add_i32 s5, s4, 0xa000000
	v_lshrrev_b32_e32 v19, 1, v18
	s_add_u32 s18, s96, s5
	v_xor_b32_e32 v20, v19, v148
	v_ashrrev_i32_e32 v19, 31, v18
	s_addc_u32 s19, s97, 0
	v_lshlrev_b64 v[18:19], 7, v[18:19]
	v_lshlrev_b32_e32 v20, 4, v20
	v_lshl_add_u64 v[18:19], s[18:19], 0, v[18:19]
	v_and_b32_e32 v34, 0x70, v20
	v_lshl_add_u64 v[86:87], v[18:19], 0, v[34:35]
	v_ashrrev_i32_e32 v18, 2, v148
	s_add_i32 s4, s4, 0xb800000
	v_add_u32_e32 v18, s42, v18
	s_add_u32 s20, s96, s4
	v_ashrrev_i32_e32 v19, 31, v18
	s_addc_u32 s21, s97, 0
	v_lshlrev_b64 v[18:19], 7, v[18:19]
	v_lshlrev_b32_e32 v20, 3, v148
	v_lshl_add_u64 v[18:19], s[20:21], 0, v[18:19]
	v_and_b32_e32 v20, 24, v20
	v_lshl_add_u64 v[18:19], s[26:27], 1, v[18:19]
	v_lshlrev_b32_e32 v34, 1, v20
	v_lshl_add_u64 v[88:89], v[18:19], 0, v[34:35]
	v_lshrrev_b32_e32 v18, 1, v148
	v_bitop3_b32 v19, v18, v116, 7 bitop3:0x6c
	v_lshlrev_b32_e32 v102, 4, v19
	v_add_u32_e32 v19, 2, v116
	v_bitop3_b32 v19, v19, v18, 7 bitop3:0x78
	s_sub_i32 s38, s2, s39
	v_lshlrev_b32_e32 v103, 4, v19
	v_add_u32_e32 v19, 4, v116
	s_add_i32 s4, s38, 0xf00
	v_bitop3_b32 v19, v19, v18, 7 bitop3:0x78
	v_or_b32_e32 v84, s4, v169
	s_add_i32 s4, s38, 0xf1e
	v_lshlrev_b32_e32 v104, 4, v19
	v_add_u32_e32 v19, 6, v116
	s_sub_i32 s30, 0xfc0, s39
	s_ashr_i32 s37, s4, 6
	v_bitop3_b32 v18, v19, v18, 7 bitop3:0x78
	v_bfe_u32 v19, v148, 2, 2
	s_mov_b32 s4, 0x3fffffc
	v_lshlrev_b32_e32 v105, 4, v18
	v_lshlrev_b32_e32 v18, 1, v148
	v_and_or_b32 v1, v1, s4, v19
	s_lshl_b32 s4, s30, 7
	v_and_b32_e32 v18, 32, v18
	v_lshlrev_b32_e32 v1, 6, v1
	s_add_i32 s66, s4, 0xffffa000
	v_or3_b32 v107, v18, v1, v20
	v_lshl_add_u64 v[18:19], v[86:87], 0, s[66:67]
	s_add_i32 s4, s24, 0x6000
	s_mov_b32 s5, m0
	s_mov_b32 m0, s4
	s_nop 0
	global_load_lds_dwordx4 v[18:19], off
	s_mov_b32 m0, s5
	v_lshl_add_u64 v[20:21], v[88:89], 0, s[66:67]
	s_add_i32 s4, s24, 0x12000
	s_mov_b32 s5, m0
	s_mov_b32 m0, s4
	s_nop 0
	global_load_lds_dwordx4 v[20:21], off
	s_mov_b32 m0, s5
	s_lshr_b32 s36, s30, 6
	s_addk_i32 s38, 0xec1
	v_lshlrev_b32_e32 v85, 7, v169
	v_lshlrev_b32_e32 v106, 2, v116
	v_cmp_gt_u32_e64 s[18:19], 32, v148
	s_cmp_gt_i32 s36, s37
	s_cbranch_scc1 .LBB0_458
	v_add_u32_e32 v1, 0, v85
	v_add_u32_e32 v22, v1, v102
	v_add_u32_e32 v26, v1, v103
	ds_read_b128 v[18:21], v22
	ds_read_b128 v[22:25], v22 offset:4096
	ds_read_b128 v[52:55], v26
	ds_read_b128 v[56:59], v26 offset:4096
	v_add_u32_e32 v26, v1, v104
	v_add_u32_e32 v1, v1, v105
	ds_read_b128 v[60:63], v26
	ds_read_b128 v[64:67], v26 offset:4096
	ds_read_b128 v[68:71], v1
	ds_read_b128 v[72:75], v1 offset:4096
	s_waitcnt lgkmcnt(7)
	v_mfma_f32_32x32x16_bf16 v[36:51], v[18:21], v[132:135], 0
	s_cmp_lt_i32 s30, s38
	s_mov_b64 s[20:21], -1
	s_waitcnt lgkmcnt(6)
	v_mfma_f32_32x32x16_bf16 v[18:33], v[22:25], v[132:135], 0
	s_waitcnt lgkmcnt(5)
	v_mfma_f32_32x32x16_bf16 v[36:51], v[52:55], v[136:139], v[36:51]
	s_waitcnt lgkmcnt(4)
	v_mfma_f32_32x32x16_bf16 v[18:33], v[56:59], v[136:139], v[18:33]
	s_waitcnt lgkmcnt(3)
	v_mfma_f32_32x32x16_bf16 v[36:51], v[60:63], v[140:143], v[36:51]
	s_waitcnt lgkmcnt(2)
	v_mfma_f32_32x32x16_bf16 v[18:33], v[64:67], v[140:143], v[18:33]
	s_waitcnt lgkmcnt(1)
	v_mfma_f32_32x32x16_bf16 v[36:51], v[68:71], v[144:147], v[36:51]
	s_waitcnt lgkmcnt(0)
	v_mfma_f32_32x32x16_bf16 v[18:33], v[72:75], v[144:147], v[18:33]
	s_nop 9
	v_exp_f32_e32 v97, v39
	v_exp_f32_e32 v95, v38
	v_exp_f32_e32 v96, v37
	v_exp_f32_e32 v94, v36
	v_exp_f32_e32 v93, v43
	v_exp_f32_e32 v92, v42
	v_exp_f32_e32 v91, v41
	v_exp_f32_e32 v90, v40
	v_exp_f32_e32 v82, v47
	v_exp_f32_e32 v83, v46
	v_exp_f32_e32 v81, v45
	v_exp_f32_e32 v80, v44
	v_exp_f32_e32 v79, v51
	v_exp_f32_e32 v78, v50
	v_exp_f32_e32 v77, v49
	v_exp_f32_e32 v76, v48
	v_exp_f32_e32 v75, v21
	v_exp_f32_e32 v74, v20
	v_exp_f32_e32 v73, v19
	v_exp_f32_e32 v72, v18
	v_exp_f32_e32 v71, v25
	v_exp_f32_e32 v70, v24
	v_exp_f32_e32 v69, v23
	v_exp_f32_e32 v68, v22
	v_exp_f32_e32 v67, v29
	v_exp_f32_e32 v66, v28
	v_exp_f32_e32 v65, v27
	v_exp_f32_e32 v64, v26
	v_exp_f32_e32 v63, v33
	v_exp_f32_e32 v62, v32
	v_exp_f32_e32 v34, v31
	v_exp_f32_e32 v1, v30
	s_cbranch_scc1 .LBB0_428
;     ...
;                     if (diag) { asm volatile("; stick-breaking: diagonal tile (masked)" ::: "memory"); SB_GROUPS(true) } else { SB_GROUPS(false) }
	v_add_f32_e32 v19, 1.0, v95
	v_rcp_f32_e32 v20, v19
	v_add_f32_e32 v19, 1.0, v96
	v_rcp_f32_e32 v21, v19
	v_add_f32_e32 v19, 1.0, v94
	v_rcp_f32_e32 v22, v19
	v_add_f32_e32 v19, 1.0, v93
	v_add_f32_e32 v18, 1.0, v97
	v_rcp_f32_e32 v23, v19
	v_add_f32_e32 v19, 1.0, v92
	v_rcp_f32_e32 v18, v18
	v_rcp_f32_e32 v24, v19
	v_add_f32_e32 v19, 1.0, v91
	v_rcp_f32_e32 v28, v19
	v_add_f32_e32 v19, 1.0, v90
	v_add_u32_e32 v56, s30, v106
	v_rcp_f32_e32 v30, v19
	v_or_b32_e32 v19, 3, v56
	v_add_u32_e32 v25, 10, v56
	v_cmp_lt_i32_e32 vcc, v19, v84
	v_add_u32_e32 v26, 11, v56
	v_add_u32_e32 v37, 26, v56
	v_cndmask_b32_e32 v19, 1.0, v18, vcc
	v_cmp_lt_i32_e32 vcc, v25, v84
	v_add_u32_e32 v40, 27, v56
	v_mov_b32_e32 v200, v19
	v_cndmask_b32_e32 v18, 1.0, v24, vcc
	v_or_b32_e32 v24, 2, v56
	v_cmp_lt_i32_e32 vcc, v24, v84
	v_add_f32_e32 v44, 1.0, v72
	v_rcp_f32_e32 v44, v44
	v_cndmask_b32_e32 v25, 1.0, v20, vcc
	v_cmp_lt_i32_e32 vcc, v26, v84
	v_or_b32_e32 v20, 1, v56
	v_add_f32_e32 v48, 1.0, v68
	v_cndmask_b32_e32 v24, 1.0, v23, vcc
	v_add_u32_e32 v23, 9, v56
	v_cmp_lt_i32_e32 vcc, v20, v84
	v_mul_f32_e32 v26, v18, v24
	v_mul_f32_e32 v27, v19, v25
	v_mov_b32_e32 v25, v201
	v_cndmask_b32_e32 v21, 1.0, v21, vcc
	v_cmp_lt_i32_e32 vcc, v23, v84
	v_mov_b32_e32 v18, v27
	v_mov_b32_e32 v23, v27
	v_cndmask_b32_e32 v20, 1.0, v28, vcc
	v_mul_f32_e32 v28, v20, v26
	v_mul_f32_e32 v29, v21, v27
	v_add_u32_e32 v20, 8, v56
	v_cmp_lt_i32_e32 vcc, v56, v84
	v_mov_b32_e32 v27, v24
	v_mov_b32_e32 v31, v29
	v_cndmask_b32_e32 v21, 1.0, v22, vcc
	v_cmp_lt_i32_e32 vcc, v20, v84
	v_mov_b32_e32 v22, v29
	v_sub_f32_e32 v24, v24, v26
	v_sub_f32_e32 v25, v25, v27
	v_cndmask_b32_e32 v20, 1.0, v30, vcc
	v_mul_f32_e32 v20, v20, v28
	v_mul_f32_e32 v21, v21, v29
	v_mov_b32_e32 v29, v26
	v_mov_b32_e32 v26, v20
	v_mov_b32_e32 v27, v28
	v_mov_b32_e32 v30, v21
	v_sub_f32_e32 v26, v28, v26
	v_sub_f32_e32 v27, v29, v27
	v_add_f32_e32 v29, 1.0, v83
	v_sub_f32_e32 v22, v22, v30
	v_sub_f32_e32 v23, v23, v31
	v_rcp_f32_e32 v30, v29
	v_add_f32_e32 v29, 1.0, v81
	v_rcp_f32_e32 v31, v29
	v_add_f32_e32 v29, 1.0, v80
	v_rcp_f32_e32 v32, v29
	v_add_f32_e32 v29, 1.0, v79
	v_add_f32_e32 v28, 1.0, v82
	v_rcp_f32_e32 v33, v29
	v_add_f32_e32 v29, 1.0, v78
	v_rcp_f32_e32 v28, v28
	v_rcp_f32_e32 v36, v29
	v_add_f32_e32 v29, 1.0, v77
	v_rcp_f32_e32 v38, v29
	v_add_f32_e32 v29, 1.0, v76
	v_rcp_f32_e32 v39, v29
	v_add_u32_e32 v29, 19, v56
	v_cmp_lt_i32_e32 vcc, v29, v84
	v_sub_f32_e32 v18, v200, v18
	v_sub_f32_e32 v19, v201, v19
	v_rcp_f32_e32 v48, v48
	v_cndmask_b32_e32 v29, 1.0, v28, vcc
	v_cmp_lt_i32_e32 vcc, v37, v84
	v_mov_b32_e32 v200, v29
	v_add_u32_e32 v58, 58, v56
	v_cndmask_b32_e32 v28, 1.0, v36, vcc
	v_add_u32_e32 v36, 18, v56
	v_cmp_lt_i32_e32 vcc, v36, v84
	s_mov_b64 s[20:21], 0
	s_nop 0
	v_cndmask_b32_e32 v37, 1.0, v30, vcc
	v_cmp_lt_i32_e32 vcc, v40, v84
	v_add_u32_e32 v30, 17, v56
	s_nop 0
	v_cndmask_b32_e32 v36, 1.0, v33, vcc
	v_add_u32_e32 v33, 25, v56
	v_cmp_lt_i32_e32 vcc, v30, v84
	v_mul_f32_e32 v40, v28, v36
	v_mul_f32_e32 v41, v29, v37
	v_mov_b32_e32 v37, v201
	v_cndmask_b32_e32 v31, 1.0, v31, vcc
	v_cmp_lt_i32_e32 vcc, v33, v84
	v_add_u32_e32 v33, 24, v56
	v_mov_b32_e32 v28, v41
	v_cndmask_b32_e32 v30, 1.0, v38, vcc
	v_mul_f32_e32 v42, v30, v40
	v_mul_f32_e32 v43, v31, v41
	v_add_u32_e32 v30, 16, v56
	v_cmp_lt_i32_e32 vcc, v30, v84
	v_sub_f32_e32 v28, v200, v28
	v_sub_f32_e32 v29, v201, v29
	s_nop 0
	v_cndmask_b32_e32 v31, 1.0, v32, vcc
	v_cmp_lt_i32_e32 vcc, v33, v84
	s_nop 1
	v_cndmask_b32_e32 v30, 1.0, v39, vcc
	v_mul_f32_e32 v32, v30, v42
	v_mul_f32_e32 v33, v31, v43
	v_mov_b32_e32 v30, v43
	v_mov_b32_e32 v31, v41
	v_mov_b32_e32 v38, v33
	v_mov_b32_e32 v39, v43
	v_mov_b32_e32 v41, v36
	v_sub_f32_e32 v30, v30, v38
	v_sub_f32_e32 v31, v31, v39
	v_sub_f32_e32 v38, v36, v40
	v_sub_f32_e32 v39, v37, v41
	v_mov_b32_e32 v43, v40
	v_mov_b32_e32 v36, v32
	v_mov_b32_e32 v37, v42
	v_sub_f32_e32 v36, v42, v36
	v_sub_f32_e32 v37, v43, v37
	v_add_f32_e32 v42, 1.0, v75
	v_rcp_f32_e32 v42, v42
	v_add_f32_e32 v43, 1.0, v74
	v_rcp_f32_e32 v43, v43
	v_add_u32_e32 v41, 35, v56
	v_cmp_lt_i32_e32 vcc, v41, v84
	v_add_u32_e32 v41, 34, v56
	v_add_u32_e32 v40, 32, v56
	v_cndmask_b32_e32 v200, 1.0, v42, vcc
	v_cmp_lt_i32_e32 vcc, v41, v84
	v_add_u32_e32 v42, 33, v56
	s_nop 0
	v_cndmask_b32_e32 v41, 1.0, v43, vcc
	v_add_f32_e32 v43, 1.0, v73
	v_rcp_f32_e32 v43, v43
	v_cmp_lt_i32_e32 vcc, v42, v84
	v_mul_f32_e32 v42, v200, v41
	v_mov_b32_e32 v47, v42
	v_cndmask_b32_e32 v45, 1.0, v43, vcc
	v_cmp_lt_i32_e32 vcc, v40, v84
	v_mul_f32_e32 v46, v45, v42
	v_mov_b32_e32 v43, v200
	v_cndmask_b32_e32 v44, 1.0, v44, vcc
	v_mul_f32_e32 v44, v44, v46
	v_mov_b32_e32 v45, v46
	v_sub_f32_e32 v40, v200, v42
	v_sub_f32_e32 v41, v201, v43
	v_sub_f32_e32 v42, v46, v44
	v_sub_f32_e32 v43, v47, v45
	v_add_f32_e32 v46, 1.0, v71
	v_rcp_f32_e32 v46, v46
	v_add_f32_e32 v47, 1.0, v70
	v_rcp_f32_e32 v47, v47
	v_add_u32_e32 v45, 43, v56
	v_cmp_lt_i32_e32 vcc, v45, v84
	v_add_u32_e32 v45, 42, v56
	s_nop 0
	v_cndmask_b32_e32 v200, 1.0, v46, vcc
	v_cmp_lt_i32_e32 vcc, v45, v84
	v_add_u32_e32 v46, 41, v56
	v_mov_b32_e32 v49, v200
	v_cndmask_b32_e32 v45, 1.0, v47, vcc
	v_add_f32_e32 v47, 1.0, v69
	v_rcp_f32_e32 v47, v47
	v_cmp_lt_i32_e32 vcc, v46, v84
	v_add_u32_e32 v46, 40, v56
	s_nop 0
	v_cndmask_b32_e32 v50, 1.0, v47, vcc
	v_cmp_lt_i32_e32 vcc, v46, v84
	s_nop 1
	v_cndmask_b32_e32 v51, 1.0, v48, vcc
	v_mul_f32_e32 v48, v200, v45
	v_mul_f32_e32 v52, v50, v48
	v_mul_f32_e32 v50, v51, v52
	v_mov_b32_e32 v53, v48
	v_mov_b32_e32 v51, v52
	v_sub_f32_e32 v46, v200, v48
	v_sub_f32_e32 v47, v201, v49
	v_sub_f32_e32 v48, v52, v50
	v_sub_f32_e32 v49, v53, v51
;     ...
;                     if (diag) { asm volatile("; stick-breaking: diagonal tile (masked)" ::: "memory"); SB_GROUPS(true) } else { SB_GROUPS(false) }
	v_add_f32_e32 v52, 1.0, v65
	v_rcp_f32_e32 v54, v52
	v_add_f32_e32 v52, 1.0, v64
	v_add_f32_e32 v45, 1.0, v67
	v_rcp_f32_e32 v57, v52
	v_add_f32_e32 v52, 1.0, v63
	v_rcp_f32_e32 v45, v45
	v_rcp_f32_e32 v55, v52
	v_add_f32_e32 v52, 1.0, v62
	v_add_f32_e32 v53, 1.0, v34
	v_add_f32_e32 v51, 1.0, v66
	v_rcp_f32_e32 v52, v52
	v_rcp_f32_e32 v60, v53
	v_add_f32_e32 v53, 1.0, v1
	v_rcp_f32_e32 v51, v51
	v_rcp_f32_e32 v61, v53
	v_add_u32_e32 v53, 51, v56
	v_cmp_lt_i32_e32 vcc, v53, v84
	s_nop 1
	v_cndmask_b32_e32 v53, 1.0, v45, vcc
	v_cmp_lt_i32_e32 vcc, v58, v84
	v_add_u32_e32 v45, 50, v56
	v_add_u32_e32 v58, 59, v56
	v_cndmask_b32_e32 v52, 1.0, v52, vcc
	v_cmp_lt_i32_e32 vcc, v45, v84
	v_add_u32_e32 v45, 49, v56
	v_mov_b32_e32 v200, v53
	v_cndmask_b32_e32 v59, 1.0, v51, vcc
	v_cmp_lt_i32_e32 vcc, v58, v84
	v_add_u32_e32 v51, 57, v56
	s_nop 0
	v_cndmask_b32_e32 v58, 1.0, v55, vcc
	v_cmp_lt_i32_e32 vcc, v45, v84
	v_add_u32_e32 v45, 48, v56
	v_mul_f32_e32 v98, v52, v58
	v_mul_f32_e32 v99, v53, v59
	v_cndmask_b32_e32 v55, 1.0, v54, vcc
	v_cmp_lt_i32_e32 vcc, v51, v84
	v_add_u32_e32 v51, 56, v56
	v_mov_b32_e32 v52, v99
	v_cndmask_b32_e32 v54, 1.0, v60, vcc
	v_cmp_lt_i32_e32 vcc, v45, v84
	v_mul_f32_e32 v100, v54, v98
	v_mul_f32_e32 v101, v55, v99
	v_mov_b32_e32 v59, v201
	v_cndmask_b32_e32 v55, 1.0, v57, vcc
	v_cmp_lt_i32_e32 vcc, v51, v84
	v_sub_f32_e32 v52, v200, v52
	v_sub_f32_e32 v53, v201, v53
	s_nop 0
	v_cndmask_b32_e32 v54, 1.0, v61, vcc
	v_mul_f32_e32 v56, v54, v100
	v_mul_f32_e32 v57, v55, v101
	v_mov_b32_e32 v54, v101
	v_mov_b32_e32 v55, v99
	v_mov_b32_e32 v60, v57
	v_mov_b32_e32 v61, v101
	v_mov_b32_e32 v99, v58
	v_sub_f32_e32 v54, v54, v60
	v_sub_f32_e32 v55, v55, v61
	v_sub_f32_e32 v60, v58, v98
	v_sub_f32_e32 v61, v59, v99
	v_mov_b32_e32 v101, v98
	v_mov_b32_e32 v58, v56
	v_mov_b32_e32 v59, v100
	v_sub_f32_e32 v58, v100, v58
	v_sub_f32_e32 v59, v101, v59
.LBB0_428:
	s_andn2_b64 vcc, exec, s[20:21]
	s_cbranch_vccnz .LBB0_430
	v_add_f32_e32 v18, 1.0, v97
	v_rcp_f32_e32 v25, v18
	v_add_f32_e32 v18, 1.0, v95
	v_rcp_f32_e32 v19, v18
	v_add_f32_e32 v18, 1.0, v96
	v_rcp_f32_e32 v21, v18
	v_add_f32_e32 v18, 1.0, v94
	v_rcp_f32_e32 v23, v18
	v_add_f32_e32 v18, 1.0, v93
	v_rcp_f32_e32 v24, v18
	v_add_f32_e32 v18, 1.0, v92
	v_rcp_f32_e32 v18, v18
	v_add_f32_e32 v20, 1.0, v91
	v_rcp_f32_e32 v20, v20
	v_add_f32_e32 v22, 1.0, v90
	v_rcp_f32_e32 v22, v22
	v_mul_f32_e32 v26, v24, v18
	v_mul_f32_e32 v27, v25, v19
	v_mov_b32_e32 v200, v25
	v_mul_f32_e32 v28, v20, v26
	v_mul_f32_e32 v29, v21, v27
	v_mov_b32_e32 v18, v27
	v_mov_b32_e32 v19, v25
	v_mul_f32_e32 v20, v22, v28
	v_mul_f32_e32 v21, v23, v29
	v_mov_b32_e32 v23, v27
	v_mov_b32_e32 v25, v201
	v_mov_b32_e32 v27, v24
	v_mov_b32_e32 v22, v29
	v_mov_b32_e32 v31, v29
	v_sub_f32_e32 v24, v24, v26
	v_sub_f32_e32 v25, v25, v27
	v_mov_b32_e32 v29, v26
	v_mov_b32_e32 v26, v20
	v_mov_b32_e32 v27, v28
	v_sub_f32_e32 v26, v28, v26
	v_sub_f32_e32 v27, v29, v27
	v_add_f32_e32 v28, 1.0, v82
	v_rcp_f32_e32 v37, v28
	v_add_f32_e32 v28, 1.0, v83
	v_mov_b32_e32 v30, v21
	v_rcp_f32_e32 v29, v28
	v_add_f32_e32 v28, 1.0, v81
	v_sub_f32_e32 v22, v22, v30
	v_sub_f32_e32 v23, v23, v31
	v_rcp_f32_e32 v31, v28
	v_add_f32_e32 v28, 1.0, v80
	v_rcp_f32_e32 v33, v28
	v_add_f32_e32 v28, 1.0, v79
	v_rcp_f32_e32 v36, v28
	v_add_f32_e32 v28, 1.0, v78
	v_rcp_f32_e32 v28, v28
	v_add_f32_e32 v30, 1.0, v77
	v_rcp_f32_e32 v30, v30
	v_add_f32_e32 v32, 1.0, v76
	v_rcp_f32_e32 v32, v32
	v_mul_f32_e32 v40, v36, v28
	v_mul_f32_e32 v41, v37, v29
	v_sub_f32_e32 v18, v200, v18
	v_sub_f32_e32 v19, v201, v19
	v_mul_f32_e32 v42, v30, v40
	v_mul_f32_e32 v43, v31, v41
	v_mov_b32_e32 v200, v37
	v_mul_f32_e32 v32, v32, v42
	v_mul_f32_e32 v33, v33, v43
	v_mov_b32_e32 v28, v41
	v_mov_b32_e32 v29, v37
	v_mov_b32_e32 v30, v43
	v_mov_b32_e32 v31, v41
	v_mov_b32_e32 v38, v33
	v_mov_b32_e32 v39, v43
	v_mov_b32_e32 v37, v201
	v_mov_b32_e32 v41, v36
	v_sub_f32_e32 v30, v30, v38
	v_sub_f32_e32 v31, v31, v39
	v_sub_f32_e32 v38, v36, v40
	v_sub_f32_e32 v39, v37, v41
	v_mov_b32_e32 v43, v40
	v_add_f32_e32 v40, 1.0, v75
	v_sub_f32_e32 v28, v200, v28
	v_sub_f32_e32 v29, v201, v29
	v_rcp_f32_e32 v200, v40
	v_add_f32_e32 v40, 1.0, v74
	v_rcp_f32_e32 v40, v40
	v_add_f32_e32 v41, 1.0, v73
	v_rcp_f32_e32 v44, v41
	v_add_f32_e32 v41, 1.0, v72
	v_rcp_f32_e32 v45, v41
	v_mov_b32_e32 v36, v32
	v_mov_b32_e32 v37, v42
	v_sub_f32_e32 v36, v42, v36
	v_sub_f32_e32 v37, v43, v37
	v_mul_f32_e32 v42, v200, v40
	v_mul_f32_e32 v46, v44, v42
	v_mov_b32_e32 v43, v200
	v_mul_f32_e32 v44, v45, v46
	v_mov_b32_e32 v47, v42
	v_mov_b32_e32 v45, v46
	v_sub_f32_e32 v40, v200, v42
	v_sub_f32_e32 v41, v201, v43
	v_sub_f32_e32 v42, v46, v44
	v_sub_f32_e32 v43, v47, v45
	v_add_f32_e32 v45, 1.0, v71
	v_rcp_f32_e32 v200, v45
	v_add_f32_e32 v45, 1.0, v70
	v_rcp_f32_e32 v45, v45
	v_add_f32_e32 v46, 1.0, v69
	v_rcp_f32_e32 v50, v46
	v_add_f32_e32 v46, 1.0, v68
	v_rcp_f32_e32 v51, v46
	v_mul_f32_e32 v48, v200, v45
	v_mul_f32_e32 v52, v50, v48
	v_add_f32_e32 v45, 1.0, v67
	v_mov_b32_e32 v49, v200
	v_mul_f32_e32 v50, v51, v52
	v_mov_b32_e32 v53, v48
	v_mov_b32_e32 v51, v52
	v_rcp_f32_e32 v59, v45
	v_add_f32_e32 v45, 1.0, v66
	v_sub_f32_e32 v46, v200, v48
	v_sub_f32_e32 v47, v201, v49
	v_sub_f32_e32 v48, v52, v50
	v_sub_f32_e32 v49, v53, v51
	v_rcp_f32_e32 v53, v45
	v_add_f32_e32 v45, 1.0, v65
	v_rcp_f32_e32 v55, v45
	v_add_f32_e32 v45, 1.0, v64
	v_rcp_f32_e32 v57, v45
	v_add_f32_e32 v45, 1.0, v63
	v_rcp_f32_e32 v58, v45
	v_add_f32_e32 v45, 1.0, v62
	v_rcp_f32_e32 v52, v45
	v_add_f32_e32 v34, 1.0, v34
	v_rcp_f32_e32 v54, v34
	v_add_f32_e32 v1, 1.0, v1
	v_rcp_f32_e32 v56, v1
	v_mul_f32_e32 v62, v58, v52
	v_mul_f32_e32 v63, v59, v53
	v_mov_b32_e32 v200, v59
	v_mul_f32_e32 v64, v54, v62
	v_mul_f32_e32 v65, v55, v63
	v_mov_b32_e32 v52, v63
	v_mul_f32_e32 v56, v56, v64
	v_mul_f32_e32 v57, v57, v65
	v_mov_b32_e32 v53, v59
	v_mov_b32_e32 v54, v65
	v_mov_b32_e32 v55, v63
	v_mov_b32_e32 v60, v57
	v_mov_b32_e32 v61, v65
	v_mov_b32_e32 v59, v201
	v_mov_b32_e32 v63, v58
	v_sub_f32_e32 v54, v54, v60
	v_sub_f32_e32 v55, v55, v61
	v_sub_f32_e32 v60, v58, v62
	v_sub_f32_e32 v61, v59, v63
	v_mov_b32_e32 v65, v62
	v_mov_b32_e32 v58, v56
	v_mov_b32_e32 v59, v64
	v_sub_f32_e32 v52, v200, v52
	v_sub_f32_e32 v53, v201, v53
	v_sub_f32_e32 v58, v64, v58
	v_sub_f32_e32 v59, v65, v59
; #define LAS __attribute__((address_space(3)))
; __device__ __forceinline__ void pv(f32x16 (&o)[2], const f32x16& p0, const f32x16& p1, const LAS unsigned char* Vb, int lane) {
;     const int hi = lane >> 5;
;     unsigned va = (unsigned)(uintptr_t)Vb + ((lane >> 4) & 1) * 32 + (lane & 3) * 8 + (4 * hi + ((lane & 15) >> 2)) * 64; asm volatile("" : "+v"(va));
;     const LAS unsigned char* vp = (const LAS unsigned char*)(uintptr_t)va;
;     s16x4 vlo[8], vhh[8];
; #pragma unroll
;     for (int i = 0; i < 8; ++i) { vlo[i] = vtr(vp + (i >> 2) * 4096 + (i & 3) * 1024); vhh[i] = vtr(vp + (i >> 2) * 4096 + (i & 3) * 1024 + 512); }
;     u32x4 pw[4];
;     pw[0] = (u32x4){cvtpk(p0[0], p0[1]), cvtpk(p0[2], p0[3]), cvtpk(p0[4], p0[5]), cvtpk(p0[6], p0[7])};
;     pw[1] = (u32x4){cvtpk(p0[8], p0[9]), cvtpk(p0[10], p0[11]), cvtpk(p0[12], p0[13]), cvtpk(p0[14], p0[15])};
;     pw[2] = (u32x4){cvtpk(p1[0], p1[1]), cvtpk(p1[2], p1[3]), cvtpk(p1[4], p1[5]), cvtpk(p1[6], p1[7])};
;     pw[3] = (u32x4){cvtpk(p1[8], p1[9]), cvtpk(p1[10], p1[11]), cvtpk(p1[12], p1[13]), cvtpk(p1[14], p1[15])};
;     __builtin_amdgcn_sched_barrier(0);
; #pragma unroll
;     for (int d0 = 0; d0 < 2; ++d0)
; #pragma unroll
;         for (int ks = 0; ks < 4; ++ks) {
;             const s16x4 lo = vlo[4 * d0 + ks], hh = vhh[4 * d0 + ks];
;             const bf16x8 vf = (bf16x8){lo[0], lo[1], lo[2], lo[3], hh[0], hh[1], hh[2], hh[3]};
;     ...
;                     float pt = P_run;
; #pragma unroll
;                     for (int k = 7; k >= 0; --k) {
;                         auto rr = __builtin_amdgcn_permlane32_swap(__float_as_uint(gp[k]), __float_as_uint(gp[k]), false, false);
;                         const float lo = __uint_as_float(rr[0]), up = __uint_as_float(rr[1]);
;                         const float mul = hi == 0 ? pt * up : pt;
;                         const int blk = k >> 2, g = k & 3;
; #pragma unroll
;                         for (int jj = 0; jj < 4; ++jj) { const int r = 4 * g + jj; if (blk) p1[r] *= mul; else p0[r] *= mul; }
;                         pt *= lo * up;
;                     }
;                     P_run = pt;
;                     pv(o, p0, p1, lds + L_V + buf * 8192, lane);
;                     wdone = __all(P_run < 1.1754944e-38f);
;                 }
;                 if (lane == 0) flags[(i & 1) * 8 + wid] = wdone ? 1 : 0;
.LBB0_430:
	v_mov_b32_e32 v62, v56
	v_mov_b32_e32 v63, v57
	s_nop 0
	v_permlane32_swap_b32_e32 v56, v62
	v_permlane32_swap_b32_e32 v57, v63
	v_mul_f32_e32 v56, v56, v62
	v_mul_f32_e32 v57, v57, v63
	v_cndmask_b32_e64 v34, 1.0, v62, s[18:19]
	v_mul_f32_e32 v1, v56, v63
	v_mul_f32_e32 v82, v58, v34
	v_mul_f32_e32 v83, v59, v34
	v_mul_f32_e32 v92, v60, v34
	v_mul_f32_e32 v93, v61, v34
	v_cndmask_b32_e64 v34, v56, v1, s[18:19]
	v_mov_b32_e32 v1, v50
	v_mov_b32_e32 v51, v44
	v_mul_f32_e32 v94, v52, v34
	v_mul_f32_e32 v95, v53, v34
	v_mul_f32_e32 v52, v56, v57
	v_mul_f32_e32 v53, v57, v56
	v_permlane32_swap_b32_e32 v50, v1
	v_permlane32_swap_b32_e32 v44, v51
	v_mul_f32_e32 v50, v50, v1
	v_mov_b32_e32 v53, v44
	v_mul_f32_e32 v80, v54, v34
	v_mul_f32_e32 v81, v55, v34
	v_mul_f32_e32 v34, v52, v1
	v_mul_f32_e32 v44, v52, v50
	v_mul_f32_e32 v45, v53, v51
	v_cndmask_b32_e64 v34, v52, v34, s[18:19]
	v_mul_f32_e32 v1, v44, v51
	v_mul_f32_e32 v48, v48, v34
	v_mul_f32_e32 v49, v49, v34
	v_mul_f32_e32 v46, v46, v34
	v_mul_f32_e32 v47, v47, v34
	v_cndmask_b32_e64 v34, v44, v1, s[18:19]
	v_mov_b32_e32 v1, v32
	v_mov_b32_e32 v51, v33
	v_pk_mul_f32 v[44:45], v[44:45], v[44:45] op_sel:[0,1] op_sel_hi:[1,0]
	v_permlane32_swap_b32_e32 v32, v1
	v_permlane32_swap_b32_e32 v33, v51
	v_mul_f32_e32 v50, v32, v1
	v_mov_b32_e32 v45, v33
	v_mul_f32_e32 v42, v42, v34
	v_mul_f32_e32 v43, v43, v34
	v_mul_f32_e32 v40, v40, v34
	v_mul_f32_e32 v41, v41, v34
	v_mul_f32_e32 v34, v44, v1
	v_mul_f32_e32 v32, v44, v50
	v_mul_f32_e32 v33, v45, v51
	v_cndmask_b32_e64 v34, v44, v34, s[18:19]
	v_mul_f32_e32 v1, v32, v51
	v_mul_f32_e32 v36, v36, v34
	v_mul_f32_e32 v37, v37, v34
	v_mul_f32_e32 v38, v38, v34
	v_mul_f32_e32 v39, v39, v34
	v_cndmask_b32_e64 v34, v32, v1, s[18:19]
	v_mov_b32_e32 v1, v20
	v_mul_f32_e32 v50, v28, v34
	v_mul_f32_e32 v51, v29, v34
	v_mul_f32_e32 v28, v32, v33
	v_mul_f32_e32 v29, v33, v32
	v_permlane32_swap_b32_e32 v20, v1
	v_mul_f32_e32 v29, v28, v1
	v_mul_f32_e32 v44, v30, v34
	v_mul_f32_e32 v45, v31, v34
	v_cndmask_b32_e64 v30, v28, v29, s[18:19]
	v_mul_f32_e32 v72, v24, v30
	v_mul_f32_e32 v73, v25, v30
	v_mov_b32_e32 v25, v21
	s_nop 1
	v_permlane32_swap_b32_e32 v21, v25
	v_mul_f32_e32 v24, v20, v1
	v_mov_b32_e32 v29, v21
	v_mul_f32_e32 v20, v28, v24
	v_mul_f32_e32 v21, v29, v25
	s_add_i32 s4, 0, 0xc000
	v_mul_f32_e32 v1, v20, v25
	v_cndmask_b32_e64 v24, v20, v1, s[18:19]
	v_add_u32_e32 v1, s4, v107
	v_mul_f32_e32 v70, v26, v30
	v_mul_f32_e32 v71, v27, v30
	v_mul_f32_e32 v68, v22, v24
	v_mul_f32_e32 v69, v23, v24
	v_mul_f32_e32 v74, v18, v24
	v_mul_f32_e32 v75, v19, v24
	v_mul_f32_e32 v90, v20, v21
	ds_read_b64_tr_b16 v[18:19], v1
	ds_read_b64_tr_b16 v[20:21], v1 offset:512
	ds_read_b64_tr_b16 v[22:23], v1 offset:1024
	ds_read_b64_tr_b16 v[24:25], v1 offset:1536
	ds_read_b64_tr_b16 v[26:27], v1 offset:2048
	ds_read_b64_tr_b16 v[28:29], v1 offset:2560
	ds_read_b64_tr_b16 v[30:31], v1 offset:3072
	ds_read_b64_tr_b16 v[32:33], v1 offset:3584
	ds_read_b64_tr_b16 v[52:53], v1 offset:4096
	ds_read_b64_tr_b16 v[54:55], v1 offset:4608
	ds_read_b64_tr_b16 v[56:57], v1 offset:5120
	ds_read_b64_tr_b16 v[58:59], v1 offset:5632
	ds_read_b64_tr_b16 v[60:61], v1 offset:6144
	ds_read_b64_tr_b16 v[62:63], v1 offset:6656
	ds_read_b64_tr_b16 v[64:65], v1 offset:7168
	ds_read_b64_tr_b16 v[66:67], v1 offset:7680
	v_cvt_pk_bf16_f32 v68, v68, v69
	v_cvt_pk_bf16_f32 v69, v74, v75
	v_cvt_pk_bf16_f32 v70, v70, v71
	v_cvt_pk_bf16_f32 v71, v72, v73
	v_cvt_pk_bf16_f32 v72, v44, v45
	v_cvt_pk_bf16_f32 v73, v50, v51
	v_cvt_pk_bf16_f32 v74, v36, v37
	v_cvt_pk_bf16_f32 v75, v38, v39
	v_cvt_pk_bf16_f32 v76, v42, v43
	v_cvt_pk_bf16_f32 v77, v40, v41
	v_cvt_pk_bf16_f32 v78, v48, v49
	v_cvt_pk_bf16_f32 v79, v46, v47
	v_cvt_pk_bf16_f32 v80, v80, v81
	v_cvt_pk_bf16_f32 v81, v94, v95
	v_cvt_pk_bf16_f32 v82, v82, v83
	v_cvt_pk_bf16_f32 v83, v92, v93
	s_waitcnt lgkmcnt(14)
	v_mfma_f32_32x32x16_bf16 v[36:51], v[18:21], v[68:71], 0
	v_cmp_gt_f32_e32 vcc, s76, v90
	s_cmp_eq_u64 vcc, exec
	s_cselect_b64 s[30:31], -1, 0
	s_waitcnt lgkmcnt(12)
	v_mfma_f32_32x32x16_bf16 v[36:51], v[22:25], v[72:75], v[36:51]
	s_waitcnt lgkmcnt(10)
	v_mfma_f32_32x32x16_bf16 v[36:51], v[26:29], v[76:79], v[36:51]
	s_waitcnt lgkmcnt(8)
	v_mfma_f32_32x32x16_bf16 v[36:51], v[30:33], v[80:83], v[36:51]
	s_waitcnt lgkmcnt(6)
	v_mfma_f32_32x32x16_bf16 v[18:33], v[52:55], v[68:71], 0
	s_waitcnt lgkmcnt(4)
	v_mfma_f32_32x32x16_bf16 v[18:33], v[56:59], v[72:75], v[18:33]
	s_waitcnt lgkmcnt(2)
	v_mfma_f32_32x32x16_bf16 v[18:33], v[60:63], v[76:79], v[18:33]
	s_waitcnt lgkmcnt(0)
	v_mfma_f32_32x32x16_bf16 v[18:33], v[64:67], v[80:83], v[18:33]
	v_cmp_eq_u32_e64 s[20:21], 0, v148
	s_and_saveexec_b64 s[34:35], s[20:21]
	s_cbranch_execnz .LBB0_459
	s_branch .LBB0_460

; #define LAS __attribute__((address_space(3)))
; __device__ __forceinline__ void qkt(f32x16& p0, f32x16& p1, const LAS unsigned char* Kb, const bf16x8 (&qr)[4], float cinit, int r32, int hi) {
;     const int sw = (r32 >> 1) & 7;
;     bf16x8 kf[8];
; #pragma unroll
;     for (int d0 = 0; d0 < 4; ++d0) {
;         unsigned ka = (unsigned)(uintptr_t)Kb + r32 * 128 + (((2 * d0 + hi) ^ sw) << 4); asm volatile("" : "+v"(ka));
;         kf[2 * d0] = *(const LAS bf16x8*)(uintptr_t)ka;
;         kf[2 * d0 + 1] = *(const LAS bf16x8*)(uintptr_t)(ka + 4096);
;     }
; #pragma unroll
;     for (int r = 0; r < 16; ++r) { p0[r] = cinit; p1[r] = cinit; }
;     __builtin_amdgcn_sched_barrier(0);
; #pragma unroll
;     for (int d0 = 0; d0 < 4; ++d0) {
;         p0 = __builtin_amdgcn_mfma_f32_32x32x16_bf16(kf[2 * d0], qr[d0], p0, 0, 0, 0);
;         p1 = __builtin_amdgcn_mfma_f32_32x32x16_bf16(kf[2 * d0 + 1], qr[d0], p1, 0, 0, 0);
;     }
;     ...
;                 const int j = jhi - i, buf = i & 3;
;                 if (j <= jhi_w) {
;                     f32x16 p0, p1;
;                     qkt(p0, p1, lds + L_K + buf * 8192, qr, cinit, r32, hi);
;                     const LAS float* ck = (const LAS float*)(lds + L_CK + buf * 256);
;                     const bool diag = (64 * j + 63 > tw);
;     ...
;                     if (diag) { asm volatile("; forgetting attention: diagonal tile (masked)" ::: "memory"); FOX_BIAS(true) } else { FOX_BIAS(false) }
.LBB0_447:
	s_add_i32 s4, s38, s34
	s_add_i32 s4, s4, 63
	s_cmp_gt_i32 s4, s31
	s_cbranch_scc1 .LBB0_435
	s_and_b32 s4, s39, 3
	s_lshl_b32 s5, s4, 13
	s_add_i32 s54, s5, 0
	v_add_u32_e32 v34, s54, v149
	v_add_u32_e32 v72, v34, v171
	v_add_u32_e32 v80, v34, v172
	ds_read_b128 v[68:71], v72
	ds_read_b128 v[72:75], v72 offset:4096
	v_add_u32_e32 v88, v34, v173
	ds_read_b128 v[76:79], v80
	ds_read_b128 v[80:83], v80 offset:4096
	v_add_u32_e32 v34, v34, v174
	ds_read_b128 v[84:87], v88
	ds_read_b128 v[88:91], v88 offset:4096
	ds_read_b128 v[92:95], v34
	ds_read_b128 v[96:99], v34 offset:4096
	s_waitcnt lgkmcnt(7)
	v_mfma_f32_32x32x16_bf16 v[116:131], v[68:71], v[132:135], v[52:67]
	s_lshl_b32 s4, s4, 8
	s_add_i32 s4, s4, 0
	s_add_i32 s4, s4, 0x21000
	s_mov_b64 s[18:19], -1
	s_cmp_gt_i32 s37, s30
	v_lshl_add_u32 v179, v175, 2, s4
	s_waitcnt lgkmcnt(6)
	v_mfma_f32_32x32x16_bf16 v[100:115], v[72:75], v[132:135], v[52:67]
	s_waitcnt lgkmcnt(5)
	v_mfma_f32_32x32x16_bf16 v[116:131], v[76:79], v[136:139], v[116:131]
	s_waitcnt lgkmcnt(4)
	v_mfma_f32_32x32x16_bf16 v[100:115], v[80:83], v[136:139], v[100:115]
	s_waitcnt lgkmcnt(3)
	v_mfma_f32_32x32x16_bf16 v[116:131], v[84:87], v[140:143], v[116:131]
	s_waitcnt lgkmcnt(2)
	v_mfma_f32_32x32x16_bf16 v[100:115], v[88:91], v[140:143], v[100:115]
	s_waitcnt lgkmcnt(1)
	v_mfma_f32_32x32x16_bf16 v[116:131], v[92:95], v[144:147], v[116:131]
	s_waitcnt lgkmcnt(0)
	v_mfma_f32_32x32x16_bf16 v[100:115], v[96:99], v[144:147], v[100:115]
	s_cbranch_scc1 .LBB0_450
	ds_read_b128 v[68:71], v179
	ds_read_b128 v[72:75], v179 offset:32
	ds_read_b128 v[76:79], v179 offset:64
	ds_read_b128 v[80:83], v179 offset:96
	ds_read_b128 v[84:87], v179 offset:128
	ds_read_b128 v[88:91], v179 offset:160
	ds_read_b128 v[92:95], v179 offset:192
	ds_read_b128 v[96:99], v179 offset:224
	s_waitcnt lgkmcnt(4)
	v_fma_f32 v82, v82, s60, v130
	v_fma_f32 v83, v83, s60, v131
	v_fma_f32 v78, v78, s60, v126
	v_fma_f32 v79, v79, s60, v127
	v_fma_f32 v74, v74, s60, v122
	v_fma_f32 v75, v75, s60, v123
	v_fma_f32 v70, v70, s60, v118
	v_fma_f32 v71, v71, s60, v119
	v_fma_f32 v80, v80, s60, v128
	v_fma_f32 v81, v81, s60, v129
	v_fma_f32 v76, v76, s60, v124
	v_fma_f32 v77, v77, s60, v125
	v_fma_f32 v72, v72, s60, v120
	v_fma_f32 v73, v73, s60, v121
	v_fma_f32 v68, v68, s60, v116
	v_fma_f32 v69, v69, s60, v117
	s_waitcnt lgkmcnt(0)
	v_fma_f32 v98, v98, s60, v114
	v_fma_f32 v99, v99, s60, v115
	v_fma_f32 v94, v94, s60, v110
	v_fma_f32 v95, v95, s60, v111
	v_fma_f32 v90, v90, s60, v106
	v_fma_f32 v91, v91, s60, v107
	v_fma_f32 v86, v86, s60, v102
	v_fma_f32 v87, v87, s60, v103
	v_fma_f32 v96, v96, s60, v112
	v_fma_f32 v97, v97, s60, v113
	v_fma_f32 v92, v92, s60, v108
	v_fma_f32 v93, v93, s60, v109
	v_fma_f32 v88, v88, s60, v104
	v_fma_f32 v89, v89, s60, v105
	v_fma_f32 v84, v84, s60, v100
	v_fma_f32 v85, v85, s60, v101
	s_cbranch_execnz .LBB0_452
	s_branch .LBB0_451

; __device__ __forceinline__ void online_step(f32x16& p0, f32x16& p1, float& m_run, float& l_part, f32x16 (&o)[2]) {
;     float mt = fmaxf(p0[0], p1[0]);
; #pragma unroll
;     for (int r = 1; r < 16; ++r) mt = fmaxf(mt, fmaxf(p0[r], p1[r]));
;     mt = other_half_max(mt);
;     const float mn = fmaxf(m_run, mt);
;     const float msafe = mn == -INFINITY ? 0.f : mn;
;     const float f = __builtin_amdgcn_exp2f(m_run - msafe);
;     float rs = 0.f;
; #pragma unroll
;     for (int r = 0; r < 16; ++r) { p0[r] = __builtin_amdgcn_exp2f(p0[r] - msafe); p1[r] = __builtin_amdgcn_exp2f(p1[r] - msafe); rs += p0[r] + p1[r]; }
;     l_part = l_part * f + rs; m_run = mn;
; #pragma unroll
;     for (int r = 0; r < 16; ++r) { o[0][r] *= f; o[1][r] *= f; }
; }
.LBB0_452:
	s_and_saveexec_b64 s[18:19], s[6:7]
	s_xor_b64 s[18:19], exec, s[18:19]
	s_cbranch_execz .LBB0_454
	v_max_f32_e32 v34, v85, v85
	s_nop 4
	v_max_f32_e32 v100, v69, v69
	v_max_f32_e32 v34, v100, v34
	v_max_f32_e32 v100, v86, v86
	v_max_f32_e32 v101, v70, v70
	v_max_f32_e32 v100, v101, v100
	v_max_f32_e32 v101, v87, v87
	v_max_f32_e32 v102, v71, v71
	v_max3_f32 v34, v68, v84, v34
	v_max_f32_e32 v101, v102, v101
	v_max3_f32 v34, v34, v100, v101
	v_max_f32_e32 v100, v88, v88
	v_max_f32_e32 v101, v72, v72
	v_max_f32_e32 v100, v101, v100
	v_max_f32_e32 v101, v89, v89
	v_max_f32_e32 v102, v73, v73
	v_max_f32_e32 v101, v102, v101
	v_max3_f32 v34, v34, v100, v101
	v_max_f32_e32 v100, v90, v90
	v_max_f32_e32 v101, v74, v74
	v_max_f32_e32 v100, v101, v100
	v_max_f32_e32 v101, v91, v91
	v_max_f32_e32 v102, v75, v75
	v_max_f32_e32 v101, v102, v101
	v_max3_f32 v34, v34, v100, v101
	v_max_f32_e32 v100, v92, v92
	v_max_f32_e32 v101, v76, v76
	v_max_f32_e32 v100, v101, v100
	v_max_f32_e32 v101, v93, v93
	v_max_f32_e32 v102, v77, v77
	v_max_f32_e32 v101, v102, v101
	v_max3_f32 v34, v34, v100, v101
	v_max_f32_e32 v100, v94, v94
	v_max_f32_e32 v101, v78, v78
	v_max_f32_e32 v100, v101, v100
	v_max_f32_e32 v101, v95, v95
	v_max_f32_e32 v102, v79, v79
	v_max_f32_e32 v101, v102, v101
	v_max3_f32 v34, v34, v100, v101
	v_max_f32_e32 v100, v96, v96
	v_max_f32_e32 v101, v80, v80
	v_max_f32_e32 v100, v101, v100
	v_max_f32_e32 v101, v97, v97
	v_max_f32_e32 v102, v81, v81
	v_max_f32_e32 v101, v102, v101
	v_max3_f32 v34, v34, v100, v101
	v_max_f32_e32 v100, v98, v98
	v_max_f32_e32 v101, v82, v82
	v_max_f32_e32 v100, v101, v100
	v_max_f32_e32 v101, v99, v99
	v_max_f32_e32 v102, v83, v83
	v_max_f32_e32 v101, v102, v101
	v_max3_f32 v34, v34, v100, v101
	v_mov_b32_e32 v100, v34
	s_nop 1
	v_permlane32_swap_b32_e32 v34, v100
	v_max3_f32 v179, v178, v34, v100
	v_cmp_neq_f32_e32 vcc, s57, v179
	s_nop 1
	v_cndmask_b32_e32 v101, 0, v179, vcc
	v_sub_f32_e32 v34, v68, v101
	v_exp_f32_e32 v116, v34
	v_sub_f32_e32 v34, v84, v101
	v_exp_f32_e32 v100, v34
	v_sub_f32_e32 v34, v69, v101
	v_exp_f32_e32 v68, v34
	v_sub_f32_e32 v34, v85, v101
	v_exp_f32_e32 v34, v34
	v_add_f32_e32 v69, v116, v100
	v_mov_b32_e32 v117, v68
	v_add_f32_e32 v84, v68, v34
	v_add_f32_e32 v85, v69, v35
	v_sub_f32_e32 v69, v70, v101
	v_exp_f32_e32 v118, v69
	v_sub_f32_e32 v69, v86, v101
	v_exp_f32_e32 v102, v69
	v_sub_f32_e32 v69, v71, v101
	v_add_f32_e32 v85, v84, v85
	v_add_f32_e32 v84, v84, v84
	v_exp_f32_e32 v70, v69
	v_sub_f32_e32 v69, v87, v101
	v_exp_f32_e32 v84, v69
	v_sub_f32_e32 v69, v72, v101
	v_add_f32_e32 v71, v118, v102
	v_exp_f32_e32 v120, v69
	v_sub_f32_e32 v69, v88, v101
	v_add_f32_e32 v86, v70, v84
	v_add_f32_e32 v87, v71, v85
	v_exp_f32_e32 v104, v69
	v_sub_f32_e32 v69, v73, v101
	v_add_f32_e32 v87, v86, v87
	v_add_f32_e32 v86, v86, v86
	v_exp_f32_e32 v72, v69
	v_sub_f32_e32 v69, v89, v101
	v_exp_f32_e32 v86, v69
	v_sub_f32_e32 v69, v74, v101
	v_add_f32_e32 v73, v120, v104
	v_exp_f32_e32 v122, v69
	v_sub_f32_e32 v69, v90, v101
	v_add_f32_e32 v88, v72, v86
	v_add_f32_e32 v89, v73, v87
	v_exp_f32_e32 v106, v69
	v_sub_f32_e32 v69, v75, v101
	v_add_f32_e32 v89, v88, v89
	v_add_f32_e32 v88, v88, v88
	v_exp_f32_e32 v74, v69
	v_sub_f32_e32 v69, v91, v101
	v_exp_f32_e32 v88, v69
	v_sub_f32_e32 v69, v76, v101
	v_add_f32_e32 v75, v122, v106
	v_exp_f32_e32 v124, v69
	v_sub_f32_e32 v69, v92, v101
	v_add_f32_e32 v90, v74, v88
	v_add_f32_e32 v91, v75, v89
	v_exp_f32_e32 v108, v69
	v_sub_f32_e32 v69, v77, v101
	v_add_f32_e32 v91, v90, v91
	v_add_f32_e32 v90, v90, v90
	v_exp_f32_e32 v76, v69
	v_sub_f32_e32 v69, v93, v101
	v_exp_f32_e32 v90, v69
	v_sub_f32_e32 v69, v78, v101
	v_add_f32_e32 v77, v124, v108
	v_exp_f32_e32 v126, v69
	v_sub_f32_e32 v69, v94, v101
	v_add_f32_e32 v92, v76, v90
	v_add_f32_e32 v93, v77, v91
	v_exp_f32_e32 v110, v69
	v_sub_f32_e32 v69, v79, v101
	v_add_f32_e32 v93, v92, v93
	v_add_f32_e32 v92, v92, v92
	v_exp_f32_e32 v78, v69
	v_sub_f32_e32 v69, v95, v101
	v_exp_f32_e32 v92, v69
	v_sub_f32_e32 v69, v80, v101
	v_add_f32_e32 v79, v126, v110
	v_exp_f32_e32 v128, v69
	v_sub_f32_e32 v69, v96, v101
	v_add_f32_e32 v94, v78, v92
	v_add_f32_e32 v95, v79, v93
	v_exp_f32_e32 v112, v69
	v_sub_f32_e32 v69, v81, v101
	v_add_f32_e32 v95, v94, v95
	v_add_f32_e32 v94, v94, v94
	v_exp_f32_e32 v80, v69
	v_sub_f32_e32 v69, v97, v101
	v_exp_f32_e32 v94, v69
	v_sub_f32_e32 v69, v82, v101
	v_exp_f32_e32 v130, v69
	v_sub_f32_e32 v69, v98, v101
	v_sub_f32_e32 v73, v83, v101
	v_sub_f32_e32 v68, v99, v101
	v_exp_f32_e32 v114, v69
	v_exp_f32_e32 v131, v73
	v_exp_f32_e32 v115, v68
	v_add_f32_e32 v81, v128, v112
	v_sub_f32_e32 v71, v178, v101
	v_add_f32_e32 v96, v80, v94
	v_add_f32_e32 v97, v81, v95
	v_mov_b32_e32 v101, v34
	v_add_f32_e32 v97, v96, v97
	v_add_f32_e32 v96, v96, v96
	v_exp_f32_e32 v34, v71
	v_add_f32_e32 v69, v130, v114
	v_mov_b32_e32 v68, v131
	v_mov_b32_e32 v96, v115
	v_add_f32_e32 v68, v68, v96
	v_add_f32_e32 v69, v69, v97
	v_mov_b32_e32 v119, v70
	v_add_f32_e32 v68, v68, v69
	v_fmac_f32_e32 v68, v177, v34
	v_mov_b32_e32 v121, v72
	v_mov_b32_e32 v123, v74
	v_mov_b32_e32 v125, v76
	v_mov_b32_e32 v127, v78
	v_mov_b32_e32 v129, v80
	v_mov_b32_e32 v103, v84
	v_mov_b32_e32 v105, v86
	v_mov_b32_e32 v107, v88
	v_mov_b32_e32 v109, v90
	v_mov_b32_e32 v111, v92
	v_mov_b32_e32 v113, v94
	v_mul_f32_e32 v50, v50, v34
	v_mul_f32_e32 v51, v51, v34
	v_mul_f32_e32 v48, v48, v34
	v_mul_f32_e32 v49, v49, v34
	v_mul_f32_e32 v46, v46, v34
	v_mul_f32_e32 v47, v47, v34
	v_mul_f32_e32 v44, v44, v34
	v_mul_f32_e32 v45, v45, v34
	v_mul_f32_e32 v42, v42, v34
	v_mul_f32_e32 v43, v43, v34
	v_mul_f32_e32 v40, v40, v34
	v_mul_f32_e32 v41, v41, v34
	v_mul_f32_e32 v38, v38, v34
	v_mul_f32_e32 v39, v39, v34
	v_mul_f32_e32 v36, v36, v34
	v_mul_f32_e32 v37, v37, v34
	v_mul_f32_e32 v32, v32, v34
	v_mul_f32_e32 v33, v33, v34
	v_mul_f32_e32 v30, v30, v34
	v_mul_f32_e32 v31, v31, v34
	v_mul_f32_e32 v28, v28, v34
	v_mul_f32_e32 v29, v29, v34
	v_mul_f32_e32 v26, v26, v34
	v_mul_f32_e32 v27, v27, v34
	v_mul_f32_e32 v24, v24, v34
	v_mul_f32_e32 v25, v25, v34
	v_mul_f32_e32 v22, v22, v34
	v_mul_f32_e32 v23, v23, v34
	v_mul_f32_e32 v20, v20, v34
	v_mul_f32_e32 v21, v21, v34
	v_mul_f32_e32 v18, v18, v34
	v_mul_f32_e32 v19, v19, v34
	v_mov_b32_e32 v178, v179
	v_mov_b32_e32 v177, v68
	s_andn2_saveexec_b64 s[18:19], s[18:19]
	s_cbranch_execz .LBB0_434
	s_branch .LBB0_455

; __device__ __forceinline__ void exp_sum(f32x16& p0, f32x16& p1, float& l_part) {
;     float rs = 0.f;
; #pragma unroll
;     for (int r = 0; r < 16; ++r) { p0[r] = __builtin_amdgcn_exp2f(p0[r]); p1[r] = __builtin_amdgcn_exp2f(p1[r]); rs += p0[r] + p1[r]; }
;     l_part += rs;
; }
.LBB0_455:
	s_nop 1
	v_exp_f32_e32 v116, v68
	s_nop 0
	v_exp_f32_e32 v100, v84
	v_exp_f32_e32 v34, v69
	v_exp_f32_e32 v68, v85
	v_exp_f32_e32 v118, v70
	v_add_f32_e32 v69, v100, v116
	v_exp_f32_e32 v102, v86
	v_add_f32_e32 v84, v68, v34
	v_add_f32_e32 v85, v69, v35
	v_exp_f32_e32 v70, v87
	v_add_f32_e32 v85, v84, v85
	v_add_f32_e32 v84, v84, v84
	v_exp_f32_e32 v84, v71
	v_add_f32_e32 v71, v102, v118
	v_exp_f32_e32 v120, v72
	v_exp_f32_e32 v104, v88
	v_add_f32_e32 v86, v70, v84
	v_add_f32_e32 v87, v71, v85
	v_exp_f32_e32 v72, v89
	v_add_f32_e32 v87, v86, v87
	v_add_f32_e32 v86, v86, v86
	v_exp_f32_e32 v86, v73
	v_add_f32_e32 v73, v104, v120
	v_exp_f32_e32 v122, v74
	v_exp_f32_e32 v106, v90
	v_add_f32_e32 v88, v72, v86
	v_add_f32_e32 v89, v73, v87
	v_exp_f32_e32 v74, v91
	v_add_f32_e32 v89, v88, v89
	v_add_f32_e32 v88, v88, v88
	v_exp_f32_e32 v88, v75
	v_add_f32_e32 v75, v106, v122
	v_exp_f32_e32 v124, v76
	v_exp_f32_e32 v108, v92
	v_add_f32_e32 v90, v74, v88
	v_add_f32_e32 v91, v75, v89
	v_exp_f32_e32 v76, v93
	v_add_f32_e32 v91, v90, v91
	v_add_f32_e32 v90, v90, v90
	v_exp_f32_e32 v90, v77
	v_add_f32_e32 v77, v108, v124
	v_exp_f32_e32 v126, v78
	v_exp_f32_e32 v110, v94
	v_add_f32_e32 v92, v76, v90
	v_add_f32_e32 v93, v77, v91
	v_exp_f32_e32 v78, v95
	v_add_f32_e32 v93, v92, v93
	v_add_f32_e32 v92, v92, v92
	v_exp_f32_e32 v92, v79
	v_add_f32_e32 v79, v110, v126
	v_exp_f32_e32 v128, v80
	v_exp_f32_e32 v112, v96
	v_add_f32_e32 v94, v78, v92
	v_add_f32_e32 v95, v79, v93
	v_exp_f32_e32 v80, v97
	v_add_f32_e32 v95, v94, v95
	v_add_f32_e32 v94, v94, v94
	v_exp_f32_e32 v94, v81
	v_exp_f32_e32 v130, v82
	v_exp_f32_e32 v114, v98
	v_exp_f32_e32 v131, v83
	v_exp_f32_e32 v115, v99
	v_add_f32_e32 v81, v112, v128
	v_add_f32_e32 v96, v80, v94
	v_add_f32_e32 v97, v81, v95
	v_add_f32_e32 v69, v114, v130
	v_add_f32_e32 v97, v96, v97
	v_add_f32_e32 v96, v96, v96
	v_mov_b32_e32 v101, v68
	v_mov_b32_e32 v68, v115
	v_mov_b32_e32 v96, v131
	v_add_f32_e32 v68, v68, v96
	v_add_f32_e32 v69, v69, v97
	v_mov_b32_e32 v117, v34
	v_add_f32_e32 v34, v68, v69
	v_mov_b32_e32 v119, v84
	v_mov_b32_e32 v121, v86
	v_mov_b32_e32 v123, v88
	v_mov_b32_e32 v125, v90
	v_mov_b32_e32 v127, v92
	v_mov_b32_e32 v129, v94
	v_mov_b32_e32 v103, v70
	v_mov_b32_e32 v105, v72
	v_mov_b32_e32 v107, v74
	v_mov_b32_e32 v109, v76
	v_mov_b32_e32 v111, v78
	v_mov_b32_e32 v113, v80
	v_add_f32_e32 v177, v177, v34
	s_branch .LBB0_434

;     ...
;                 if (j <= jhi_w && !wdone) {
;                     f32x16 p0, p1;
;                     qkt(p0, p1, lds + L_K + buf * 8192, qr, 0.f, r32, hi);
;                     const bool diag = (64 * j + 63 >= tw);
;                     float gp[8];
.LBB0_473:
	s_add_i32 s4, s36, s75
	s_add_i32 s4, s4, 2
	s_cmp_gt_i32 s4, s37
	s_cselect_b64 s[34:35], -1, 0
	s_or_b64 s[34:35], s[34:35], s[30:31]
	s_and_b64 vcc, exec, s[34:35]
	s_cbranch_vccnz .LBB0_479
	s_and_b32 s4, s78, 0x6000
	s_add_i32 s34, s4, 0
	v_add_u32_e32 v34, s34, v85
	v_add_u32_e32 v56, v34, v102
	v_add_u32_e32 v60, v34, v103
	ds_read_b128 v[52:55], v56
	ds_read_b128 v[56:59], v56 offset:4096
	ds_read_b128 v[92:95], v60
	ds_read_b128 v[96:99], v60 offset:4096
	v_add_u32_e32 v60, v34, v104
	v_add_u32_e32 v34, v34, v105
	ds_read_b128 v[108:111], v60
	ds_read_b128 v[112:115], v60 offset:4096
	ds_read_b128 v[118:121], v34
	ds_read_b128 v[172:175], v34 offset:4096
	s_waitcnt lgkmcnt(7)
	v_mfma_f32_32x32x16_bf16 v[68:83], v[52:55], v[132:135], 0
	s_add_i32 s4, s55, 0xf80
	s_cmp_ge_i32 s4, s38
	s_mov_b64 s[30:31], -1
	s_waitcnt lgkmcnt(6)
	v_mfma_f32_32x32x16_bf16 v[52:67], v[56:59], v[132:135], 0
	s_waitcnt lgkmcnt(5)
	v_mfma_f32_32x32x16_bf16 v[68:83], v[92:95], v[136:139], v[68:83]
	s_waitcnt lgkmcnt(4)
	v_mfma_f32_32x32x16_bf16 v[52:67], v[96:99], v[136:139], v[52:67]
	s_waitcnt lgkmcnt(3)
	v_mfma_f32_32x32x16_bf16 v[68:83], v[108:111], v[140:143], v[68:83]
	s_waitcnt lgkmcnt(2)
	v_mfma_f32_32x32x16_bf16 v[52:67], v[112:115], v[140:143], v[52:67]
	s_waitcnt lgkmcnt(1)
	v_mfma_f32_32x32x16_bf16 v[68:83], v[118:121], v[144:147], v[68:83]
	s_waitcnt lgkmcnt(0)
	v_mfma_f32_32x32x16_bf16 v[52:67], v[172:175], v[144:147], v[52:67]
	s_nop 9
	v_exp_f32_e32 v155, v71
	v_exp_f32_e32 v153, v70
	v_exp_f32_e32 v154, v69
	v_exp_f32_e32 v152, v68
	v_exp_f32_e32 v151, v75
	v_exp_f32_e32 v150, v74
	v_exp_f32_e32 v149, v73
	v_exp_f32_e32 v131, v72
	v_exp_f32_e32 v129, v79
	v_exp_f32_e32 v130, v78
	v_exp_f32_e32 v128, v77
	v_exp_f32_e32 v127, v76
	v_exp_f32_e32 v126, v83
	v_exp_f32_e32 v125, v82
	v_exp_f32_e32 v124, v81
	v_exp_f32_e32 v123, v80
	v_exp_f32_e32 v122, v55
	v_exp_f32_e32 v121, v54
	v_exp_f32_e32 v120, v53
	v_exp_f32_e32 v119, v52
	v_exp_f32_e32 v118, v59
	v_exp_f32_e32 v117, v58
	v_exp_f32_e32 v115, v57
	v_exp_f32_e32 v114, v56
	v_exp_f32_e32 v113, v63
	v_exp_f32_e32 v112, v62
	v_exp_f32_e32 v111, v61
	v_exp_f32_e32 v110, v60
	v_exp_f32_e32 v109, v67
	v_exp_f32_e32 v108, v66
	v_exp_f32_e32 v91, v65
	v_exp_f32_e32 v34, v64
	s_cbranch_scc0 .LBB0_476
	v_add_f32_e32 v53, 1.0, v153
	v_rcp_f32_e32 v54, v53
	v_add_f32_e32 v53, 1.0, v154
	v_rcp_f32_e32 v55, v53
	v_add_f32_e32 v53, 1.0, v152
	v_rcp_f32_e32 v56, v53
	v_add_f32_e32 v53, 1.0, v151
	v_add_f32_e32 v52, 1.0, v155
	v_rcp_f32_e32 v57, v53
	v_add_f32_e32 v53, 1.0, v150
	v_rcp_f32_e32 v52, v52
	v_rcp_f32_e32 v58, v53
	v_add_f32_e32 v53, 1.0, v149
	v_rcp_f32_e32 v62, v53
	v_add_f32_e32 v53, 1.0, v131
	v_add_u32_e32 v96, s55, v106
	v_rcp_f32_e32 v64, v53
	v_add_u32_e32 v53, 0xf83, v96
	v_add_u32_e32 v59, 0xf8a, v96
	v_cmp_lt_i32_e32 vcc, v53, v1
	v_add_u32_e32 v60, 0xf8b, v96
	v_add_u32_e32 v65, 0xf80, v96
	v_cndmask_b32_e32 v53, 1.0, v52, vcc
	v_cmp_lt_i32_e32 vcc, v59, v84
	v_add_u32_e32 v69, 0xf9a, v96
	v_add_u32_e32 v72, 0xf9b, v96
	v_cndmask_b32_e32 v52, 1.0, v58, vcc
	v_add_u32_e32 v58, 0xf82, v96
	v_cmp_lt_i32_e32 vcc, v58, v1
	v_mov_b32_e32 v200, v53
	v_add_f32_e32 v76, 1.0, v119
	v_cndmask_b32_e32 v59, 1.0, v54, vcc
	v_cmp_lt_i32_e32 vcc, v60, v84
	v_add_u32_e32 v54, 0xf81, v96
	v_rcp_f32_e32 v76, v76
	v_cndmask_b32_e32 v58, 1.0, v57, vcc
	v_add_u32_e32 v57, 0xf89, v96
	v_cmp_lt_i32_e32 vcc, v54, v1
	v_mul_f32_e32 v60, v52, v58
	v_mul_f32_e32 v61, v53, v59
	v_mov_b32_e32 v59, v201
	v_cndmask_b32_e32 v55, 1.0, v55, vcc
	v_cmp_lt_i32_e32 vcc, v57, v84
	v_mov_b32_e32 v52, v61
	v_mov_b32_e32 v57, v61
	v_cndmask_b32_e32 v54, 1.0, v62, vcc
	v_mul_f32_e32 v62, v54, v60
	v_mul_f32_e32 v63, v55, v61
	v_add_u32_e32 v54, 0xf88, v96
	v_cmp_lt_i32_e32 vcc, v65, v1
	v_mov_b32_e32 v61, v58
	v_mov_b32_e32 v65, v63
	v_cndmask_b32_e32 v55, 1.0, v56, vcc
	v_cmp_lt_i32_e32 vcc, v54, v84
	v_mov_b32_e32 v56, v63
	v_sub_f32_e32 v58, v58, v60
	v_sub_f32_e32 v59, v59, v61
	v_cndmask_b32_e32 v54, 1.0, v64, vcc
	v_mul_f32_e32 v54, v54, v62
	v_mul_f32_e32 v55, v55, v63
	v_mov_b32_e32 v63, v60
	v_mov_b32_e32 v60, v54
	v_mov_b32_e32 v61, v62
	v_mov_b32_e32 v64, v55
	v_sub_f32_e32 v60, v62, v60
	v_sub_f32_e32 v61, v63, v61
	v_add_f32_e32 v63, 1.0, v130
	v_sub_f32_e32 v56, v56, v64
	v_sub_f32_e32 v57, v57, v65
	v_rcp_f32_e32 v64, v63
	v_add_f32_e32 v63, 1.0, v128
	v_rcp_f32_e32 v65, v63
	v_add_f32_e32 v63, 1.0, v127
	v_rcp_f32_e32 v66, v63
	v_add_f32_e32 v63, 1.0, v126
	v_add_f32_e32 v62, 1.0, v129
	v_rcp_f32_e32 v67, v63
	v_add_f32_e32 v63, 1.0, v125
	v_rcp_f32_e32 v62, v62
	v_rcp_f32_e32 v68, v63
	v_add_f32_e32 v63, 1.0, v124
	v_rcp_f32_e32 v70, v63
	v_add_f32_e32 v63, 1.0, v123
	v_rcp_f32_e32 v71, v63
	v_add_u32_e32 v63, 0xf93, v96
	v_cmp_lt_i32_e32 vcc, v63, v1
	v_sub_f32_e32 v52, v200, v52
	v_sub_f32_e32 v53, v201, v53
	v_add_f32_e32 v80, 1.0, v114
	v_cndmask_b32_e32 v63, 1.0, v62, vcc
	v_cmp_lt_i32_e32 vcc, v69, v84
	v_mov_b32_e32 v200, v63
	v_rcp_f32_e32 v80, v80
	v_cndmask_b32_e32 v62, 1.0, v68, vcc
	v_add_u32_e32 v68, 0xf92, v96
	v_cmp_lt_i32_e32 vcc, v68, v1
	v_add_u32_e32 v98, 0xfba, v96
	s_mov_b64 s[30:31], 0
	v_cndmask_b32_e32 v69, 1.0, v64, vcc
	v_cmp_lt_i32_e32 vcc, v72, v84
	v_add_u32_e32 v64, 0xf91, v96
	s_nop 0
	v_cndmask_b32_e32 v68, 1.0, v67, vcc
	v_add_u32_e32 v67, 0xf99, v96
	v_cmp_lt_i32_e32 vcc, v64, v1
	v_mul_f32_e32 v72, v62, v68
	v_mul_f32_e32 v73, v63, v69
	v_mov_b32_e32 v69, v201
	v_cndmask_b32_e32 v65, 1.0, v65, vcc
	v_cmp_lt_i32_e32 vcc, v67, v84
	v_add_u32_e32 v67, 0xf98, v96
	v_mov_b32_e32 v62, v73
	v_cndmask_b32_e32 v64, 1.0, v70, vcc
	v_mul_f32_e32 v74, v64, v72
	v_mul_f32_e32 v75, v65, v73
	v_add_u32_e32 v64, 0xf90, v96
	v_cmp_lt_i32_e32 vcc, v64, v1
	v_sub_f32_e32 v62, v200, v62
	v_sub_f32_e32 v63, v201, v63
	s_nop 0
	v_cndmask_b32_e32 v65, 1.0, v66, vcc
	v_cmp_lt_i32_e32 vcc, v67, v84
	s_nop 1
	v_cndmask_b32_e32 v64, 1.0, v71, vcc
	v_mul_f32_e32 v66, v64, v74
	v_mul_f32_e32 v67, v65, v75
	v_mov_b32_e32 v64, v75
	v_mov_b32_e32 v65, v73
	v_mov_b32_e32 v70, v67
	v_mov_b32_e32 v71, v75
	v_mov_b32_e32 v73, v68
	v_sub_f32_e32 v64, v64, v70
	v_sub_f32_e32 v65, v65, v71
	v_sub_f32_e32 v70, v68, v72
	v_sub_f32_e32 v71, v69, v73
	v_mov_b32_e32 v75, v72
	v_mov_b32_e32 v68, v66
	v_mov_b32_e32 v69, v74
	v_sub_f32_e32 v68, v74, v68
	v_sub_f32_e32 v69, v75, v69
	v_add_f32_e32 v74, 1.0, v122
	v_rcp_f32_e32 v74, v74
	v_add_f32_e32 v75, 1.0, v121
	v_rcp_f32_e32 v75, v75
	v_add_u32_e32 v73, 0xfa3, v96
	v_cmp_lt_i32_e32 vcc, v73, v84
	v_add_u32_e32 v73, 0xfa2, v96
	v_add_u32_e32 v72, 0xfa0, v96
	v_cndmask_b32_e32 v200, 1.0, v74, vcc
	v_cmp_lt_i32_e32 vcc, v73, v84
	v_add_u32_e32 v74, 0xfa1, v96
	s_nop 0
	v_cndmask_b32_e32 v73, 1.0, v75, vcc
	v_add_f32_e32 v75, 1.0, v120
	v_rcp_f32_e32 v75, v75
	v_cmp_lt_i32_e32 vcc, v74, v84
	v_mul_f32_e32 v74, v200, v73
	v_mov_b32_e32 v79, v74
	v_cndmask_b32_e32 v77, 1.0, v75, vcc
	v_cmp_lt_i32_e32 vcc, v72, v84
	v_mul_f32_e32 v78, v77, v74
	v_mov_b32_e32 v75, v200
	v_cndmask_b32_e32 v76, 1.0, v76, vcc
	v_mul_f32_e32 v76, v76, v78
	v_mov_b32_e32 v77, v78
	v_sub_f32_e32 v72, v200, v74
	v_sub_f32_e32 v73, v201, v75
	v_sub_f32_e32 v74, v78, v76
	v_sub_f32_e32 v75, v79, v77
	v_add_f32_e32 v78, 1.0, v118
	v_rcp_f32_e32 v78, v78
	v_add_f32_e32 v79, 1.0, v117
	v_rcp_f32_e32 v79, v79
	v_add_u32_e32 v77, 0xfab, v96
	v_cmp_lt_i32_e32 vcc, v77, v84
	v_add_u32_e32 v77, 0xfaa, v96
	s_nop 0
	v_cndmask_b32_e32 v200, 1.0, v78, vcc
	v_cmp_lt_i32_e32 vcc, v77, v84
	v_add_u32_e32 v78, 0xfa9, v96
	v_mov_b32_e32 v81, v200
	v_cndmask_b32_e32 v77, 1.0, v79, vcc
	v_add_f32_e32 v79, 1.0, v115
	v_rcp_f32_e32 v79, v79
	v_cmp_lt_i32_e32 vcc, v78, v84
	v_add_u32_e32 v78, 0xfa8, v96
	s_nop 0
	v_cndmask_b32_e32 v82, 1.0, v79, vcc
	v_cmp_lt_i32_e32 vcc, v78, v84
	s_nop 1
	v_cndmask_b32_e32 v83, 1.0, v80, vcc
	v_mul_f32_e32 v80, v200, v77
	v_mul_f32_e32 v92, v82, v80
	v_mul_f32_e32 v82, v83, v92
	v_mov_b32_e32 v93, v80
	v_mov_b32_e32 v83, v92
	v_sub_f32_e32 v78, v200, v80
	v_sub_f32_e32 v79, v201, v81
	v_sub_f32_e32 v80, v92, v82
	v_sub_f32_e32 v81, v93, v83
	v_add_f32_e32 v92, 1.0, v111
	v_rcp_f32_e32 v94, v92
	v_add_f32_e32 v92, 1.0, v110
	v_add_f32_e32 v77, 1.0, v113
	v_rcp_f32_e32 v97, v92
	v_add_f32_e32 v92, 1.0, v109
	v_rcp_f32_e32 v77, v77
	v_rcp_f32_e32 v95, v92
	v_add_f32_e32 v92, 1.0, v108
	v_add_f32_e32 v93, 1.0, v91
	v_add_f32_e32 v83, 1.0, v112
	v_rcp_f32_e32 v92, v92
	v_rcp_f32_e32 v100, v93
	v_add_f32_e32 v93, 1.0, v34
	v_rcp_f32_e32 v83, v83
	v_rcp_f32_e32 v101, v93
	v_add_u32_e32 v93, 0xfb3, v96
	v_cmp_lt_i32_e32 vcc, v93, v1
	s_nop 1
	v_cndmask_b32_e32 v93, 1.0, v77, vcc
	v_cmp_lt_i32_e32 vcc, v98, v84
	v_add_u32_e32 v77, 0xfb2, v96
	v_add_u32_e32 v98, 0xfbb, v96
	v_cndmask_b32_e32 v92, 1.0, v92, vcc
	v_cmp_lt_i32_e32 vcc, v77, v1
	v_add_u32_e32 v77, 0xfb1, v96
	v_mov_b32_e32 v200, v93
	v_cndmask_b32_e32 v99, 1.0, v83, vcc
	v_cmp_lt_i32_e32 vcc, v98, v84
	v_add_u32_e32 v83, 0xfb9, v96
	s_nop 0
	v_cndmask_b32_e32 v98, 1.0, v95, vcc
	v_cmp_lt_i32_e32 vcc, v77, v1
	v_add_u32_e32 v77, 0xfb0, v96
	v_mul_f32_e32 v172, v92, v98
	v_mul_f32_e32 v173, v93, v99
	v_cndmask_b32_e32 v95, 1.0, v94, vcc
	v_cmp_lt_i32_e32 vcc, v83, v84
	v_add_u32_e32 v83, 0xfb8, v96
	v_mov_b32_e32 v92, v173
	v_cndmask_b32_e32 v94, 1.0, v100, vcc
	v_cmp_lt_i32_e32 vcc, v77, v1
	v_mul_f32_e32 v174, v94, v172
	v_mul_f32_e32 v175, v95, v173
	v_mov_b32_e32 v99, v201
	v_cndmask_b32_e32 v95, 1.0, v97, vcc
	v_cmp_lt_i32_e32 vcc, v83, v84
	v_sub_f32_e32 v92, v200, v92
	v_sub_f32_e32 v93, v201, v93
	s_nop 0
	v_cndmask_b32_e32 v94, 1.0, v101, vcc
	v_mul_f32_e32 v96, v94, v174
	v_mul_f32_e32 v97, v95, v175
	v_mov_b32_e32 v94, v175
	v_mov_b32_e32 v95, v173
	v_mov_b32_e32 v100, v97
	v_mov_b32_e32 v101, v175
	v_mov_b32_e32 v173, v98
	v_sub_f32_e32 v94, v94, v100
	v_sub_f32_e32 v95, v95, v101
	v_sub_f32_e32 v100, v98, v172
	v_sub_f32_e32 v101, v99, v173
	v_mov_b32_e32 v175, v172
	v_mov_b32_e32 v98, v96
	v_mov_b32_e32 v99, v174
	v_sub_f32_e32 v98, v174, v98
	v_sub_f32_e32 v99, v175, v99
.LBB0_476:
	s_andn2_b64 vcc, exec, s[30:31]
	s_cbranch_vccnz .LBB0_478
	v_add_f32_e32 v52, 1.0, v155
	v_rcp_f32_e32 v59, v52
	v_add_f32_e32 v52, 1.0, v153
	v_rcp_f32_e32 v53, v52
	v_add_f32_e32 v52, 1.0, v154
	v_rcp_f32_e32 v55, v52
	v_add_f32_e32 v52, 1.0, v152
	v_rcp_f32_e32 v57, v52
	v_add_f32_e32 v52, 1.0, v151
	v_rcp_f32_e32 v58, v52
	v_add_f32_e32 v52, 1.0, v150
	v_rcp_f32_e32 v52, v52
	v_add_f32_e32 v54, 1.0, v149
	v_rcp_f32_e32 v54, v54
	v_add_f32_e32 v56, 1.0, v131
	v_rcp_f32_e32 v56, v56
	v_mul_f32_e32 v60, v58, v52
	v_mul_f32_e32 v61, v59, v53
	v_mov_b32_e32 v200, v59
	v_mul_f32_e32 v62, v54, v60
	v_mul_f32_e32 v63, v55, v61
	v_mov_b32_e32 v52, v61
	v_mov_b32_e32 v53, v59
	v_mul_f32_e32 v54, v56, v62
	v_mul_f32_e32 v55, v57, v63
	v_mov_b32_e32 v57, v61
	v_mov_b32_e32 v59, v201
	v_mov_b32_e32 v61, v58
	v_mov_b32_e32 v56, v63
	v_mov_b32_e32 v65, v63
	v_sub_f32_e32 v58, v58, v60
	v_sub_f32_e32 v59, v59, v61
	v_mov_b32_e32 v63, v60
	v_mov_b32_e32 v60, v54
	v_mov_b32_e32 v61, v62
	v_sub_f32_e32 v60, v62, v60
	v_sub_f32_e32 v61, v63, v61
	v_add_f32_e32 v62, 1.0, v129
	v_rcp_f32_e32 v69, v62
	v_add_f32_e32 v62, 1.0, v130
	v_mov_b32_e32 v64, v55
	v_rcp_f32_e32 v63, v62
	v_add_f32_e32 v62, 1.0, v128
	v_sub_f32_e32 v56, v56, v64
	v_sub_f32_e32 v57, v57, v65
	v_rcp_f32_e32 v65, v62
	v_add_f32_e32 v62, 1.0, v127
	v_rcp_f32_e32 v67, v62
	v_add_f32_e32 v62, 1.0, v126
	v_rcp_f32_e32 v68, v62
	v_add_f32_e32 v62, 1.0, v125
	v_rcp_f32_e32 v62, v62
	v_add_f32_e32 v64, 1.0, v124
	v_rcp_f32_e32 v64, v64
	v_add_f32_e32 v66, 1.0, v123
	v_rcp_f32_e32 v66, v66
	v_mul_f32_e32 v72, v68, v62
	v_mul_f32_e32 v73, v69, v63
	v_sub_f32_e32 v52, v200, v52
	v_sub_f32_e32 v53, v201, v53
	v_mul_f32_e32 v74, v64, v72
	v_mul_f32_e32 v75, v65, v73
	v_mov_b32_e32 v200, v69
	v_mul_f32_e32 v66, v66, v74
	v_mul_f32_e32 v67, v67, v75
	v_mov_b32_e32 v62, v73
	v_mov_b32_e32 v63, v69
	v_mov_b32_e32 v64, v75
	v_mov_b32_e32 v65, v73
	v_mov_b32_e32 v70, v67
	v_mov_b32_e32 v71, v75
	v_mov_b32_e32 v69, v201
	v_mov_b32_e32 v73, v68
	v_sub_f32_e32 v64, v64, v70
	v_sub_f32_e32 v65, v65, v71
	v_sub_f32_e32 v70, v68, v72
	v_sub_f32_e32 v71, v69, v73
	v_mov_b32_e32 v75, v72
	v_add_f32_e32 v72, 1.0, v122
	v_sub_f32_e32 v62, v200, v62
	v_sub_f32_e32 v63, v201, v63
	v_rcp_f32_e32 v200, v72
	v_add_f32_e32 v72, 1.0, v121
	v_rcp_f32_e32 v72, v72
	v_add_f32_e32 v73, 1.0, v120
	v_rcp_f32_e32 v76, v73
	v_add_f32_e32 v73, 1.0, v119
	v_rcp_f32_e32 v77, v73
	v_mov_b32_e32 v68, v66
	v_mov_b32_e32 v69, v74
	v_sub_f32_e32 v68, v74, v68
	v_sub_f32_e32 v69, v75, v69
	v_mul_f32_e32 v74, v200, v72
	v_mul_f32_e32 v78, v76, v74
	v_mov_b32_e32 v75, v200
	v_mul_f32_e32 v76, v77, v78
	v_mov_b32_e32 v79, v74
	v_mov_b32_e32 v77, v78
	v_sub_f32_e32 v72, v200, v74
	v_sub_f32_e32 v73, v201, v75
	v_sub_f32_e32 v74, v78, v76
	v_sub_f32_e32 v75, v79, v77
	v_add_f32_e32 v77, 1.0, v118
	v_rcp_f32_e32 v200, v77
	v_add_f32_e32 v77, 1.0, v117
	v_rcp_f32_e32 v77, v77
	v_add_f32_e32 v78, 1.0, v115
	v_rcp_f32_e32 v82, v78
	v_add_f32_e32 v78, 1.0, v114
	v_rcp_f32_e32 v83, v78
	v_mul_f32_e32 v80, v200, v77
	v_mul_f32_e32 v92, v82, v80
	v_add_f32_e32 v77, 1.0, v113
	v_mov_b32_e32 v81, v200
	v_mul_f32_e32 v82, v83, v92
	v_mov_b32_e32 v93, v80
	v_mov_b32_e32 v83, v92
	v_rcp_f32_e32 v99, v77
	v_add_f32_e32 v77, 1.0, v112
	v_sub_f32_e32 v78, v200, v80
	v_sub_f32_e32 v79, v201, v81
	v_sub_f32_e32 v80, v92, v82
	v_sub_f32_e32 v81, v93, v83
	v_rcp_f32_e32 v93, v77
	v_add_f32_e32 v77, 1.0, v111
	v_rcp_f32_e32 v95, v77
	v_add_f32_e32 v77, 1.0, v110
	v_rcp_f32_e32 v97, v77
	v_add_f32_e32 v77, 1.0, v109
	v_rcp_f32_e32 v98, v77
	v_add_f32_e32 v77, 1.0, v108
	v_rcp_f32_e32 v92, v77
	v_add_f32_e32 v77, 1.0, v91
	v_rcp_f32_e32 v94, v77
	v_add_f32_e32 v34, 1.0, v34
	v_rcp_f32_e32 v96, v34
	v_mul_f32_e32 v108, v98, v92
	v_mul_f32_e32 v109, v99, v93
	v_mov_b32_e32 v200, v99
	v_mul_f32_e32 v110, v94, v108
	v_mul_f32_e32 v111, v95, v109
	v_mov_b32_e32 v92, v109
	v_mul_f32_e32 v96, v96, v110
	v_mul_f32_e32 v97, v97, v111
	v_mov_b32_e32 v93, v99
	v_mov_b32_e32 v94, v111
	v_mov_b32_e32 v95, v109
	v_mov_b32_e32 v100, v97
	v_mov_b32_e32 v101, v111
	v_mov_b32_e32 v99, v201
	v_mov_b32_e32 v109, v98
	v_sub_f32_e32 v94, v94, v100
	v_sub_f32_e32 v95, v95, v101
	v_sub_f32_e32 v100, v98, v108
	v_sub_f32_e32 v101, v99, v109
	v_mov_b32_e32 v111, v108
	v_mov_b32_e32 v98, v96
	v_mov_b32_e32 v99, v110
	v_sub_f32_e32 v92, v200, v92
	v_sub_f32_e32 v93, v201, v93
	v_sub_f32_e32 v98, v110, v98
	v_sub_f32_e32 v99, v111, v99
;     ...
;                     float pt = P_run;
; #pragma unroll
;                     for (int k = 7; k >= 0; --k) {
;                         auto rr = __builtin_amdgcn_permlane32_swap(__float_as_uint(gp[k]), __float_as_uint(gp[k]), false, false);
;                         const float lo = __uint_as_float(rr[0]), up = __uint_as_float(rr[1]);
;                         const float mul = hi == 0 ? pt * up : pt;
;                         const int blk = k >> 2, g = k & 3;
; #pragma unroll
;                         for (int jj = 0; jj < 4; ++jj) { const int r = 4 * g + jj; if (blk) p1[r] *= mul; else p0[r] *= mul; }
;                         pt *= lo * up;
;                     }
;                     P_run = pt;
;                     pv(o, p0, p1, lds + L_V + buf * 8192, lane);
;                     wdone = __all(P_run < 1.1754944e-38f);
.LBB0_478:
	v_mov_b32_e32 v77, v96
	s_nop 1
	v_permlane32_swap_b32_e32 v96, v77
	v_mul_f32_e32 v34, v90, v77
	v_cndmask_b32_e64 v34, v90, v34, s[18:19]
	v_mul_f32_e32 v114, v98, v34
	v_mul_f32_e32 v115, v99, v34
	v_mov_b32_e32 v99, v97
	s_nop 1
	v_permlane32_swap_b32_e32 v97, v99
	v_mul_f32_e32 v98, v96, v77
	v_mov_b32_e32 v91, v97
	v_mul_f32_e32 v90, v90, v98
	v_mul_f32_e32 v91, v91, v99
	v_mul_f32_e32 v100, v100, v34
	v_mul_f32_e32 v101, v101, v34
	v_mul_f32_e32 v34, v90, v99
	v_mov_b32_e32 v77, v82
	v_cndmask_b32_e64 v34, v90, v34, s[18:19]
	v_pk_mul_f32 v[90:91], v[90:91], v[90:91] op_sel:[0,1] op_sel_hi:[1,0]
	v_permlane32_swap_b32_e32 v82, v77
	v_mul_f32_e32 v112, v94, v34
	v_mul_f32_e32 v113, v95, v34
	v_mul_f32_e32 v118, v92, v34
	v_mul_f32_e32 v119, v93, v34
	v_mul_f32_e32 v34, v90, v77
	v_cndmask_b32_e64 v34, v90, v34, s[18:19]
	v_mul_f32_e32 v120, v78, v34
	v_mul_f32_e32 v121, v79, v34
	v_mov_b32_e32 v79, v76
	s_nop 1
	v_permlane32_swap_b32_e32 v76, v79
	v_mul_f32_e32 v78, v82, v77
	v_mov_b32_e32 v91, v76
	v_mul_f32_e32 v76, v90, v78
	v_mul_f32_e32 v77, v91, v79
	v_mul_f32_e32 v110, v80, v34
	v_mul_f32_e32 v111, v81, v34
	v_mul_f32_e32 v34, v76, v79
	v_cndmask_b32_e64 v34, v76, v34, s[18:19]
	v_mul_f32_e32 v122, v72, v34
	v_mul_f32_e32 v123, v73, v34
	v_mul_f32_e32 v72, v76, v77
	v_mul_f32_e32 v73, v77, v76
	v_mul_f32_e32 v108, v74, v34
	v_mul_f32_e32 v109, v75, v34
	v_mov_b32_e32 v73, v66
	s_nop 1
	v_permlane32_swap_b32_e32 v66, v73
	v_mul_f32_e32 v34, v72, v73
	v_cndmask_b32_e64 v34, v72, v34, s[18:19]
	v_mul_f32_e32 v98, v68, v34
	v_mul_f32_e32 v99, v69, v34
	v_mov_b32_e32 v69, v67
	s_nop 1
	v_permlane32_swap_b32_e32 v67, v69
	v_mul_f32_e32 v68, v66, v73
	v_mov_b32_e32 v73, v67
	v_mul_f32_e32 v66, v72, v68
	v_mul_f32_e32 v67, v73, v69
	v_mul_f32_e32 v124, v70, v34
	v_mul_f32_e32 v125, v71, v34
	v_mul_f32_e32 v34, v66, v69
	v_cndmask_b32_e64 v34, v66, v34, s[18:19]
	v_mul_f32_e32 v126, v62, v34
	v_mul_f32_e32 v127, v63, v34
	v_mul_f32_e32 v62, v66, v67
	v_mul_f32_e32 v63, v67, v66
	v_mul_f32_e32 v96, v64, v34
	v_mul_f32_e32 v97, v65, v34
	v_mov_b32_e32 v63, v54
	s_nop 1
	v_permlane32_swap_b32_e32 v54, v63
	v_mul_f32_e32 v34, v62, v63
	v_cndmask_b32_e64 v34, v62, v34, s[18:19]
	v_mul_f32_e32 v128, v58, v34
	v_mul_f32_e32 v129, v59, v34
	v_mov_b32_e32 v59, v55
	s_nop 1
	v_permlane32_swap_b32_e32 v55, v59
	v_mul_f32_e32 v58, v54, v63
	v_mov_b32_e32 v63, v55
	v_mul_f32_e32 v54, v62, v58
	v_mul_f32_e32 v55, v63, v59
	v_mul_f32_e32 v94, v60, v34
	v_mul_f32_e32 v95, v61, v34
	v_mul_f32_e32 v34, v54, v59
	v_cndmask_b32_e64 v34, v54, v34, s[18:19]
	s_add_i32 s34, s34, 0xc000
	v_mul_f32_e32 v92, v56, v34
	v_mul_f32_e32 v93, v57, v34
	v_mul_f32_e32 v130, v52, v34
	v_mul_f32_e32 v131, v53, v34
	v_add_u32_e32 v34, s34, v107
	v_mul_f32_e32 v90, v54, v55
	ds_read_b64_tr_b16 v[52:53], v34
	ds_read_b64_tr_b16 v[54:55], v34 offset:512
	ds_read_b64_tr_b16 v[56:57], v34 offset:1024
	ds_read_b64_tr_b16 v[58:59], v34 offset:1536
	ds_read_b64_tr_b16 v[60:61], v34 offset:2048
	ds_read_b64_tr_b16 v[62:63], v34 offset:2560
	ds_read_b64_tr_b16 v[64:65], v34 offset:3072
	ds_read_b64_tr_b16 v[66:67], v34 offset:3584
	ds_read_b64_tr_b16 v[68:69], v34 offset:4096
	ds_read_b64_tr_b16 v[70:71], v34 offset:4608
	ds_read_b64_tr_b16 v[72:73], v34 offset:5120
	ds_read_b64_tr_b16 v[74:75], v34 offset:5632
	ds_read_b64_tr_b16 v[76:77], v34 offset:6144
	ds_read_b64_tr_b16 v[78:79], v34 offset:6656
	ds_read_b64_tr_b16 v[80:81], v34 offset:7168
	ds_read_b64_tr_b16 v[82:83], v34 offset:7680
	v_cvt_pk_bf16_f32 v92, v92, v93
	v_cvt_pk_bf16_f32 v93, v130, v131
	v_cvt_pk_bf16_f32 v94, v94, v95
	v_cvt_pk_bf16_f32 v95, v128, v129
	v_cvt_pk_bf16_f32 v96, v96, v97
	v_cvt_pk_bf16_f32 v97, v126, v127
	v_cvt_pk_bf16_f32 v98, v98, v99
	v_cvt_pk_bf16_f32 v99, v124, v125
	v_cvt_pk_bf16_f32 v108, v108, v109
	v_cvt_pk_bf16_f32 v109, v122, v123
	v_cvt_pk_bf16_f32 v110, v110, v111
	v_cvt_pk_bf16_f32 v111, v120, v121
	v_cvt_pk_bf16_f32 v112, v112, v113
	v_cvt_pk_bf16_f32 v113, v118, v119
	v_cvt_pk_bf16_f32 v114, v114, v115
	v_cvt_pk_bf16_f32 v115, v100, v101
	s_waitcnt lgkmcnt(14)
	v_mfma_f32_32x32x16_bf16 v[36:51], v[52:55], v[92:95], v[36:51]
	v_cmp_gt_f32_e32 vcc, s76, v90
	s_cmp_eq_u64 vcc, exec
	s_cselect_b64 s[30:31], -1, 0
	s_waitcnt lgkmcnt(6)
	v_mfma_f32_32x32x16_bf16 v[18:33], v[68:71], v[92:95], v[18:33]
	v_mfma_f32_32x32x16_bf16 v[36:51], v[56:59], v[96:99], v[36:51]
	s_waitcnt lgkmcnt(4)
	v_mfma_f32_32x32x16_bf16 v[18:33], v[72:75], v[96:99], v[18:33]
	v_mfma_f32_32x32x16_bf16 v[36:51], v[60:63], v[108:111], v[36:51]
	s_waitcnt lgkmcnt(2)
	v_mfma_f32_32x32x16_bf16 v[18:33], v[76:79], v[108:111], v[18:33]
	v_mfma_f32_32x32x16_bf16 v[36:51], v[64:67], v[112:115], v[36:51]
	s_waitcnt lgkmcnt(0)
	v_mfma_f32_32x32x16_bf16 v[18:33], v[80:83], v[112:115], v[18:33]

; #define LAS __attribute__((address_space(3)))
; __device__ __forceinline__ int crow(int r, int hi) { return (r & 3) + 8 * (r >> 2) + 4 * hi; }
; __device__ __forceinline__ void online_step(f32x16& p0, f32x16& p1, float& m_run, float& l_part, f32x16 (&o)[2]) {
;     float mt = fmaxf(p0[0], p1[0]);
; #pragma unroll
;     for (int r = 1; r < 16; ++r) mt = fmaxf(mt, fmaxf(p0[r], p1[r]));
;     mt = other_half_max(mt);
;     const float mn = fmaxf(m_run, mt);
;     const float msafe = mn == -INFINITY ? 0.f : mn;
;     const float f = __builtin_amdgcn_exp2f(m_run - msafe);
;     float rs = 0.f;
; #pragma unroll
;     for (int r = 0; r < 16; ++r) { p0[r] = __builtin_amdgcn_exp2f(p0[r] - msafe); p1[r] = __builtin_amdgcn_exp2f(p1[r] - msafe); rs += p0[r] + p1[r]; }
;     ...
; #pragma unroll 1
;     ...
;                 if (tt < tt_lo) break;
;                 f32x16 p0, p1;
;                 qkt(p0, p1, lds + L_K + tt * 8192, qr, cinit, r32, hi);
;                 const LAS float* tb = tab + (32 * wid + r32 + 192 - 64 * tt - 4 * hi - 63);
; #pragma unroll
;                 for (int r = 0; r < 16; ++r) { p0[r] += tb[63 - crow(r, 0)]; p1[r] += tb[31 - crow(r, 0)]; }
.LBB0_486:
	v_add_u32_e32 v34, s69, v117
	ds_read_b128 v[52:55], v34
	ds_read_b128 v[84:87], v34 offset:4096
	v_add_u32_e32 v34, s69, v118
	ds_read_b128 v[88:91], v34
	ds_read_b128 v[92:95], v34 offset:4096
	v_add_u32_e32 v34, s69, v119
	ds_read_b128 v[96:99], v34
	ds_read_b128 v[100:103], v34 offset:4096
	v_add_u32_e32 v34, s69, v120
	ds_read_b128 v[104:107], v34
	ds_read_b128 v[108:111], v34 offset:4096
	s_waitcnt lgkmcnt(7)
	v_mfma_f32_32x32x16_bf16 v[68:83], v[52:55], v[132:135], v[2:17]
	s_waitcnt lgkmcnt(6)
	v_mfma_f32_32x32x16_bf16 v[52:67], v[84:87], v[132:135], v[2:17]
	ds_read2_b32 v[84:85], v1 offset0:58 offset1:59
	s_waitcnt lgkmcnt(6)
	v_mfma_f32_32x32x16_bf16 v[68:83], v[88:91], v[136:139], v[68:83]
	s_waitcnt lgkmcnt(5)
	v_mfma_f32_32x32x16_bf16 v[52:67], v[92:95], v[136:139], v[52:67]
	s_waitcnt lgkmcnt(4)
	v_mfma_f32_32x32x16_bf16 v[68:83], v[96:99], v[140:143], v[68:83]
	s_waitcnt lgkmcnt(3)
	v_mfma_f32_32x32x16_bf16 v[52:67], v[100:103], v[140:143], v[52:67]
	s_waitcnt lgkmcnt(2)
	v_mfma_f32_32x32x16_bf16 v[68:83], v[104:107], v[144:147], v[68:83]
	s_waitcnt lgkmcnt(1)
	v_mfma_f32_32x32x16_bf16 v[52:67], v[108:111], v[144:147], v[52:67]
	s_waitcnt lgkmcnt(0)
	s_nop 8
	v_add_f32_e64 v112, v68, v85
	v_add_f32_e64 v113, v69, v84
	ds_read2_b32 v[68:69], v1 offset0:26 offset1:27
	s_waitcnt lgkmcnt(0)
	v_add_f32_e32 v114, v52, v69
	v_add_f32_e32 v115, v53, v68
	ds_read2_b32 v[52:53], v1 offset0:56 offset1:57
	s_waitcnt lgkmcnt(0)
	v_add_f32_e32 v100, v70, v53
	v_add_f32_e32 v101, v71, v52
	ds_read2_b32 v[52:53], v1 offset0:24 offset1:25
	s_waitcnt lgkmcnt(0)
	v_add_f32_e32 v110, v54, v53
	v_add_f32_e32 v111, v55, v52
	ds_read2_b32 v[52:53], v1 offset0:50 offset1:51
	s_waitcnt lgkmcnt(0)
	v_add_f32_e32 v102, v72, v53
	v_add_f32_e32 v103, v73, v52
	ds_read2_b32 v[52:53], v1 offset0:18 offset1:19
	s_waitcnt lgkmcnt(0)
	v_add_f32_e32 v108, v56, v53
	v_add_f32_e32 v109, v57, v52
	ds_read2_b32 v[52:53], v1 offset0:48 offset1:49
	s_waitcnt lgkmcnt(0)
	v_add_f32_e32 v96, v74, v53
	v_add_f32_e32 v97, v75, v52
	ds_read2_b32 v[52:53], v1 offset0:16 offset1:17
	s_waitcnt lgkmcnt(0)
	v_add_f32_e32 v106, v58, v53
	v_add_f32_e32 v107, v59, v52
	ds_read2_b32 v[52:53], v1 offset0:42 offset1:43
	s_waitcnt lgkmcnt(0)
	v_add_f32_e32 v94, v76, v53
	v_add_f32_e32 v95, v77, v52
	ds_read2_b32 v[52:53], v1 offset0:10 offset1:11
	s_waitcnt lgkmcnt(0)
	v_add_f32_e32 v104, v60, v53
	v_add_f32_e32 v105, v61, v52
	ds_read2_b32 v[52:53], v1 offset0:40 offset1:41
	s_waitcnt lgkmcnt(0)
	v_add_f32_e32 v90, v78, v53
	v_add_f32_e32 v91, v79, v52
	ds_read2_b32 v[52:53], v1 offset0:8 offset1:9
	s_waitcnt lgkmcnt(0)
	v_add_f32_e32 v98, v62, v53
	v_add_f32_e32 v99, v63, v52
	ds_read2_b32 v[52:53], v1 offset0:34 offset1:35
	s_waitcnt lgkmcnt(0)
	v_add_f32_e32 v88, v80, v53
	v_add_f32_e32 v89, v81, v52
	ds_read2_b32 v[52:53], v1 offset0:2 offset1:3
	s_waitcnt lgkmcnt(0)
	v_add_f32_e32 v92, v64, v53
	v_add_f32_e32 v93, v65, v52
	ds_read2_b32 v[52:53], v1 offset0:32 offset1:33
	s_waitcnt lgkmcnt(0)
	v_add_f32_e32 v86, v82, v53
	v_add_f32_e32 v87, v83, v52
	ds_read2_b32 v[52:53], v1 offset1:1
	s_waitcnt lgkmcnt(0)
	v_add_f32_e32 v84, v66, v53
	v_add_f32_e32 v85, v67, v52
	s_and_saveexec_b64 s[18:19], s[8:9]
	s_xor_b64 s[18:19], exec, s[18:19]
	s_cbranch_execz .LBB0_488
	v_max_f32_e32 v34, v115, v115
	v_max_f32_e32 v52, v113, v113
	v_max_f32_e32 v34, v52, v34
	v_max_f32_e32 v52, v110, v110
	v_max_f32_e32 v53, v100, v100
	v_max_f32_e32 v52, v53, v52
	v_max_f32_e32 v53, v111, v111
	v_max_f32_e32 v54, v101, v101
	v_max3_f32 v34, v112, v114, v34
	v_max_f32_e32 v53, v54, v53
	v_max3_f32 v34, v34, v52, v53
	v_max_f32_e32 v52, v108, v108
	v_max_f32_e32 v53, v102, v102
	v_max_f32_e32 v52, v53, v52
	v_max_f32_e32 v53, v109, v109
	v_max_f32_e32 v54, v103, v103
	v_max_f32_e32 v53, v54, v53
	v_max3_f32 v34, v34, v52, v53
	v_max_f32_e32 v52, v106, v106
	v_max_f32_e32 v53, v96, v96
	v_max_f32_e32 v52, v53, v52
	v_max_f32_e32 v53, v107, v107
	v_max_f32_e32 v54, v97, v97
	v_max_f32_e32 v53, v54, v53
	v_max3_f32 v34, v34, v52, v53
	v_max_f32_e32 v52, v104, v104
	v_max_f32_e32 v53, v94, v94
	v_max_f32_e32 v52, v53, v52
	v_max_f32_e32 v53, v105, v105
	v_max_f32_e32 v54, v95, v95
	v_max_f32_e32 v53, v54, v53
	v_max3_f32 v34, v34, v52, v53
	v_max_f32_e32 v52, v98, v98
	v_max_f32_e32 v53, v90, v90
	v_max_f32_e32 v52, v53, v52
	v_max_f32_e32 v53, v99, v99
	v_max_f32_e32 v54, v91, v91
	v_max_f32_e32 v53, v54, v53
	v_max3_f32 v34, v34, v52, v53
	v_max_f32_e32 v52, v92, v92
	v_max_f32_e32 v53, v88, v88
	v_max_f32_e32 v52, v53, v52
	v_max_f32_e32 v53, v93, v93
	v_max_f32_e32 v54, v89, v89
	v_max_f32_e32 v53, v54, v53
	v_max3_f32 v34, v34, v52, v53
	v_max_f32_e32 v52, v84, v84
	v_max_f32_e32 v53, v86, v86
	v_max_f32_e32 v52, v53, v52
	v_max_f32_e32 v53, v85, v85
	v_max_f32_e32 v54, v87, v87
	v_max_f32_e32 v53, v54, v53
	v_max3_f32 v34, v34, v52, v53
	v_mov_b32_e32 v52, v34
	s_nop 1
	v_permlane32_swap_b32_e32 v34, v52
	v_max3_f32 v124, v123, v34, v52
	v_cmp_neq_f32_e32 vcc, s57, v124
	s_nop 1
	v_cndmask_b32_e32 v53, 0, v124, vcc
	v_sub_f32_e32 v34, v112, v53
	v_exp_f32_e32 v68, v34
	v_sub_f32_e32 v34, v114, v53
	v_exp_f32_e32 v52, v34
	v_sub_f32_e32 v34, v113, v53
	v_exp_f32_e32 v112, v34
	v_sub_f32_e32 v34, v115, v53
	v_exp_f32_e32 v34, v34
	v_add_f32_e32 v113, v68, v52
	v_mov_b32_e32 v69, v112
	v_add_f32_e32 v54, v112, v34
	v_add_f32_e32 v55, v113, v35
	s_nop 0
	v_add_f32_e32 v114, v54, v54
	v_add_f32_e32 v115, v54, v55
	v_sub_f32_e32 v54, v100, v53
	v_exp_f32_e32 v70, v54
	v_sub_f32_e32 v54, v110, v53
	v_sub_f32_e32 v55, v101, v53
	v_exp_f32_e32 v54, v54
	v_exp_f32_e32 v100, v55
; __device__ __forceinline__ void exp_sum(f32x16& p0, f32x16& p1, float& l_part) {
;     float rs = 0.f;
; #pragma unroll
;     for (int r = 0; r < 16; ++r) { p0[r] = __builtin_amdgcn_exp2f(p0[r]); p1[r] = __builtin_amdgcn_exp2f(p1[r]); rs += p0[r] + p1[r]; }
;     l_part += rs;
; }
; __device__ __forceinline__ void online_step(f32x16& p0, f32x16& p1, float& m_run, float& l_part, f32x16 (&o)[2]) {
;     float mt = fmaxf(p0[0], p1[0]);
; #pragma unroll
;     for (int r = 1; r < 16; ++r) mt = fmaxf(mt, fmaxf(p0[r], p1[r]));
;     mt = other_half_max(mt);
;     const float mn = fmaxf(m_run, mt);
;     const float msafe = mn == -INFINITY ? 0.f : mn;
;     const float f = __builtin_amdgcn_exp2f(m_run - msafe);
;     float rs = 0.f;
; #pragma unroll
;     for (int r = 0; r < 16; ++r) { p0[r] = __builtin_amdgcn_exp2f(p0[r] - msafe); p1[r] = __builtin_amdgcn_exp2f(p1[r] - msafe); rs += p0[r] + p1[r]; }
;     l_part = l_part * f + rs; m_run = mn;
; #pragma unroll
;     for (int r = 0; r < 16; ++r) { o[0][r] *= f; o[1][r] *= f; }
; }
	v_sub_f32_e32 v55, v111, v53
	v_exp_f32_e32 v114, v55
	v_add_f32_e32 v101, v70, v54
	v_sub_f32_e32 v55, v102, v53
	v_exp_f32_e32 v72, v55
	v_add_f32_e32 v56, v100, v114
	v_add_f32_e32 v57, v101, v115
	v_sub_f32_e32 v55, v108, v53
	v_add_f32_e32 v110, v56, v56
	v_add_f32_e32 v111, v56, v57
	v_exp_f32_e32 v56, v55
	v_sub_f32_e32 v55, v103, v53
	v_exp_f32_e32 v102, v55
	v_sub_f32_e32 v55, v109, v53
	v_exp_f32_e32 v110, v55
	v_add_f32_e32 v103, v72, v56
	v_sub_f32_e32 v55, v96, v53
	v_exp_f32_e32 v74, v55
	v_add_f32_e32 v58, v102, v110
	v_add_f32_e32 v59, v103, v111
	v_sub_f32_e32 v55, v106, v53
	v_add_f32_e32 v108, v58, v58
	v_add_f32_e32 v109, v58, v59
	v_exp_f32_e32 v58, v55
	v_sub_f32_e32 v55, v97, v53
	v_exp_f32_e32 v96, v55
	v_sub_f32_e32 v55, v107, v53
	v_exp_f32_e32 v108, v55
	v_add_f32_e32 v97, v74, v58
	v_sub_f32_e32 v55, v94, v53
	v_exp_f32_e32 v76, v55
	v_add_f32_e32 v60, v96, v108
	v_add_f32_e32 v61, v97, v109
	v_sub_f32_e32 v55, v104, v53
	v_add_f32_e32 v106, v60, v60
	v_add_f32_e32 v107, v60, v61
	v_exp_f32_e32 v60, v55
	v_sub_f32_e32 v55, v95, v53
	v_exp_f32_e32 v94, v55
	v_sub_f32_e32 v55, v105, v53
	v_exp_f32_e32 v106, v55
	v_add_f32_e32 v95, v76, v60
	v_sub_f32_e32 v55, v90, v53
	v_exp_f32_e32 v78, v55
	v_add_f32_e32 v62, v94, v106
	v_add_f32_e32 v63, v95, v107
	v_sub_f32_e32 v55, v98, v53
	v_add_f32_e32 v104, v62, v62
	v_add_f32_e32 v105, v62, v63
	v_exp_f32_e32 v62, v55
	v_sub_f32_e32 v55, v91, v53
	v_exp_f32_e32 v90, v55
	v_sub_f32_e32 v55, v99, v53
	v_exp_f32_e32 v104, v55
	v_add_f32_e32 v91, v78, v62
	v_sub_f32_e32 v55, v88, v53
	v_exp_f32_e32 v80, v55
	v_add_f32_e32 v64, v90, v104
	v_add_f32_e32 v65, v91, v105
	v_sub_f32_e32 v55, v92, v53
	v_add_f32_e32 v98, v64, v64
	v_add_f32_e32 v99, v64, v65
	v_exp_f32_e32 v64, v55
	v_sub_f32_e32 v55, v89, v53
	v_exp_f32_e32 v88, v55
	v_sub_f32_e32 v55, v93, v53
	v_exp_f32_e32 v98, v55
	v_sub_f32_e32 v55, v86, v53
	v_exp_f32_e32 v82, v55
	v_sub_f32_e32 v55, v84, v53
	v_sub_f32_e32 v95, v123, v53
	v_exp_f32_e32 v66, v55
	v_sub_f32_e32 v55, v87, v53
	v_sub_f32_e32 v53, v85, v53
	v_exp_f32_e32 v83, v55
	v_exp_f32_e32 v67, v53
	v_add_f32_e32 v89, v80, v64
	v_add_f32_e32 v92, v88, v98
	v_add_f32_e32 v93, v89, v99
	v_mov_b32_e32 v53, v34
	v_add_f32_e32 v93, v92, v93
	v_add_f32_e32 v92, v92, v92
	v_exp_f32_e32 v34, v95
	v_add_f32_e32 v89, v82, v66
	v_mov_b32_e32 v81, v88
	v_mov_b32_e32 v88, v83
	v_mov_b32_e32 v92, v67
	v_add_f32_e32 v84, v88, v92
	v_add_f32_e32 v85, v89, v93
	v_mov_b32_e32 v71, v100
	v_add_f32_e32 v125, v84, v85
	v_mov_b32_e32 v73, v102
	v_mov_b32_e32 v75, v96
	v_mov_b32_e32 v77, v94
	v_mov_b32_e32 v79, v90
	v_mov_b32_e32 v55, v114
	v_mov_b32_e32 v57, v110
	v_mov_b32_e32 v59, v108
	v_mov_b32_e32 v61, v106
	v_mov_b32_e32 v63, v104
	v_mov_b32_e32 v65, v98
	v_fmac_f32_e32 v125, v122, v34
	v_mul_f32_e32 v50, v50, v34
	v_mul_f32_e32 v51, v51, v34
	v_mul_f32_e32 v48, v48, v34
	v_mul_f32_e32 v49, v49, v34
	v_mul_f32_e32 v46, v46, v34
	v_mul_f32_e32 v47, v47, v34
	v_mul_f32_e32 v44, v44, v34
	v_mul_f32_e32 v45, v45, v34
	v_mul_f32_e32 v42, v42, v34
	v_mul_f32_e32 v43, v43, v34
	v_mul_f32_e32 v40, v40, v34
	v_mul_f32_e32 v41, v41, v34
	v_mul_f32_e32 v38, v38, v34
	v_mul_f32_e32 v39, v39, v34
	v_mul_f32_e32 v36, v36, v34
	v_mul_f32_e32 v37, v37, v34
	v_mul_f32_e32 v32, v32, v34
	v_mul_f32_e32 v33, v33, v34
	v_mul_f32_e32 v30, v30, v34
	v_mul_f32_e32 v31, v31, v34
	v_mul_f32_e32 v28, v28, v34
	v_mul_f32_e32 v29, v29, v34
	v_mul_f32_e32 v26, v26, v34
	v_mul_f32_e32 v27, v27, v34
	v_mul_f32_e32 v24, v24, v34
	v_mul_f32_e32 v25, v25, v34
	v_mul_f32_e32 v22, v22, v34
	v_mul_f32_e32 v23, v23, v34
	v_mul_f32_e32 v20, v20, v34
	v_mul_f32_e32 v21, v21, v34
	v_mul_f32_e32 v18, v18, v34
	v_mul_f32_e32 v19, v19, v34
.LBB0_488:
	s_andn2_saveexec_b64 s[18:19], s[18:19]
	s_cbranch_execz .LBB0_490
	v_exp_f32_e32 v68, v112
	v_exp_f32_e32 v52, v114
	v_exp_f32_e32 v57, v113
	v_exp_f32_e32 v59, v115
	v_exp_f32_e32 v70, v100
	v_exp_f32_e32 v54, v110
	v_exp_f32_e32 v71, v101
	v_add_f32_e32 v56, v68, v52
	v_mov_b32_e32 v58, v35
	v_exp_f32_e32 v63, v111
	v_add_f32_e32 v60, v56, v58
	v_add_f32_e32 v61, v57, v59
	v_exp_f32_e32 v72, v102
	v_exp_f32_e32 v56, v108
	v_pk_add_f32 v[60:61], v[60:61], v[60:61] op_sel:[0,1] op_sel_hi:[1,0]
	v_exp_f32_e32 v73, v103
	v_add_f32_e32 v62, v70, v54
	v_mov_b32_e32 v61, v71
	v_exp_f32_e32 v65, v109
	v_add_f32_e32 v60, v60, v62
	v_add_f32_e32 v61, v61, v63
	v_exp_f32_e32 v74, v96
	v_exp_f32_e32 v58, v106
	v_pk_add_f32 v[60:61], v[60:61], v[60:61] op_sel:[0,1] op_sel_hi:[1,0]
	v_exp_f32_e32 v75, v97
	v_add_f32_e32 v64, v72, v56
	v_mov_b32_e32 v61, v73
	v_exp_f32_e32 v97, v107
	v_add_f32_e32 v66, v60, v64
	v_add_f32_e32 v67, v61, v65
	v_exp_f32_e32 v76, v94
	v_exp_f32_e32 v60, v104
	v_pk_add_f32 v[66:67], v[66:67], v[66:67] op_sel:[0,1] op_sel_hi:[1,0]
	v_exp_f32_e32 v77, v95
	v_add_f32_e32 v96, v74, v58
	v_mov_b32_e32 v67, v75
	v_exp_f32_e32 v95, v105
	v_add_f32_e32 v66, v66, v96
	v_add_f32_e32 v67, v67, v97
	v_exp_f32_e32 v78, v90
	v_exp_f32_e32 v62, v98
	v_pk_add_f32 v[66:67], v[66:67], v[66:67] op_sel:[0,1] op_sel_hi:[1,0]
	v_exp_f32_e32 v79, v91
	v_add_f32_e32 v94, v76, v60
	v_mov_b32_e32 v67, v77
	v_exp_f32_e32 v91, v99
	v_add_f32_e32 v66, v66, v94
	v_add_f32_e32 v67, v67, v95
	v_exp_f32_e32 v80, v88
	v_exp_f32_e32 v64, v92
	v_pk_add_f32 v[66:67], v[66:67], v[66:67] op_sel:[0,1] op_sel_hi:[1,0]
	v_exp_f32_e32 v81, v89
	v_add_f32_e32 v90, v78, v62
	v_mov_b32_e32 v67, v79
	v_exp_f32_e32 v89, v93
	v_add_f32_e32 v98, v66, v90
	v_add_f32_e32 v99, v67, v91
	v_exp_f32_e32 v82, v86
	v_exp_f32_e32 v66, v84
	v_add_f32_e32 v92, v98, v99
	v_add_f32_e32 v93, v99, v98
	v_exp_f32_e32 v83, v87
	v_exp_f32_e32 v67, v85
	v_add_f32_e32 v88, v80, v64
	v_mov_b32_e32 v93, v81
	v_add_f32_e32 v92, v92, v88
	v_add_f32_e32 v93, v93, v89
	v_add_f32_e32 v84, v82, v66
	v_add_f32_e32 v86, v92, v93
	v_add_f32_e32 v87, v93, v92
	v_mov_b32_e32 v85, v67
	v_mov_b32_e32 v87, v83
	v_add_f32_e32 v84, v86, v84
	v_add_f32_e32 v85, v87, v85
	v_mov_b32_e32 v69, v57
	v_add_f32_e32 v34, v84, v85
	v_mov_b32_e32 v53, v59
	v_mov_b32_e32 v55, v63
	v_mov_b32_e32 v57, v65
	v_mov_b32_e32 v59, v97
	v_mov_b32_e32 v61, v95
	v_mov_b32_e32 v63, v91
	v_mov_b32_e32 v65, v89
	v_add_f32_e32 v125, v122, v34
	v_mov_b32_e32 v124, v123

; #define LAS __attribute__((address_space(3)))
; __device__ __forceinline__ unsigned cvtpk(float lo, float hi) { f32x2_t v = {lo, hi}; bf16x2_t b = __builtin_convertvector(v, bf16x2_t); return __builtin_bit_cast(unsigned, b); }
; template <class RowPtr, class GatePtr>
; __device__ __forceinline__ void store_o(const f32x16 (&o)[2], float scale, LAS unsigned char* lds, int wid, int lane, const RowPtr& rowp, const GatePtr& gatep, bool has_gate) {
;     ...
; #pragma unroll
;     for (int d0 = 0; d0 < 2; ++d0)
; #pragma unroll
;         for (int g = 0; g < 4; ++g) {
;             u32x2 w; w.x = cvtpk(o[d0][4 * g] * scale, o[d0][4 * g + 1] * scale); w.y = cvtpk(o[d0][4 * g + 2] * scale, o[d0][4 * g + 3] * scale);
;             *(LAS u32x2*)(stg + r32 * OST_PITCH + (32 * d0 + 8 * g + 4 * hi) * 2) = w;
;         }
;     asm volatile("s_waitcnt lgkmcnt(0)" ::: "memory");
;     ...
;             } else if (u < AT_NFOX + AT_NDIL) {
;                 const int v2 = u - AT_NFOX, bh = v2 % 48, rest = v2 / 48, b = bh / 6, h = bh % 6, p = rest >> 4, x = rest & 15;
;                 const int dil = p == 0 ? 1 : p == 1 ? 4 : 16, res = x % dil, nb2 = x / dil;
;                 const size_t rb = (size_t)b * S;
;                 const int mw = 256 * nb2 + 32 * wid;
;                 bf16_t* O = dilo + (((size_t)p * 6 + h) * NTOK + rb) * 64;
;                 const size_t mw_row = (size_t)mw * dil + res;
;                 store_o(o, oscale, lds, wid, lane, [&](int row) { return O + (mw_row + (size_t)row * dil) * 64; }, [&](int row) { return (const bf16_t*)nullptr; }, false);
;                 if (hi == 0) dill[((size_t)p * 6 + h) * NTOK + rb + (size_t)(mw + r32) * dil + res] = lse;
.LBB0_517:
	s_andn2_b64 vcc, exec, s[20:21]
	s_cbranch_vccnz .LBB0_521
	s_add_i32 s4, s73, 0xfffffe00
	s_and_b32 s5, s4, 0xffff
	s_mul_i32 s5, s5, 0xaaab
	s_lshr_b32 s12, s5, 21
	s_mul_i32 s13, s12, 48
	s_sub_i32 s13, s4, s13
	s_mul_i32 s14, s13, 0xab
	s_bfe_u32 s16, s14, 0x6000a
	s_mul_i32 s14, s16, 6
	s_sub_i32 s13, s13, s14
	s_and_b32 s13, s13, 0xff
	s_lshr_b32 s17, s5, 25
	s_bfe_u32 s20, s5, 0x40015
	s_cmpk_lt_u32 s4, 0x300
	v_mul_f32_e32 v52, v36, v56
	v_mul_f32_e32 v53, v37, v56
	v_mul_f32_e32 v54, v38, v56
	v_mul_f32_e32 v55, v39, v56
	s_cselect_b64 s[4:5], -1, 0
	s_cmp_eq_u32 s17, 1
	v_cvt_pk_bf16_f32 v52, v52, v53
	v_cvt_pk_bf16_f32 v53, v54, v55
	v_ashrrev_i32_e32 v54, 2, v148
	s_cselect_b32 s21, 3, 15
	s_cselect_b32 s25, 2, 4
	s_and_b64 s[14:15], s[4:5], exec
	v_mul_u32_u24_e32 v34, 0x90, v169
	v_and_b32_e32 v54, -8, v54
	s_cselect_b32 s14, 0, s21
	v_add3_u32 v34, s49, v34, v54
	v_mul_f32_e32 v54, v40, v56
	v_mul_f32_e32 v55, v41, v56
	v_mul_f32_e32 v58, v42, v56
	v_mul_f32_e32 v59, v43, v56
	s_and_b32 s34, s14, s12
	v_cvt_pk_bf16_f32 v54, v54, v55
	v_cvt_pk_bf16_f32 v55, v58, v59
	s_and_b64 s[4:5], s[4:5], exec
	ds_write2_b64 v34, v[52:53], v[54:55] offset1:2
	v_mul_f32_e32 v52, v44, v56
	v_mul_f32_e32 v53, v45, v56
	v_mul_f32_e32 v54, v46, v56
	v_mul_f32_e32 v55, v47, v56
	s_cselect_b32 s35, 0, s25
	v_cvt_pk_bf16_f32 v52, v52, v53
	v_cvt_pk_bf16_f32 v53, v54, v55
	v_mul_f32_e32 v54, v48, v56
	v_mul_f32_e32 v55, v49, v56
	v_mul_f32_e32 v58, v50, v56
	v_mul_f32_e32 v59, v51, v56
	s_lshr_b32 s4, s20, s35
	v_cvt_pk_bf16_f32 v54, v54, v55
	v_cvt_pk_bf16_f32 v55, v58, v59
	s_lshl_b32 s4, s4, 8
	ds_write2_b64 v34, v[52:53], v[54:55] offset0:4 offset1:6
	v_mul_f32_e32 v52, v18, v56
	v_mul_f32_e32 v53, v19, v56
	v_mul_f32_e32 v54, v20, v56
	v_mul_f32_e32 v55, v21, v56
	s_add_i32 s20, s4, s2
	s_mul_i32 s4, s17, 6
	v_cvt_pk_bf16_f32 v52, v52, v53
	v_cvt_pk_bf16_f32 v53, v54, v55
	v_mul_f32_e32 v54, v22, v56
	v_mul_f32_e32 v55, v23, v56
	v_mul_f32_e32 v58, v24, v56
	v_mul_f32_e32 v59, v25, v56
	s_add_i32 s4, s4, s13
	v_cvt_pk_bf16_f32 v54, v54, v55
	v_cvt_pk_bf16_f32 v55, v58, v59
	s_lshl_b32 s5, s16, 12
	s_lshl_b32 s4, s4, 15
	ds_write2_b64 v34, v[52:53], v[54:55] offset0:8 offset1:10
	v_mul_f32_e32 v52, v26, v56
	v_mul_f32_e32 v53, v27, v56
	v_mul_f32_e32 v54, v28, v56
	v_mul_f32_e32 v55, v29, v56
	s_add_i32 s66, s5, s4
	v_readlane_b32 s12, v252, 8
	v_cvt_pk_bf16_f32 v52, v52, v53
	v_cvt_pk_bf16_f32 v53, v54, v55
	v_mul_f32_e32 v54, v30, v56
	v_mul_f32_e32 v55, v31, v56
	v_mul_f32_e32 v58, v32, v56
	v_mul_f32_e32 v59, v33, v56
	s_lshl_b64 s[4:5], s[66:67], 7
	v_readlane_b32 s14, v252, 10
	v_cvt_pk_bf16_f32 v54, v54, v55
	v_cvt_pk_bf16_f32 v55, v58, v59
	v_readlane_b32 s15, v252, 11
	s_add_u32 s28, s14, s4
	ds_write2_b64 v34, v[52:53], v[54:55] offset0:12 offset1:14
	v_ashrrev_i32_e32 v58, 3, v148
	v_lshlrev_b32_e32 v34, 4, v148
	s_movk_i32 s4, 0x90
	s_addc_u32 s29, s15, s5
	s_ashr_i32 s21, s20, 31
	v_and_b32_e32 v34, 0x70, v34
	v_mul_lo_u32 v52, v58, s4
	s_lshl_b64 s[30:31], s[20:21], s35
	s_waitcnt lgkmcnt(0)
	v_add3_u32 v57, s49, v34, v52
	v_ashrrev_i32_e32 v59, 31, v58
	s_or_b32 s30, s30, s34
	ds_read_b128 v[52:55], v57
	v_lshlrev_b64 v[60:61], s35, v[58:59]
	v_lshl_add_u64 v[60:61], v[60:61], 0, s[30:31]
	v_lshlrev_b64 v[60:61], 7, v[60:61]
	v_lshl_add_u64 v[60:61], s[28:29], 0, v[60:61]
	v_lshl_add_u64 v[60:61], v[60:61], 0, v[34:35]
	s_waitcnt lgkmcnt(0)
	global_store_dwordx4 v[60:61], v[52:55], off
	v_add_u32_e32 v60, 8, v58
	v_ashrrev_i32_e32 v61, 31, v60
	ds_read_b128 v[52:55], v57 offset:1152
	v_lshlrev_b64 v[60:61], s35, v[60:61]
	v_lshl_add_u64 v[60:61], v[60:61], 0, s[30:31]
	v_lshlrev_b64 v[60:61], 7, v[60:61]
	v_lshl_add_u64 v[60:61], s[28:29], 0, v[60:61]
	v_lshl_add_u64 v[60:61], v[60:61], 0, v[34:35]
	s_waitcnt lgkmcnt(0)
	global_store_dwordx4 v[60:61], v[52:55], off
	v_add_u32_e32 v60, 16, v58
	v_ashrrev_i32_e32 v61, 31, v60
	ds_read_b128 v[52:55], v57 offset:2304
	v_lshlrev_b64 v[60:61], s35, v[60:61]
	v_lshl_add_u64 v[60:61], v[60:61], 0, s[30:31]
	v_lshlrev_b64 v[60:61], 7, v[60:61]
	v_lshl_add_u64 v[60:61], s[28:29], 0, v[60:61]
	v_add_u32_e32 v58, 24, v58
	v_lshl_add_u64 v[60:61], v[60:61], 0, v[34:35]
	v_ashrrev_i32_e32 v59, 31, v58
	s_waitcnt lgkmcnt(0)
	global_store_dwordx4 v[60:61], v[52:55], off
	ds_read_b128 v[52:55], v57 offset:3456
	v_lshlrev_b64 v[58:59], s35, v[58:59]
	v_lshl_add_u64 v[58:59], v[58:59], 0, s[30:31]
	v_lshlrev_b64 v[58:59], 7, v[58:59]
	v_lshl_add_u64 v[58:59], s[28:29], 0, v[58:59]
	v_lshl_add_u64 v[58:59], v[58:59], 0, v[34:35]
	s_waitcnt lgkmcnt(0)
	global_store_dwordx4 v[58:59], v[52:55], off
	s_waitcnt lgkmcnt(0)
	v_cmp_gt_u32_e32 vcc, 32, v148
	v_readlane_b32 s13, v252, 9
	s_and_saveexec_b64 s[28:29], vcc
	s_cbranch_execz .LBB0_520
	s_lshl_b32 s4, s66, 2
	v_or_b32_e32 v52, s20, v148
	s_add_u32 s4, s82, s4
	v_ashrrev_i32_e32 v53, 31, v52
	s_addc_u32 s5, s83, 0
	v_lshlrev_b64 v[52:53], s35, v[52:53]
	v_lshl_add_u64 v[52:53], v[52:53], 2, s[4:5]
	s_lshl_b32 s66, s34, 2
	v_lshl_add_u64 v[52:53], v[52:53], 0, s[66:67]
	global_store_dword v[52:53], v1, off

; #define LAS __attribute__((address_space(3)))
; __device__ __forceinline__ unsigned cvtpk(float lo, float hi) { f32x2_t v = {lo, hi}; bf16x2_t b = __builtin_convertvector(v, bf16x2_t); return __builtin_bit_cast(unsigned, b); }
; template <class RowPtr, class GatePtr>
; __device__ __forceinline__ void store_o(const f32x16 (&o)[2], float scale, LAS unsigned char* lds, int wid, int lane, const RowPtr& rowp, const GatePtr& gatep, bool has_gate) {
;     ...
;     u32x4 gv[4];
;     if (has_gate) {
; #pragma unroll
;         for (int i = 0; i < 4; ++i) gv[i] = *(const u32x4*)(gatep(i * 8 + (lane >> 3)) + (lane & 7) * 8);
;     }
; #pragma unroll
;     for (int d0 = 0; d0 < 2; ++d0)
; #pragma unroll
;         for (int g = 0; g < 4; ++g) {
;             u32x2 w; w.x = cvtpk(o[d0][4 * g] * scale, o[d0][4 * g + 1] * scale); w.y = cvtpk(o[d0][4 * g + 2] * scale, o[d0][4 * g + 3] * scale);
;             *(LAS u32x2*)(stg + r32 * OST_PITCH + (32 * d0 + 8 * g + 4 * hi) * 2) = w;
;         }
;     ...
;             if (u < AT_NFOX) {
;                 const int qb = 15 - (u >> 5), bh = u & 31, b = bh >> 2, h = bh & 3, tw = qb * 256 + 32 * wid;
;                 const size_t rb = (size_t)b * S;
;                 const bf16_t* G = proj + ((size_t)(12 + h) * NTOK + rb + tw) * 64;
;                 bf16_t* O = mix + ((size_t)h * NTOK + rb + tw) * 64;
;                 store_o(o, oscale, lds, wid, lane, [&](int row) { return O + (size_t)row * 64; }, [&](int row) { return G + (size_t)row * 64; }, true);
.LBB0_522:
	s_lshl_b32 s4, s73, 3
	s_and_b32 s4, s4, 0xffffff00
	s_sub_i32 s20, s48, s4
	s_lshl_b32 s4, s73, 10
	s_lshl_b32 s5, s73, 15
	s_and_b32 s4, s4, 0x7000
	s_and_b32 s5, s5, 0x18000
	s_or_b32 s21, s5, s4
	s_or_b32 s4, s21, 0x60000
	s_ashr_i32 s28, s20, 31
	s_add_u32 s4, s4, s20
	s_addc_u32 s5, 0, s28
	s_lshl_b64 s[4:5], s[4:5], 7
	s_add_u32 s4, s96, s4
	v_ashrrev_i32_e32 v60, 3, v148
	v_lshlrev_b32_e32 v1, 4, v148
	s_addc_u32 s5, s97, s5
	v_and_b32_e32 v34, 0x70, v1
	v_ashrrev_i32_e32 v61, 31, v60
	v_lshl_add_u64 v[62:63], s[4:5], 0, v[34:35]
	v_lshlrev_b64 v[58:59], 7, v[60:61]
	v_lshl_add_u64 v[52:53], v[62:63], 0, v[58:59]
	global_load_dwordx4 v[52:55], v[52:53], off
	s_mov_b64 s[4:5], 0x400
	v_mul_f32_e32 v68, v40, v56
	v_mul_f32_e32 v69, v41, v56
	v_lshl_add_u64 v[40:41], v[58:59], 0, s[4:5]
	v_mul_f32_e32 v64, v36, v56
	v_mul_f32_e32 v65, v37, v56
	v_lshl_add_u64 v[36:37], v[62:63], 0, v[40:41]
	v_mul_f32_e32 v66, v38, v56
	v_mul_f32_e32 v67, v39, v56
	global_load_dwordx4 v[36:39], v[36:37], off
	v_mul_f32_e32 v42, v42, v56
	v_mul_f32_e32 v43, v43, v56
	v_mul_f32_e32 v44, v44, v56
	v_mul_f32_e32 v45, v45, v56
	v_mul_f32_e32 v48, v48, v56
	v_mul_f32_e32 v49, v49, v56
	v_mul_f32_e32 v22, v22, v56
	v_mul_f32_e32 v23, v23, v56
	v_mul_f32_e32 v46, v46, v56
	v_mul_f32_e32 v47, v47, v56
	v_mul_f32_e32 v50, v50, v56
	v_mul_f32_e32 v51, v51, v56
	v_mul_f32_e32 v18, v18, v56
	v_mul_f32_e32 v19, v19, v56
	v_mul_f32_e32 v20, v20, v56
	v_mul_f32_e32 v21, v21, v56
	v_mul_f32_e32 v24, v24, v56
	v_mul_f32_e32 v25, v25, v56
	v_mul_f32_e32 v26, v26, v56
	v_mul_f32_e32 v27, v27, v56
	v_mul_f32_e32 v28, v28, v56
	v_mul_f32_e32 v29, v29, v56
	v_mul_f32_e32 v30, v30, v56
	v_mul_f32_e32 v31, v31, v56
	v_mul_f32_e32 v32, v32, v56
	v_mul_f32_e32 v33, v33, v56
	v_cvt_pk_bf16_f32 v56, v64, v65
	v_cvt_pk_bf16_f32 v65, v42, v43
	v_cvt_pk_bf16_f32 v42, v44, v45
	v_cvt_pk_bf16_f32 v44, v48, v49
	v_cvt_pk_bf16_f32 v48, v22, v23
	v_lshl_add_u64 v[22:23], v[58:59], 0, s[86:87]
	v_cvt_pk_bf16_f32 v43, v46, v47
	v_cvt_pk_bf16_f32 v46, v18, v19
	v_lshl_add_u64 v[18:19], v[62:63], 0, v[22:23]
	v_cvt_pk_bf16_f32 v47, v20, v21
	global_load_dwordx4 v[18:21], v[18:19], off
	v_ashrrev_i32_e32 v61, 2, v148
	s_movk_i32 s4, 0x90
	v_mul_u32_u24_e32 v1, 0x90, v169
	v_and_b32_e32 v61, -8, v61
	v_cvt_pk_bf16_f32 v49, v24, v25
	v_mul_lo_u32 v24, v60, s4
	s_mov_b64 s[4:5], 0xc00
	v_cvt_pk_bf16_f32 v57, v66, v67
	v_cvt_pk_bf16_f32 v64, v68, v69
	v_cvt_pk_bf16_f32 v26, v26, v27
	v_cvt_pk_bf16_f32 v27, v28, v29
	v_add3_u32 v1, s49, v1, v61
	v_add3_u32 v60, s49, v34, v24
	v_lshl_add_u64 v[24:25], v[58:59], 0, s[4:5]
	v_cvt_pk_bf16_f32 v45, v50, v51
	v_cvt_pk_bf16_f32 v28, v30, v31
	v_cvt_pk_bf16_f32 v29, v32, v33
	ds_write2_b64 v1, v[56:57], v[64:65] offset1:2
	ds_write2_b64 v1, v[42:43], v[44:45] offset0:4 offset1:6
	ds_write2_b64 v1, v[46:47], v[48:49] offset0:8 offset1:10
	ds_write2_b64 v1, v[26:27], v[28:29] offset0:12 offset1:14
	v_lshl_add_u64 v[26:27], v[62:63], 0, v[24:25]
	global_load_dwordx4 v[26:29], v[26:27], off
	s_waitcnt lgkmcnt(0)
	ds_read_b128 v[30:33], v60
	ds_read_b128 v[42:45], v60 offset:1152
	s_add_u32 s4, s21, s20
	s_addc_u32 s5, 0, s28
	s_lshl_b64 s[4:5], s[4:5], 7
	s_waitcnt lgkmcnt(1)
	v_lshlrev_b32_e32 v46, 16, v30
	v_and_b32_e32 v47, 0xffff0000, v30
	v_lshlrev_b32_e32 v30, 16, v31
	v_and_b32_e32 v31, 0xffff0000, v31
	s_add_u32 s20, s80, s4
	s_addc_u32 s21, s81, s5
	v_lshl_add_u64 v[40:41], s[20:21], 0, v[40:41]
	v_lshl_add_u64 v[40:41], v[40:41], 0, v[34:35]
	v_lshl_add_u64 v[22:23], s[20:21], 0, v[22:23]
	v_lshl_add_u64 v[22:23], v[22:23], 0, v[34:35]
	s_waitcnt vmcnt(3)
; #define LAS __attribute__((address_space(3)))
; __device__ __forceinline__ unsigned cvtpk(float lo, float hi) { f32x2_t v = {lo, hi}; bf16x2_t b = __builtin_convertvector(v, bf16x2_t); return __builtin_bit_cast(unsigned, b); }
; template <class RowPtr, class GatePtr>
; __device__ __forceinline__ void store_o(const f32x16 (&o)[2], float scale, LAS unsigned char* lds, int wid, int lane, const RowPtr& rowp, const GatePtr& gatep, bool has_gate) {
;     ...
; #pragma unroll
;     for (int i = 0; i < 4; ++i) {
;         const int row = i * 8 + (lane >> 3), ch = lane & 7;
;         u32x4 v = *(const LAS u32x4*)(stg + row * OST_PITCH + ch * 16);
;         if (has_gate) {
; #pragma unroll
;             for (int k = 0; k < 4; ++k) {
;                 const float a0 = __uint_as_float(v[k] << 16) * __uint_as_float(gv[i][k] << 16), a1 = __uint_as_float(v[k] & 0xffff0000u) * __uint_as_float(gv[i][k] & 0xffff0000u);
;                 v[k] = cvtpk(a0, a1);
;             }
;         }
;         *(u32x4*)(rowp(row) + ch * 8) = v;
;     }
	v_lshlrev_b32_e32 v48, 16, v52
	v_and_b32_e32 v49, 0xffff0000, v52
	v_lshlrev_b32_e32 v50, 16, v53
	v_and_b32_e32 v51, 0xffff0000, v53
	v_mul_f32_e32 v46, v48, v46
	v_mul_f32_e32 v47, v49, v47
	v_mul_f32_e32 v48, v50, v30
	v_mul_f32_e32 v49, v51, v31
	v_cvt_pk_bf16_f32 v30, v46, v47
	v_cvt_pk_bf16_f32 v31, v48, v49
	v_lshlrev_b32_e32 v46, 16, v32
	v_and_b32_e32 v47, 0xffff0000, v32
	v_lshlrev_b32_e32 v48, 16, v54
	v_and_b32_e32 v49, 0xffff0000, v54
	v_mul_f32_e32 v46, v48, v46
	v_mul_f32_e32 v47, v49, v47
	v_lshlrev_b32_e32 v48, 16, v55
	v_cvt_pk_bf16_f32 v32, v46, v47
	v_lshlrev_b32_e32 v46, 16, v33
	v_and_b32_e32 v47, 0xffff0000, v33
	v_and_b32_e32 v49, 0xffff0000, v55
	v_mul_f32_e32 v46, v48, v46
	v_mul_f32_e32 v47, v49, v47
	s_nop 0
	v_cvt_pk_bf16_f32 v33, v46, v47
	v_lshl_add_u64 v[46:47], s[20:21], 0, v[58:59]
	v_lshl_add_u64 v[46:47], v[46:47], 0, v[34:35]
	global_store_dwordx4 v[46:47], v[30:33], off
	s_waitcnt lgkmcnt(0)
	s_nop 0
	v_lshlrev_b32_e32 v30, 16, v42
	v_and_b32_e32 v31, 0xffff0000, v42
	s_waitcnt vmcnt(3)
	v_lshlrev_b32_e32 v32, 16, v36
	v_and_b32_e32 v33, 0xffff0000, v36
	v_mul_f32_e32 v30, v32, v30
	v_mul_f32_e32 v31, v33, v31
	v_lshlrev_b32_e32 v32, 16, v43
	v_and_b32_e32 v33, 0xffff0000, v43
	v_lshlrev_b32_e32 v36, 16, v37
	v_and_b32_e32 v37, 0xffff0000, v37
	v_mul_f32_e32 v32, v36, v32
	v_mul_f32_e32 v33, v37, v33
	v_cvt_pk_bf16_f32 v30, v30, v31
	v_cvt_pk_bf16_f32 v31, v32, v33
	v_lshlrev_b32_e32 v32, 16, v44
	v_and_b32_e32 v33, 0xffff0000, v44
	v_lshlrev_b32_e32 v36, 16, v38
	v_and_b32_e32 v37, 0xffff0000, v38
	v_mul_f32_e32 v32, v36, v32
	v_mul_f32_e32 v33, v37, v33
	v_lshlrev_b32_e32 v36, 16, v45
	v_and_b32_e32 v37, 0xffff0000, v45
	v_lshlrev_b32_e32 v38, 16, v39
	v_and_b32_e32 v39, 0xffff0000, v39
	v_mul_f32_e32 v36, v38, v36
	v_mul_f32_e32 v37, v39, v37
	v_cvt_pk_bf16_f32 v32, v32, v33
	v_cvt_pk_bf16_f32 v33, v36, v37
	ds_read_b128 v[36:39], v60 offset:2304
	global_store_dwordx4 v[40:41], v[30:33], off
	ds_read_b128 v[30:33], v60 offset:3456
	s_waitcnt vmcnt(3)
	v_lshlrev_b32_e32 v42, 16, v18
	v_and_b32_e32 v43, 0xffff0000, v18
	s_waitcnt lgkmcnt(1)
	v_lshlrev_b32_e32 v40, 16, v36
	v_and_b32_e32 v41, 0xffff0000, v36
	v_mul_f32_e32 v40, v42, v40
	v_mul_f32_e32 v41, v43, v41
	v_lshlrev_b32_e32 v36, 16, v37
	v_cvt_pk_bf16_f32 v18, v40, v41
	v_and_b32_e32 v37, 0xffff0000, v37
	v_lshlrev_b32_e32 v40, 16, v19
	v_and_b32_e32 v41, 0xffff0000, v19
	v_mul_f32_e32 v36, v40, v36
	v_mul_f32_e32 v37, v41, v37
	v_lshlrev_b32_e32 v40, 16, v20
	v_cvt_pk_bf16_f32 v19, v36, v37
	v_lshlrev_b32_e32 v36, 16, v38
	v_and_b32_e32 v37, 0xffff0000, v38
	v_and_b32_e32 v41, 0xffff0000, v20
	v_mul_f32_e32 v36, v40, v36
	v_mul_f32_e32 v37, v41, v37
	v_lshlrev_b32_e32 v38, 16, v21
	v_cvt_pk_bf16_f32 v20, v36, v37
	v_lshlrev_b32_e32 v36, 16, v39
	v_and_b32_e32 v37, 0xffff0000, v39
	v_and_b32_e32 v39, 0xffff0000, v21
	v_mul_f32_e32 v36, v38, v36
	v_mul_f32_e32 v37, v39, v37
	s_nop 0
	v_cvt_pk_bf16_f32 v21, v36, v37
	global_store_dwordx4 v[22:23], v[18:21], off
	s_waitcnt vmcnt(3)
	v_lshlrev_b32_e32 v22, 16, v27
	v_and_b32_e32 v23, 0xffff0000, v27
	s_waitcnt lgkmcnt(0)
	v_lshlrev_b32_e32 v18, 16, v30
	v_and_b32_e32 v19, 0xffff0000, v30
	v_lshlrev_b32_e32 v20, 16, v26
	v_and_b32_e32 v21, 0xffff0000, v26
	v_mul_f32_e32 v18, v20, v18
	v_mul_f32_e32 v19, v21, v19
	v_lshlrev_b32_e32 v20, 16, v31
	v_and_b32_e32 v21, 0xffff0000, v31
	v_mul_f32_e32 v20, v22, v20
	v_mul_f32_e32 v21, v23, v21
	v_cvt_pk_bf16_f32 v18, v18, v19
	v_cvt_pk_bf16_f32 v19, v20, v21
	v_lshlrev_b32_e32 v20, 16, v32
	v_and_b32_e32 v21, 0xffff0000, v32
	v_lshlrev_b32_e32 v22, 16, v28
	v_and_b32_e32 v23, 0xffff0000, v28
	v_mul_f32_e32 v20, v22, v20
	v_mul_f32_e32 v21, v23, v21
	v_lshlrev_b32_e32 v22, 16, v33
	v_and_b32_e32 v23, 0xffff0000, v33
	v_lshlrev_b32_e32 v26, 16, v29
	v_and_b32_e32 v27, 0xffff0000, v29
	v_mul_f32_e32 v22, v26, v22
	v_mul_f32_e32 v23, v27, v23
	v_cvt_pk_bf16_f32 v20, v20, v21
	v_cvt_pk_bf16_f32 v21, v22, v23
	v_lshl_add_u64 v[22:23], s[20:21], 0, v[24:25]
	v_lshl_add_u64 v[22:23], v[22:23], 0, v[34:35]
	global_store_dwordx4 v[22:23], v[18:21], off
	s_waitcnt lgkmcnt(0)
	s_branch .LBB0_414

; __device__ __forceinline__ void at_dil(const Args& a, LAS unsigned char* lds, int layer) {
;     ...
;     { const int l64 = tid & 63;
;       float g2 = fabsf(a.in[I_QGD][layer * 64 + l64]), g3 = fabsf(a.in[I_KGD][layer * 64 + l64]);
;       float rbm = 0.f;
;       for (int i = l64; i < 32 * 6; i += 64) rbm = fmaxf(rbm, a.in[I_RELB][i]);
; #pragma unroll
;       for (int o2 = 1; o2 < 64; o2 <<= 1) { g2 = fmaxf(g2, __shfl_xor(g2, o2)); g3 = fmaxf(g3, __shfl_xor(g3, o2)); rbm = fmaxf(rbm, __shfl_xor(rbm, o2)); }
;       bdil = 8.f * g2 * g3 * LOG2E * 1.01f; bmax = fmaxf(rbm, 0.f) * LOG2E; }
;     const bool dil_fixed = (bdil + bmax) < 40.f;
;     const float m_dil = bdil + bmax;
.LBB0_544:
	s_andn2_b64 vcc, exec, s[6:7]
	s_cbranch_vccnz .LBB0_601
	v_mul_f32_e32 v3, 0x41000000, v3
	v_mul_f32_e32 v3, v6, v3
	s_ashr_i32 s41, s20, 7
	v_mul_f32_e32 v3, 0x3fb8aa3b, v3
	s_mov_b32 s6, 0x3fb8aa3b
	s_add_i32 s42, s41, 2
	s_mul_i32 s16, s22, 0x1200
	s_add_i32 s47, s41, 1
	v_mul_f32_e32 v4, 0x3f8147ae, v3
	s_mov_b32 s7, 0x3f8147ae
	s_add_i32 s45, s16, 0
	s_lshl_b32 s16, s42, 13
	s_lshl_b32 s17, s47, 13
	v_fma_f32 v132, v2, s6, v4
	v_fma_f32 v133, v3, s7, v4
	s_add_i32 s46, s16, 0
	s_not_b32 s16, s41
	s_add_i32 s48, s17, 0
	s_lshl_b32 s17, s41, 13
	s_lshl_b32 s39, s22, 3
	v_subrev_u32_e32 v133, 64, v18
	s_movk_i32 s10, 0x81
	s_add_i32 s44, 0, 0x21600
	s_add_i32 s49, s17, 0
	s_lshl_b32 s17, s42, 8
	s_lshl_b32 s16, s16, 8
	s_lshl_b32 s8, s22, 4
	s_and_b32 s14, s39, 0xffffffe0
	v_cmp_gt_u32_e64 s[10:11], s10, v133
	s_sub_i32 s73, s44, s17
	s_add_i32 s75, s44, s16
	s_lshl_b32 s16, s22, 7
	s_lshl_b32 s17, s41, 8
	s_mov_b32 s6, 0x42200000
	s_and_b32 s38, s8, 48
	s_ashr_i32 s15, s14, 31
	v_xor_b32_e32 v2, 0x80000000, v132
	s_movk_i32 s8, 0x100
	v_writelane_b32 v254, s10, 22
	s_sub_i32 s16, s16, s17
	s_add_i32 s2, s21, 1
	v_cmp_ngt_f32_e64 s[6:7], s6, v132
	s_lshl_b32 s40, s22, 10
	s_lshl_b32 s43, s22, 5
	v_mov_b32_e32 v3, v2
	v_mov_b32_e32 v4, v2
	v_mov_b32_e32 v5, v2
	v_mov_b32_e32 v6, v2
	v_mov_b32_e32 v7, v2
	v_mov_b32_e32 v8, v2
	v_mov_b32_e32 v9, v2
	v_mov_b32_e32 v10, v2
	v_mov_b32_e32 v11, v2
	v_mov_b32_e32 v12, v2
	v_mov_b32_e32 v13, v2
	v_mov_b32_e32 v14, v2
	v_mov_b32_e32 v15, v2
	v_mov_b32_e32 v16, v2
	v_mov_b32_e32 v17, v2
	v_cmp_gt_i32_e64 s[8:9], s8, v18
	v_writelane_b32 v254, s11, 23
	v_lshl_add_u32 v134, v18, 2, s44
	s_add_i32 s45, s45, 0x18000
	s_add_i32 s68, s46, 0xc000
	s_add_i32 s69, s48, 0xc000
	s_add_i32 s72, s49, 0xc000
	s_lshl_b32 s36, s41, 6
	s_add_i32 s37, s16, 0
	s_mov_b64 s[16:17], 0
	s_lshl_b64 s[14:15], s[14:15], 1
	s_branch .LBB0_547

; #define LAS __attribute__((address_space(3)))
; __device__ __forceinline__ int crow(int r, int hi) { return (r & 3) + 8 * (r >> 2) + 4 * hi; }
; __device__ __forceinline__ unsigned cvtpk(float lo, float hi) { f32x2_t v = {lo, hi}; bf16x2_t b = __builtin_convertvector(v, bf16x2_t); return __builtin_bit_cast(unsigned, b); }
; __device__ __forceinline__ void at_dil(const Args& a, LAS unsigned char* lds, int layer) {
;     ...
;         if (dil_fixed) {
; #pragma unroll
;             for (int j = 0; j < 3; ++j) {
;                 const int tt = twlo + 2 - j;
;                 if (tt >= tt_lo) {
;                     f32x16 p0, p1;
;                     qkt(p0, p1, lds + L_K + tt * 8192, qr, -m_dil, r32, hi);
;                     const LAS float* tb = tab + (32 * wid + r32 + 192 - 64 * tt - 4 * hi - 63);
; #pragma unroll
;                     for (int r = 0; r < 16; ++r) { p0[r] += tb[63 - crow(r, 0)]; p1[r] += tb[31 - crow(r, 0)]; }
;                     exp_sum(p0, p1, l_part);
;                     pw[j][0] = (u32x4){cvtpk(p0[0], p0[1]), cvtpk(p0[2], p0[3]), cvtpk(p0[4], p0[5]), cvtpk(p0[6], p0[7])};
;                     pw[j][1] = (u32x4){cvtpk(p0[8], p0[9]), cvtpk(p0[10], p0[11]), cvtpk(p0[12], p0[13]), cvtpk(p0[14], p0[15])};
;                     pw[j][2] = (u32x4){cvtpk(p1[0], p1[1]), cvtpk(p1[2], p1[3]), cvtpk(p1[4], p1[5]), cvtpk(p1[6], p1[7])};
;                     pw[j][3] = (u32x4){cvtpk(p1[8], p1[9]), cvtpk(p1[10], p1[11]), cvtpk(p1[12], p1[13]), cvtpk(p1[14], p1[15])};
;                 }
;             }
.LBB0_563:
	v_mov_b32_e32 v138, 0
	s_cmp_lt_i32 s42, s54
	v_lshlrev_b32_e32 v52, 2, v139
	s_cbranch_scc1 .LBB0_572
	s_nop 4
	v_add_u32_e32 v18, s46, v143
	v_add_u32_e32 v19, v144, v18
	ds_read_b128 v[36:39], v19
	ds_read_b128 v[54:57], v19 offset:4096
	v_add_u32_e32 v19, v142, v18
	ds_read_b128 v[58:61], v19
	ds_read_b128 v[62:65], v19 offset:4096
	v_add_u32_e32 v19, v141, v18
	v_add_u32_e32 v18, v140, v18
	ds_read_b128 v[88:91], v19
	ds_read_b128 v[96:99], v19 offset:4096
	ds_read_b128 v[104:107], v18
	ds_read_b128 v[112:115], v18 offset:4096
	s_waitcnt lgkmcnt(7)
	v_mfma_f32_32x32x16_bf16 v[18:33], v[36:39], v[68:71], v[2:17]
	v_add_lshl_u32 v53, v136, s43, 2
	v_add3_u32 v53, s73, v52, v53
	s_waitcnt lgkmcnt(6)
	v_mfma_f32_32x32x16_bf16 v[36:51], v[54:57], v[68:71], v[2:17]
	ds_read2_b32 v[54:55], v53 offset0:191 offset1:192
	ds_read2_b32 v[56:57], v53 offset0:189 offset1:190
	s_waitcnt lgkmcnt(7)
	v_mfma_f32_32x32x16_bf16 v[18:33], v[58:61], v[72:75], v[18:33]
	ds_read2_b32 v[58:59], v53 offset0:159 offset1:160
	ds_read2_b32 v[60:61], v53 offset0:157 offset1:158
	s_waitcnt lgkmcnt(8)
	v_mfma_f32_32x32x16_bf16 v[36:51], v[62:65], v[72:75], v[36:51]
	s_waitcnt lgkmcnt(7)
	v_mfma_f32_32x32x16_bf16 v[18:33], v[88:91], v[76:79], v[18:33]
	s_waitcnt lgkmcnt(6)
	v_mfma_f32_32x32x16_bf16 v[36:51], v[96:99], v[76:79], v[36:51]
	s_waitcnt lgkmcnt(5)
	v_mfma_f32_32x32x16_bf16 v[18:33], v[104:107], v[80:83], v[18:33]
	s_waitcnt lgkmcnt(4)
	v_mfma_f32_32x32x16_bf16 v[36:51], v[112:115], v[80:83], v[36:51]
	s_waitcnt lgkmcnt(3)
	s_nop 8
	v_add_f32_e32 v55, v18, v55
	v_add_f32_e32 v54, v19, v54
	ds_read2_b32 v[18:19], v53 offset0:183 offset1:184
	s_waitcnt lgkmcnt(3)
	v_add_f32_e32 v57, v20, v57
	v_add_f32_e32 v56, v21, v56
	ds_read2_b32 v[20:21], v53 offset0:181 offset1:182
	v_exp_f32_e32 v55, v55
	s_waitcnt lgkmcnt(3)
	v_add_f32_e32 v59, v36, v59
	v_add_f32_e32 v58, v37, v58
	ds_read2_b32 v[36:37], v53 offset0:151 offset1:152
	s_waitcnt lgkmcnt(3)
	v_add_f32_e32 v61, v38, v61
	v_add_f32_e32 v60, v39, v60
	ds_read2_b32 v[38:39], v53 offset0:149 offset1:150
	s_waitcnt lgkmcnt(3)
	v_add_f32_e32 v62, v22, v19
	s_waitcnt lgkmcnt(1)
	v_add_f32_e32 v37, v40, v37
	v_add_f32_e32 v40, v23, v18
	v_add_f32_e32 v36, v41, v36
	v_add_f32_e32 v41, v24, v21
	s_waitcnt lgkmcnt(0)
	v_add_f32_e32 v39, v42, v39
	ds_read2_b32 v[18:19], v53 offset0:175 offset1:176
	ds_read2_b32 v[22:23], v53 offset0:173 offset1:174
	v_add_f32_e32 v42, v25, v20
	ds_read2_b32 v[20:21], v53 offset0:143 offset1:144
	ds_read2_b32 v[24:25], v53 offset0:141 offset1:142
	v_add_f32_e32 v38, v43, v38
	s_waitcnt lgkmcnt(3)
	v_add_f32_e32 v43, v26, v19
	v_add_f32_e32 v63, v27, v18
	s_waitcnt lgkmcnt(1)
	v_add_f32_e32 v44, v44, v21
	v_add_f32_e32 v45, v45, v20
	ds_read2_b32 v[18:19], v53 offset0:167 offset1:168
	ds_read2_b32 v[20:21], v53 offset0:135 offset1:136
	v_add_f32_e32 v64, v28, v23
	v_add_f32_e32 v65, v29, v22
	ds_read2_b32 v[22:23], v53 offset0:165 offset1:166
	v_exp_f32_e32 v59, v59
	s_waitcnt lgkmcnt(3)
	v_add_f32_e32 v46, v46, v25
	v_add_f32_e32 v47, v47, v24
	s_waitcnt lgkmcnt(2)
	v_add_f32_e32 v66, v30, v19
	ds_read2_b32 v[24:25], v53 offset0:133 offset1:134
	s_waitcnt lgkmcnt(2)
	v_add_f32_e32 v48, v48, v21
	v_exp_f32_e32 v19, v54
	v_exp_f32_e32 v21, v58
	v_add_f32_e32 v53, v31, v18
	v_add_f32_e32 v49, v49, v20
	v_add_f32_e32 v18, v55, v59
	v_mov_b32_e32 v20, v35
	s_waitcnt lgkmcnt(1)
	v_add_f32_e32 v67, v32, v23
	v_add_f32_e32 v88, v33, v22
	v_exp_f32_e32 v54, v57
	v_exp_f32_e32 v57, v61
	v_add_f32_e32 v22, v18, v20
	v_add_f32_e32 v23, v19, v21
	v_exp_f32_e32 v18, v56
	s_waitcnt lgkmcnt(0)
	v_add_f32_e32 v50, v50, v25
	v_exp_f32_e32 v25, v60
	v_pk_add_f32 v[22:23], v[22:23], v[22:23] op_sel:[0,1] op_sel_hi:[1,0]
	v_add_f32_e32 v51, v51, v24
	v_add_f32_e32 v24, v54, v57
	v_mov_b32_e32 v23, v18
	v_exp_f32_e32 v20, v62
	v_exp_f32_e32 v56, v37
	v_add_f32_e32 v22, v22, v24
	v_add_f32_e32 v23, v23, v25
	v_exp_f32_e32 v24, v40
	v_exp_f32_e32 v27, v36
	v_pk_add_f32 v[22:23], v[22:23], v[22:23] op_sel:[0,1] op_sel_hi:[1,0]
	v_add_f32_e32 v26, v20, v56
	v_mov_b32_e32 v23, v24
	v_exp_f32_e32 v40, v41
	v_exp_f32_e32 v41, v39
	v_add_f32_e32 v22, v22, v26
	v_add_f32_e32 v23, v23, v27
	v_exp_f32_e32 v26, v42
	v_exp_f32_e32 v29, v38
	v_pk_add_f32 v[22:23], v[22:23], v[22:23] op_sel:[0,1] op_sel_hi:[1,0]
	v_add_f32_e32 v28, v40, v41
	v_mov_b32_e32 v23, v26
	v_exp_f32_e32 v42, v43
	v_exp_f32_e32 v43, v44
	v_add_f32_e32 v22, v22, v28
	v_add_f32_e32 v23, v23, v29
	v_exp_f32_e32 v28, v63
	v_exp_f32_e32 v31, v45
	v_pk_add_f32 v[22:23], v[22:23], v[22:23] op_sel:[0,1] op_sel_hi:[1,0]
	v_add_f32_e32 v30, v42, v43
	v_mov_b32_e32 v23, v28
	v_exp_f32_e32 v44, v64
	v_exp_f32_e32 v45, v46
	v_add_f32_e32 v22, v22, v30
	v_add_f32_e32 v23, v23, v31
	v_exp_f32_e32 v30, v65
	v_exp_f32_e32 v33, v47
	v_pk_add_f32 v[22:23], v[22:23], v[22:23] op_sel:[0,1] op_sel_hi:[1,0]
	v_add_f32_e32 v32, v44, v45
	v_mov_b32_e32 v23, v30
	v_exp_f32_e32 v46, v66
	v_exp_f32_e32 v47, v48
	v_add_f32_e32 v22, v22, v32
	v_add_f32_e32 v23, v23, v33
	v_exp_f32_e32 v32, v53
	v_exp_f32_e32 v37, v49
	v_pk_add_f32 v[22:23], v[22:23], v[22:23] op_sel:[0,1] op_sel_hi:[1,0]
	v_add_f32_e32 v36, v46, v47
	v_mov_b32_e32 v23, v32
	v_exp_f32_e32 v48, v67
	v_exp_f32_e32 v49, v50
	v_add_f32_e32 v22, v22, v36
	v_add_f32_e32 v23, v23, v37
	v_exp_f32_e32 v36, v88
	v_exp_f32_e32 v39, v51
	v_pk_add_f32 v[22:23], v[22:23], v[22:23] op_sel:[0,1] op_sel_hi:[1,0]
	v_add_f32_e32 v38, v48, v49
	v_mov_b32_e32 v23, v36
	v_add_f32_e32 v22, v22, v38
	v_add_f32_e32 v23, v23, v39
	v_cvt_pk_bf16_f32 v88, v55, v19
	v_add_f32_e32 v22, v22, v23
	v_add_f32_e32 v138, 0, v22
	v_cvt_pk_bf16_f32 v89, v54, v18
	v_cvt_pk_bf16_f32 v90, v20, v24
	v_cvt_pk_bf16_f32 v91, v40, v26
	v_cvt_pk_bf16_f32 v96, v42, v28
	v_cvt_pk_bf16_f32 v97, v44, v30
	v_cvt_pk_bf16_f32 v98, v46, v32
	v_cvt_pk_bf16_f32 v99, v48, v36
	v_cvt_pk_bf16_f32 v104, v59, v21
	v_cvt_pk_bf16_f32 v105, v57, v25
	v_cvt_pk_bf16_f32 v106, v56, v27
	v_cvt_pk_bf16_f32 v107, v41, v29
	v_cvt_pk_bf16_f32 v112, v43, v31
	v_cvt_pk_bf16_f32 v113, v45, v33
	v_cvt_pk_bf16_f32 v114, v47, v37
	v_cvt_pk_bf16_f32 v115, v49, v39
	s_cmp_lt_i32 s47, s54
	s_cbranch_scc1 .LBB0_574
	s_branch .LBB0_573
; #define LAS __attribute__((address_space(3)))
; __device__ __forceinline__ int crow(int r, int hi) { return (r & 3) + 8 * (r >> 2) + 4 * hi; }
; __device__ __forceinline__ unsigned cvtpk(float lo, float hi) { f32x2_t v = {lo, hi}; bf16x2_t b = __builtin_convertvector(v, bf16x2_t); return __builtin_bit_cast(unsigned, b); }
; __device__ __forceinline__ void at_dil(const Args& a, LAS unsigned char* lds, int layer) {
;     ...
;             mt = other_half_max(mt);
;             m_run = mt;
; #pragma unroll
;             for (int j = 0; j < 3; ++j) {
;                 const int tt = twlo + 2 - j;
;                 if (tt >= tt_lo) {
;                     f32x16 p0, p1;
;                     qkt(p0, p1, lds + L_K + tt * 8192, qr, -mt, r32, hi);
;                     const LAS float* tb = tab + (32 * wid + r32 + 192 - 64 * tt - 4 * hi - 63);
; #pragma unroll
;                     for (int r = 0; r < 16; ++r) { p0[r] += tb[63 - crow(r, 0)]; p1[r] += tb[31 - crow(r, 0)]; }
;                     exp_sum(p0, p1, l_part);
;                     pw[j][0] = (u32x4){cvtpk(p0[0], p0[1]), cvtpk(p0[2], p0[3]), cvtpk(p0[4], p0[5]), cvtpk(p0[6], p0[7])};
;                     pw[j][1] = (u32x4){cvtpk(p0[8], p0[9]), cvtpk(p0[10], p0[11]), cvtpk(p0[12], p0[13]), cvtpk(p0[14], p0[15])};
;                     pw[j][2] = (u32x4){cvtpk(p1[0], p1[1]), cvtpk(p1[2], p1[3]), cvtpk(p1[4], p1[5]), cvtpk(p1[6], p1[7])};
;                     pw[j][3] = (u32x4){cvtpk(p1[8], p1[9]), cvtpk(p1[10], p1[11]), cvtpk(p1[12], p1[13]), cvtpk(p1[14], p1[15])};
.LBB0_565:
	v_mov_b32_e32 v18, v58
	s_nop 1
	v_permlane32_swap_b32_e32 v58, v18
	v_max_f32_e32 v18, v18, v18
	v_max_f32_e32 v19, v58, v58
	v_max_f32_e32 v137, v19, v18
	v_xor_b32_e32 v18, 0x80000000, v137
	v_mov_b32_e32 v19, v18
	v_mov_b32_e32 v20, v18
	v_mov_b32_e32 v21, v18
	v_mov_b32_e32 v22, v18
	v_mov_b32_e32 v23, v18
	v_mov_b32_e32 v24, v18
	v_mov_b32_e32 v25, v18
	v_mov_b32_e32 v26, v18
	v_mov_b32_e32 v27, v18
	v_mov_b32_e32 v28, v18
	v_mov_b32_e32 v29, v18
	v_mov_b32_e32 v30, v18
	v_mov_b32_e32 v31, v18
	v_mov_b32_e32 v32, v18
	v_mov_b32_e32 v33, v18
	s_cmp_ge_i32 s42, s54
	v_mov_b32_e32 v138, 0
	s_cbranch_scc0 .LBB0_589
	v_add_u32_e32 v36, s46, v143
	v_add_u32_e32 v37, v144, v36
	ds_read_b128 v[52:55], v37
	ds_read_b128 v[88:91], v37 offset:4096
	v_add_u32_e32 v37, v142, v36
	ds_read_b128 v[96:99], v37
	ds_read_b128 v[104:107], v37 offset:4096
	v_add_u32_e32 v37, v141, v36
	v_add_u32_e32 v36, v140, v36
	ds_read_b128 v[112:115], v37
	ds_read_b128 v[146:149], v37 offset:4096
	ds_read_b128 v[150:153], v36
	ds_read_b128 v[154:157], v36 offset:4096
	s_waitcnt lgkmcnt(7)
	v_mfma_f32_32x32x16_bf16 v[36:51], v[52:55], v[68:71], v[18:33]
	s_waitcnt lgkmcnt(6)
	v_mfma_f32_32x32x16_bf16 v[52:67], v[88:91], v[68:71], v[18:33]
	v_lshlrev_b32_e32 v88, 2, v139
	v_add_lshl_u32 v89, v136, s43, 2
	s_waitcnt lgkmcnt(5)
	v_mfma_f32_32x32x16_bf16 v[36:51], v[96:99], v[72:75], v[36:51]
	s_waitcnt lgkmcnt(4)
	v_mfma_f32_32x32x16_bf16 v[52:67], v[104:107], v[72:75], v[52:67]
	v_add3_u32 v104, s73, v88, v89
	ds_read2_b32 v[88:89], v104 offset0:191 offset1:192
	ds_read2_b32 v[90:91], v104 offset0:189 offset1:190
	ds_read2_b32 v[96:97], v104 offset0:159 offset1:160
	ds_read2_b32 v[98:99], v104 offset0:157 offset1:158
	s_waitcnt lgkmcnt(7)
	v_mfma_f32_32x32x16_bf16 v[36:51], v[112:115], v[76:79], v[36:51]
	s_waitcnt lgkmcnt(6)
	v_mfma_f32_32x32x16_bf16 v[52:67], v[146:149], v[76:79], v[52:67]
	s_waitcnt lgkmcnt(5)
	v_mfma_f32_32x32x16_bf16 v[36:51], v[150:153], v[80:83], v[36:51]
	s_waitcnt lgkmcnt(4)
	v_mfma_f32_32x32x16_bf16 v[52:67], v[154:157], v[80:83], v[52:67]
	s_waitcnt lgkmcnt(3)
	s_nop 8
	v_add_f32_e32 v89, v36, v89
	v_add_f32_e32 v88, v37, v88
	ds_read2_b32 v[36:37], v104 offset0:183 offset1:184
	s_waitcnt lgkmcnt(3)
	v_add_f32_e32 v91, v38, v91
	v_add_f32_e32 v90, v39, v90
	ds_read2_b32 v[38:39], v104 offset0:181 offset1:182
	v_exp_f32_e32 v89, v89
	s_waitcnt lgkmcnt(3)
	v_add_f32_e32 v97, v52, v97
	v_add_f32_e32 v96, v53, v96
	ds_read2_b32 v[52:53], v104 offset0:151 offset1:152
	s_waitcnt lgkmcnt(3)
	v_add_f32_e32 v99, v54, v99
	v_add_f32_e32 v98, v55, v98
	ds_read2_b32 v[54:55], v104 offset0:149 offset1:150
	s_waitcnt lgkmcnt(3)
	v_add_f32_e32 v105, v40, v37
	s_waitcnt lgkmcnt(1)
	v_add_f32_e32 v53, v56, v53
	v_add_f32_e32 v56, v41, v36
	v_add_f32_e32 v52, v57, v52
	v_add_f32_e32 v57, v42, v39
	s_waitcnt lgkmcnt(0)
	v_add_f32_e32 v55, v58, v55
	ds_read2_b32 v[36:37], v104 offset0:175 offset1:176
	ds_read2_b32 v[40:41], v104 offset0:173 offset1:174
	v_add_f32_e32 v58, v43, v38
	ds_read2_b32 v[38:39], v104 offset0:143 offset1:144
	ds_read2_b32 v[42:43], v104 offset0:141 offset1:142
	v_add_f32_e32 v54, v59, v54
	s_waitcnt lgkmcnt(3)
	v_add_f32_e32 v59, v44, v37
	v_add_f32_e32 v106, v45, v36
	s_waitcnt lgkmcnt(1)
	v_add_f32_e32 v60, v60, v39
	v_add_f32_e32 v61, v61, v38
	ds_read2_b32 v[36:37], v104 offset0:167 offset1:168
	ds_read2_b32 v[38:39], v104 offset0:135 offset1:136
	v_add_f32_e32 v107, v46, v41
	v_add_f32_e32 v112, v47, v40
	ds_read2_b32 v[40:41], v104 offset0:165 offset1:166
	v_exp_f32_e32 v145, v97
	s_waitcnt lgkmcnt(3)
	v_add_f32_e32 v62, v62, v43
	v_add_f32_e32 v63, v63, v42
	s_waitcnt lgkmcnt(2)
	v_add_f32_e32 v113, v48, v37
	ds_read2_b32 v[42:43], v104 offset0:133 offset1:134
	s_waitcnt lgkmcnt(2)
	v_add_f32_e32 v64, v64, v39
	v_exp_f32_e32 v37, v88
	v_exp_f32_e32 v39, v96
	v_add_f32_e32 v104, v49, v36
	v_add_f32_e32 v65, v65, v38
	v_add_f32_e32 v36, v89, v145
	v_mov_b32_e32 v38, v35
	s_waitcnt lgkmcnt(1)
	v_add_f32_e32 v114, v50, v41
	v_add_f32_e32 v115, v51, v40
	v_exp_f32_e32 v91, v91
	v_exp_f32_e32 v146, v99
	v_add_f32_e32 v40, v36, v38
	v_add_f32_e32 v41, v37, v39
	v_exp_f32_e32 v36, v90
	s_waitcnt lgkmcnt(0)
	v_add_f32_e32 v66, v66, v43
	v_exp_f32_e32 v43, v98
	v_pk_add_f32 v[40:41], v[40:41], v[40:41] op_sel:[0,1] op_sel_hi:[1,0]
	v_add_f32_e32 v67, v67, v42
	v_add_f32_e32 v42, v91, v146
	v_mov_b32_e32 v41, v36
	v_exp_f32_e32 v38, v105
	v_exp_f32_e32 v147, v53
	v_add_f32_e32 v40, v40, v42
	v_add_f32_e32 v41, v41, v43
	v_exp_f32_e32 v42, v56
	v_exp_f32_e32 v45, v52
	v_pk_add_f32 v[40:41], v[40:41], v[40:41] op_sel:[0,1] op_sel_hi:[1,0]
	v_add_f32_e32 v44, v38, v147
	v_mov_b32_e32 v41, v42
	v_exp_f32_e32 v56, v57
	v_exp_f32_e32 v57, v55
	v_add_f32_e32 v40, v40, v44
	v_add_f32_e32 v41, v41, v45
	v_exp_f32_e32 v44, v58
	v_exp_f32_e32 v47, v54
	v_pk_add_f32 v[40:41], v[40:41], v[40:41] op_sel:[0,1] op_sel_hi:[1,0]
	v_add_f32_e32 v46, v56, v57
	v_mov_b32_e32 v41, v44
	v_exp_f32_e32 v58, v59
	v_exp_f32_e32 v59, v60
	v_add_f32_e32 v40, v40, v46
	v_add_f32_e32 v41, v41, v47
	v_exp_f32_e32 v46, v106
	v_exp_f32_e32 v49, v61
	v_pk_add_f32 v[40:41], v[40:41], v[40:41] op_sel:[0,1] op_sel_hi:[1,0]
	v_add_f32_e32 v48, v58, v59
	v_mov_b32_e32 v41, v46
	v_exp_f32_e32 v60, v107
	v_exp_f32_e32 v61, v62
	v_add_f32_e32 v40, v40, v48
	v_add_f32_e32 v41, v41, v49
	v_exp_f32_e32 v48, v112
	v_exp_f32_e32 v51, v63
	v_pk_add_f32 v[40:41], v[40:41], v[40:41] op_sel:[0,1] op_sel_hi:[1,0]
	v_add_f32_e32 v50, v60, v61
	v_mov_b32_e32 v41, v48
	v_exp_f32_e32 v62, v113
	v_exp_f32_e32 v63, v64
	v_add_f32_e32 v40, v40, v50
	v_add_f32_e32 v41, v41, v51
	v_exp_f32_e32 v50, v104
	v_exp_f32_e32 v53, v65
	v_pk_add_f32 v[40:41], v[40:41], v[40:41] op_sel:[0,1] op_sel_hi:[1,0]
	v_add_f32_e32 v52, v62, v63
	v_mov_b32_e32 v41, v50
	v_exp_f32_e32 v64, v114
	v_exp_f32_e32 v65, v66
	v_add_f32_e32 v40, v40, v52
	v_add_f32_e32 v41, v41, v53
	v_exp_f32_e32 v52, v115
	v_exp_f32_e32 v55, v67
	v_pk_add_f32 v[40:41], v[40:41], v[40:41] op_sel:[0,1] op_sel_hi:[1,0]
	v_add_f32_e32 v54, v64, v65
	v_mov_b32_e32 v41, v52
	v_add_f32_e32 v40, v40, v54
	v_add_f32_e32 v41, v41, v55
	v_cvt_pk_bf16_f32 v88, v89, v37
	v_add_f32_e32 v40, v40, v41
	v_add_f32_e32 v138, 0, v40
	v_cvt_pk_bf16_f32 v89, v91, v36
	v_cvt_pk_bf16_f32 v90, v38, v42
	v_cvt_pk_bf16_f32 v91, v56, v44
	v_cvt_pk_bf16_f32 v96, v58, v46
	v_cvt_pk_bf16_f32 v97, v60, v48
	v_cvt_pk_bf16_f32 v98, v62, v50
	v_cvt_pk_bf16_f32 v99, v64, v52
	v_cvt_pk_bf16_f32 v104, v145, v39
	v_cvt_pk_bf16_f32 v105, v146, v43
	v_cvt_pk_bf16_f32 v106, v147, v45
	v_cvt_pk_bf16_f32 v107, v57, v47
	v_cvt_pk_bf16_f32 v112, v59, v49
	v_cvt_pk_bf16_f32 v113, v61, v51
	v_cvt_pk_bf16_f32 v114, v63, v53
	v_cvt_pk_bf16_f32 v115, v65, v55
	s_cmp_lt_i32 s47, s54
	s_cbranch_scc0 .LBB0_590

; #define LAS __attribute__((address_space(3)))
; __device__ __forceinline__ int crow(int r, int hi) { return (r & 3) + 8 * (r >> 2) + 4 * hi; }
; __device__ __forceinline__ unsigned cvtpk(float lo, float hi) { f32x2_t v = {lo, hi}; bf16x2_t b = __builtin_convertvector(v, bf16x2_t); return __builtin_bit_cast(unsigned, b); }
; __device__ __forceinline__ void at_dil(const Args& a, LAS unsigned char* lds, int layer) {
;     ...
;         if (dil_fixed) {
; #pragma unroll
;             for (int j = 0; j < 3; ++j) {
;                 const int tt = twlo + 2 - j;
;                 if (tt >= tt_lo) {
;                     f32x16 p0, p1;
;                     qkt(p0, p1, lds + L_K + tt * 8192, qr, -m_dil, r32, hi);
;                     const LAS float* tb = tab + (32 * wid + r32 + 192 - 64 * tt - 4 * hi - 63);
; #pragma unroll
;                     for (int r = 0; r < 16; ++r) { p0[r] += tb[63 - crow(r, 0)]; p1[r] += tb[31 - crow(r, 0)]; }
;                     exp_sum(p0, p1, l_part);
;                     pw[j][0] = (u32x4){cvtpk(p0[0], p0[1]), cvtpk(p0[2], p0[3]), cvtpk(p0[4], p0[5]), cvtpk(p0[6], p0[7])};
;                     pw[j][1] = (u32x4){cvtpk(p0[8], p0[9]), cvtpk(p0[10], p0[11]), cvtpk(p0[12], p0[13]), cvtpk(p0[14], p0[15])};
;                     pw[j][2] = (u32x4){cvtpk(p1[0], p1[1]), cvtpk(p1[2], p1[3]), cvtpk(p1[4], p1[5]), cvtpk(p1[6], p1[7])};
;                     pw[j][3] = (u32x4){cvtpk(p1[8], p1[9]), cvtpk(p1[10], p1[11]), cvtpk(p1[12], p1[13]), cvtpk(p1[14], p1[15])};
;                 }
;             }
.LBB0_571:
	v_subrev_u32_e32 v52, s36, v139
	v_lshlrev_b32_e32 v52, 2, v52
	v_add_lshl_u32 v53, v136, s43, 2
	v_add3_u32 v56, s44, v52, v53
	ds_read2_b32 v[52:53], v56 offset0:191 offset1:192
	ds_read2_b32 v[54:55], v56 offset0:159 offset1:160
	s_waitcnt lgkmcnt(1)
	v_add_f32_e32 v53, v36, v53
	v_add_f32_e32 v52, v37, v52
	ds_read2_b32 v[36:37], v56 offset0:157 offset1:158
	v_exp_f32_e32 v53, v53
	s_waitcnt lgkmcnt(0)
	v_add_f32_e32 v37, v20, v37
	v_add_f32_e32 v36, v21, v36
	ds_read2_b32 v[20:21], v56 offset0:151 offset1:152
	s_waitcnt lgkmcnt(0)
	v_add_f32_e32 v57, v22, v21
	v_add_f32_e32 v58, v23, v20
	ds_read2_b32 v[20:21], v56 offset0:149 offset1:150
	s_waitcnt lgkmcnt(0)
	v_add_f32_e32 v59, v24, v21
	v_add_f32_e32 v60, v25, v20
	ds_read2_b32 v[20:21], v56 offset0:143 offset1:144
	v_exp_f32_e32 v25, v36
	s_waitcnt lgkmcnt(0)
	v_add_f32_e32 v61, v26, v21
	v_add_f32_e32 v62, v27, v20
	ds_read2_b32 v[20:21], v56 offset0:141 offset1:142
	v_exp_f32_e32 v27, v58
	s_waitcnt lgkmcnt(0)
	v_add_f32_e32 v63, v28, v21
	v_add_f32_e32 v64, v29, v20
	ds_read2_b32 v[20:21], v56 offset0:135 offset1:136
	v_exp_f32_e32 v29, v60
	s_waitcnt lgkmcnt(0)
	v_add_f32_e32 v65, v30, v21
	v_add_f32_e32 v66, v31, v20
	ds_read2_b32 v[20:21], v56 offset0:133 offset1:134
	v_add_f32_e32 v55, v18, v55
	v_add_f32_e32 v54, v19, v54
	ds_read2_b32 v[18:19], v56 offset0:189 offset1:190
	v_exp_f32_e32 v55, v55
	s_waitcnt lgkmcnt(1)
	v_add_f32_e32 v67, v33, v20
	v_exp_f32_e32 v31, v62
	v_exp_f32_e32 v33, v64
	s_waitcnt lgkmcnt(0)
	v_add_f32_e32 v38, v38, v19
	v_add_f32_e32 v39, v39, v18
	ds_read2_b32 v[18:19], v56 offset0:183 offset1:184
	v_add_f32_e32 v20, v53, v55
	s_waitcnt lgkmcnt(0)
	v_add_f32_e32 v40, v40, v19
	v_add_f32_e32 v41, v41, v18
	ds_read2_b32 v[18:19], v56 offset0:181 offset1:182
	v_exp_f32_e32 v41, v41
	s_waitcnt lgkmcnt(0)
	v_add_f32_e32 v42, v42, v19
	v_add_f32_e32 v43, v43, v18
	ds_read2_b32 v[18:19], v56 offset0:175 offset1:176
	v_exp_f32_e32 v43, v43
	s_waitcnt lgkmcnt(0)
	v_add_f32_e32 v44, v44, v19
	v_add_f32_e32 v45, v45, v18
	ds_read2_b32 v[18:19], v56 offset0:173 offset1:174
	v_exp_f32_e32 v45, v45
	s_waitcnt lgkmcnt(0)
	v_add_f32_e32 v46, v46, v19
	v_add_f32_e32 v47, v47, v18
	ds_read2_b32 v[18:19], v56 offset0:167 offset1:168
	v_exp_f32_e32 v47, v47
	s_waitcnt lgkmcnt(0)
	v_add_f32_e32 v48, v48, v19
	v_add_f32_e32 v49, v49, v18
	ds_read2_b32 v[18:19], v56 offset0:165 offset1:166
	v_add_f32_e32 v56, v32, v21
	v_exp_f32_e32 v21, v52
	v_exp_f32_e32 v52, v39
	v_exp_f32_e32 v49, v49
	s_waitcnt lgkmcnt(0)
	v_add_f32_e32 v50, v50, v19
	v_exp_f32_e32 v19, v54
	v_add_f32_e32 v51, v51, v18
	v_mov_b32_e32 v18, v35
	v_exp_f32_e32 v51, v51
	v_add_f32_e32 v22, v20, v18
	v_add_f32_e32 v23, v21, v19
	v_exp_f32_e32 v18, v38
	v_exp_f32_e32 v20, v37
	v_pk_add_f32 v[22:23], v[22:23], v[22:23] op_sel:[0,1] op_sel_hi:[1,0]
	v_exp_f32_e32 v37, v66
	v_mov_b32_e32 v23, v52
	v_add_f32_e32 v24, v18, v20
	v_add_f32_e32 v22, v22, v24
	v_add_f32_e32 v23, v23, v25
	v_exp_f32_e32 v24, v40
	v_exp_f32_e32 v40, v57
	v_pk_add_f32 v[22:23], v[22:23], v[22:23] op_sel:[0,1] op_sel_hi:[1,0]
	v_exp_f32_e32 v39, v67
	v_mov_b32_e32 v23, v41
	v_add_f32_e32 v26, v24, v40
	v_add_f32_e32 v22, v22, v26
	v_add_f32_e32 v23, v23, v27
	v_exp_f32_e32 v26, v42
	v_exp_f32_e32 v42, v59
	v_pk_add_f32 v[22:23], v[22:23], v[22:23] op_sel:[0,1] op_sel_hi:[1,0]
	v_cvt_pk_bf16_f32 v116, v53, v21
	v_mov_b32_e32 v23, v43
	v_add_f32_e32 v28, v26, v42
	v_add_f32_e32 v22, v22, v28
	v_add_f32_e32 v23, v23, v29
	v_exp_f32_e32 v28, v44
	v_exp_f32_e32 v44, v61
	v_pk_add_f32 v[22:23], v[22:23], v[22:23] op_sel:[0,1] op_sel_hi:[1,0]
	v_cvt_pk_bf16_f32 v117, v18, v52
	v_mov_b32_e32 v23, v45
	v_add_f32_e32 v30, v28, v44
	v_add_f32_e32 v22, v22, v30
	v_add_f32_e32 v23, v23, v31
	v_exp_f32_e32 v30, v46
	v_exp_f32_e32 v46, v63
	v_pk_add_f32 v[22:23], v[22:23], v[22:23] op_sel:[0,1] op_sel_hi:[1,0]
	v_cvt_pk_bf16_f32 v118, v24, v41
	v_mov_b32_e32 v23, v47
	v_add_f32_e32 v32, v30, v46
	v_add_f32_e32 v22, v22, v32
	v_add_f32_e32 v23, v23, v33
	v_exp_f32_e32 v32, v48
	v_exp_f32_e32 v48, v65
	v_pk_add_f32 v[22:23], v[22:23], v[22:23] op_sel:[0,1] op_sel_hi:[1,0]
	v_cvt_pk_bf16_f32 v119, v26, v43
	v_mov_b32_e32 v23, v49
	v_add_f32_e32 v36, v32, v48
	v_add_f32_e32 v22, v22, v36
	v_add_f32_e32 v23, v23, v37
	v_exp_f32_e32 v36, v50
	v_exp_f32_e32 v50, v56
	v_pk_add_f32 v[22:23], v[22:23], v[22:23] op_sel:[0,1] op_sel_hi:[1,0]
	v_cvt_pk_bf16_f32 v120, v28, v45
	v_mov_b32_e32 v23, v51
	v_add_f32_e32 v38, v36, v50
	v_add_f32_e32 v22, v22, v38
	v_add_f32_e32 v23, v23, v39
	v_cvt_pk_bf16_f32 v121, v30, v47
	v_add_f32_e32 v22, v22, v23
	v_add_f32_e32 v138, v138, v22
	v_cvt_pk_bf16_f32 v122, v32, v49
	v_cvt_pk_bf16_f32 v123, v36, v51
	v_cvt_pk_bf16_f32 v124, v55, v19
	v_cvt_pk_bf16_f32 v125, v20, v25
	v_cvt_pk_bf16_f32 v126, v40, v27
	v_cvt_pk_bf16_f32 v127, v42, v29
	v_cvt_pk_bf16_f32 v128, v44, v31
	v_cvt_pk_bf16_f32 v129, v46, v33
	v_cvt_pk_bf16_f32 v130, v48, v37
	v_cvt_pk_bf16_f32 v131, v50, v39
	s_or_b64 exec, exec, s[22:23]
	s_and_saveexec_b64 s[22:23], s[4:5]
	s_cbranch_execnz .LBB0_578
	s_branch .LBB0_579

; #define LAS __attribute__((address_space(3)))
; __device__ __forceinline__ int crow(int r, int hi) { return (r & 3) + 8 * (r >> 2) + 4 * hi; }
; __device__ __forceinline__ unsigned cvtpk(float lo, float hi) { f32x2_t v = {lo, hi}; bf16x2_t b = __builtin_convertvector(v, bf16x2_t); return __builtin_bit_cast(unsigned, b); }
; __device__ __forceinline__ void at_dil(const Args& a, LAS unsigned char* lds, int layer) {
;     ...
;             for (int j = 0; j < 3; ++j) {
;                 const int tt = twlo + 2 - j;
;                 if (tt >= tt_lo) {
;                     f32x16 p0, p1;
;                     qkt(p0, p1, lds + L_K + tt * 8192, qr, -m_dil, r32, hi);
;                     const LAS float* tb = tab + (32 * wid + r32 + 192 - 64 * tt - 4 * hi - 63);
; #pragma unroll
;                     for (int r = 0; r < 16; ++r) { p0[r] += tb[63 - crow(r, 0)]; p1[r] += tb[31 - crow(r, 0)]; }
;                     exp_sum(p0, p1, l_part);
;                     pw[j][0] = (u32x4){cvtpk(p0[0], p0[1]), cvtpk(p0[2], p0[3]), cvtpk(p0[4], p0[5]), cvtpk(p0[6], p0[7])};
;                     pw[j][1] = (u32x4){cvtpk(p0[8], p0[9]), cvtpk(p0[10], p0[11]), cvtpk(p0[12], p0[13]), cvtpk(p0[14], p0[15])};
;                     pw[j][2] = (u32x4){cvtpk(p1[0], p1[1]), cvtpk(p1[2], p1[3]), cvtpk(p1[4], p1[5]), cvtpk(p1[6], p1[7])};
;                     pw[j][3] = (u32x4){cvtpk(p1[8], p1[9]), cvtpk(p1[10], p1[11]), cvtpk(p1[12], p1[13]), cvtpk(p1[14], p1[15])};
;                 }
.LBB0_573:
	s_nop 2
	v_add_u32_e32 v18, s48, v143
	v_add_u32_e32 v19, v144, v18
	ds_read_b128 v[36:39], v19
	ds_read_b128 v[54:57], v19 offset:4096
	v_add_u32_e32 v19, v142, v18
	ds_read_b128 v[58:61], v19
	ds_read_b128 v[62:65], v19 offset:4096
	v_add_u32_e32 v19, v141, v18
	v_add_u32_e32 v18, v140, v18
	ds_read_b128 v[84:87], v19
	ds_read_b128 v[92:95], v19 offset:4096
	ds_read_b128 v[100:103], v18
	ds_read_b128 v[108:111], v18 offset:4096
	s_waitcnt lgkmcnt(7)
	v_mfma_f32_32x32x16_bf16 v[18:33], v[36:39], v[68:71], v[2:17]
	v_add_lshl_u32 v53, v136, s43, 2
	s_waitcnt lgkmcnt(6)
	v_mfma_f32_32x32x16_bf16 v[36:51], v[54:57], v[68:71], v[2:17]
	s_waitcnt lgkmcnt(5)
	v_mfma_f32_32x32x16_bf16 v[18:33], v[58:61], v[72:75], v[18:33]
	v_add3_u32 v60, s75, v52, v53
	ds_read2_b32 v[52:53], v60 offset0:191 offset1:192
	ds_read2_b32 v[54:55], v60 offset0:189 offset1:190
	ds_read2_b32 v[56:57], v60 offset0:159 offset1:160
	ds_read2_b32 v[58:59], v60 offset0:157 offset1:158
	s_waitcnt lgkmcnt(8)
	v_mfma_f32_32x32x16_bf16 v[36:51], v[62:65], v[72:75], v[36:51]
	s_waitcnt lgkmcnt(7)
	v_mfma_f32_32x32x16_bf16 v[18:33], v[84:87], v[76:79], v[18:33]
	s_waitcnt lgkmcnt(6)
	v_mfma_f32_32x32x16_bf16 v[36:51], v[92:95], v[76:79], v[36:51]
	s_waitcnt lgkmcnt(5)
	v_mfma_f32_32x32x16_bf16 v[18:33], v[100:103], v[80:83], v[18:33]
	s_waitcnt lgkmcnt(4)
	v_mfma_f32_32x32x16_bf16 v[36:51], v[108:111], v[80:83], v[36:51]
	s_waitcnt lgkmcnt(3)
	s_nop 8
	v_add_f32_e32 v53, v18, v53
	v_add_f32_e32 v52, v19, v52
	ds_read2_b32 v[18:19], v60 offset0:183 offset1:184
	s_waitcnt lgkmcnt(3)
	v_add_f32_e32 v55, v20, v55
	v_add_f32_e32 v54, v21, v54
	ds_read2_b32 v[20:21], v60 offset0:181 offset1:182
	v_exp_f32_e32 v53, v53
	s_waitcnt lgkmcnt(3)
	v_add_f32_e32 v57, v36, v57
	v_add_f32_e32 v56, v37, v56
	ds_read2_b32 v[36:37], v60 offset0:151 offset1:152
	s_waitcnt lgkmcnt(3)
	v_add_f32_e32 v59, v38, v59
	v_add_f32_e32 v58, v39, v58
	ds_read2_b32 v[38:39], v60 offset0:149 offset1:150
	s_waitcnt lgkmcnt(3)
	v_add_f32_e32 v61, v22, v19
	s_waitcnt lgkmcnt(1)
	v_add_f32_e32 v37, v40, v37
	v_add_f32_e32 v40, v23, v18
	v_add_f32_e32 v36, v41, v36
	v_add_f32_e32 v41, v24, v21
	s_waitcnt lgkmcnt(0)
	v_add_f32_e32 v39, v42, v39
	ds_read2_b32 v[18:19], v60 offset0:175 offset1:176
	ds_read2_b32 v[22:23], v60 offset0:173 offset1:174
	v_add_f32_e32 v42, v25, v20
	ds_read2_b32 v[20:21], v60 offset0:143 offset1:144
	ds_read2_b32 v[24:25], v60 offset0:141 offset1:142
	v_add_f32_e32 v38, v43, v38
	s_waitcnt lgkmcnt(3)
	v_add_f32_e32 v43, v26, v19
	v_add_f32_e32 v62, v27, v18
	s_waitcnt lgkmcnt(1)
	v_add_f32_e32 v44, v44, v21
	v_add_f32_e32 v45, v45, v20
	ds_read2_b32 v[18:19], v60 offset0:167 offset1:168
	ds_read2_b32 v[20:21], v60 offset0:135 offset1:136
	v_add_f32_e32 v63, v28, v23
	v_add_f32_e32 v64, v29, v22
	ds_read2_b32 v[22:23], v60 offset0:165 offset1:166
	v_exp_f32_e32 v57, v57
	s_waitcnt lgkmcnt(3)
	v_add_f32_e32 v46, v46, v25
	v_add_f32_e32 v47, v47, v24
	s_waitcnt lgkmcnt(2)
	v_add_f32_e32 v65, v30, v19
	ds_read2_b32 v[24:25], v60 offset0:133 offset1:134
	s_waitcnt lgkmcnt(2)
	v_add_f32_e32 v48, v48, v21
	v_exp_f32_e32 v19, v52
	v_exp_f32_e32 v21, v56
	v_add_f32_e32 v60, v31, v18
	v_add_f32_e32 v49, v49, v20
	v_add_f32_e32 v18, v53, v57
	v_mov_b32_e32 v20, v35
	s_waitcnt lgkmcnt(1)
	v_add_f32_e32 v66, v32, v23
	v_add_f32_e32 v67, v33, v22
	v_exp_f32_e32 v52, v55
	v_exp_f32_e32 v55, v59
	v_add_f32_e32 v22, v18, v20
	v_add_f32_e32 v23, v19, v21
	v_exp_f32_e32 v18, v54
	s_waitcnt lgkmcnt(0)
	v_add_f32_e32 v50, v50, v25
	v_exp_f32_e32 v25, v58
	v_pk_add_f32 v[22:23], v[22:23], v[22:23] op_sel:[0,1] op_sel_hi:[1,0]
	v_add_f32_e32 v51, v51, v24
	v_add_f32_e32 v24, v52, v55
	v_mov_b32_e32 v23, v18
	v_exp_f32_e32 v20, v61
	v_exp_f32_e32 v54, v37
	v_add_f32_e32 v22, v22, v24
	v_add_f32_e32 v23, v23, v25
	v_exp_f32_e32 v24, v40
	v_exp_f32_e32 v27, v36
	v_pk_add_f32 v[22:23], v[22:23], v[22:23] op_sel:[0,1] op_sel_hi:[1,0]
	v_add_f32_e32 v26, v20, v54
	v_mov_b32_e32 v23, v24
	v_exp_f32_e32 v40, v41
	v_exp_f32_e32 v41, v39
	v_add_f32_e32 v22, v22, v26
	v_add_f32_e32 v23, v23, v27
	v_exp_f32_e32 v26, v42
	v_exp_f32_e32 v29, v38
	v_pk_add_f32 v[22:23], v[22:23], v[22:23] op_sel:[0,1] op_sel_hi:[1,0]
	v_add_f32_e32 v28, v40, v41
	v_mov_b32_e32 v23, v26
	v_exp_f32_e32 v42, v43
	v_exp_f32_e32 v43, v44
	v_add_f32_e32 v22, v22, v28
	v_add_f32_e32 v23, v23, v29
	v_exp_f32_e32 v28, v62
	v_exp_f32_e32 v31, v45
	v_pk_add_f32 v[22:23], v[22:23], v[22:23] op_sel:[0,1] op_sel_hi:[1,0]
	v_add_f32_e32 v30, v42, v43
	v_mov_b32_e32 v23, v28
	v_exp_f32_e32 v44, v63
	v_exp_f32_e32 v45, v46
	v_add_f32_e32 v22, v22, v30
	v_add_f32_e32 v23, v23, v31
	v_exp_f32_e32 v30, v64
	v_exp_f32_e32 v33, v47
	v_pk_add_f32 v[22:23], v[22:23], v[22:23] op_sel:[0,1] op_sel_hi:[1,0]
	v_add_f32_e32 v32, v44, v45
	v_mov_b32_e32 v23, v30
	v_exp_f32_e32 v46, v65
	v_exp_f32_e32 v47, v48
	v_add_f32_e32 v22, v22, v32
	v_add_f32_e32 v23, v23, v33
	v_exp_f32_e32 v32, v60
	v_exp_f32_e32 v37, v49
	v_pk_add_f32 v[22:23], v[22:23], v[22:23] op_sel:[0,1] op_sel_hi:[1,0]
	v_add_f32_e32 v36, v46, v47
	v_mov_b32_e32 v23, v32
	v_exp_f32_e32 v48, v66
	v_exp_f32_e32 v49, v50
	v_add_f32_e32 v22, v22, v36
	v_add_f32_e32 v23, v23, v37
	v_exp_f32_e32 v36, v67
	v_exp_f32_e32 v39, v51
	v_pk_add_f32 v[22:23], v[22:23], v[22:23] op_sel:[0,1] op_sel_hi:[1,0]
	v_add_f32_e32 v38, v48, v49
	v_mov_b32_e32 v23, v36
	v_add_f32_e32 v22, v22, v38
	v_add_f32_e32 v23, v23, v39
	v_cvt_pk_bf16_f32 v84, v53, v19
	v_add_f32_e32 v22, v22, v23
	v_add_f32_e32 v138, v138, v22
	v_cvt_pk_bf16_f32 v85, v52, v18
	v_cvt_pk_bf16_f32 v86, v20, v24
	v_cvt_pk_bf16_f32 v87, v40, v26
	v_cvt_pk_bf16_f32 v92, v42, v28
	v_cvt_pk_bf16_f32 v93, v44, v30
	v_cvt_pk_bf16_f32 v94, v46, v32
	v_cvt_pk_bf16_f32 v95, v48, v36
	v_cvt_pk_bf16_f32 v100, v57, v21
	v_cvt_pk_bf16_f32 v101, v55, v25
	v_cvt_pk_bf16_f32 v102, v54, v27
	v_cvt_pk_bf16_f32 v103, v41, v29
	v_cvt_pk_bf16_f32 v108, v43, v31
	v_cvt_pk_bf16_f32 v109, v45, v33
	v_cvt_pk_bf16_f32 v110, v47, v37
	v_cvt_pk_bf16_f32 v111, v49, v39

; #define LAS __attribute__((address_space(3)))
; __device__ __forceinline__ int crow(int r, int hi) { return (r & 3) + 8 * (r >> 2) + 4 * hi; }
; __device__ __forceinline__ unsigned cvtpk(float lo, float hi) { f32x2_t v = {lo, hi}; bf16x2_t b = __builtin_convertvector(v, bf16x2_t); return __builtin_bit_cast(unsigned, b); }
; __device__ __forceinline__ void at_dil(const Args& a, LAS unsigned char* lds, int layer) {
;     ...
;             for (int j = 0; j < 3; ++j) {
;                 const int tt = twlo + 2 - j;
;                 if (tt >= tt_lo) {
;                     f32x16 p0, p1;
;                     qkt(p0, p1, lds + L_K + tt * 8192, qr, -mt, r32, hi);
;                     const LAS float* tb = tab + (32 * wid + r32 + 192 - 64 * tt - 4 * hi - 63);
; #pragma unroll
;                     for (int r = 0; r < 16; ++r) { p0[r] += tb[63 - crow(r, 0)]; p1[r] += tb[31 - crow(r, 0)]; }
;                     exp_sum(p0, p1, l_part);
;                     pw[j][0] = (u32x4){cvtpk(p0[0], p0[1]), cvtpk(p0[2], p0[3]), cvtpk(p0[4], p0[5]), cvtpk(p0[6], p0[7])};
;                     pw[j][1] = (u32x4){cvtpk(p0[8], p0[9]), cvtpk(p0[10], p0[11]), cvtpk(p0[12], p0[13]), cvtpk(p0[14], p0[15])};
;                     pw[j][2] = (u32x4){cvtpk(p1[0], p1[1]), cvtpk(p1[2], p1[3]), cvtpk(p1[4], p1[5]), cvtpk(p1[6], p1[7])};
;                     pw[j][3] = (u32x4){cvtpk(p1[8], p1[9]), cvtpk(p1[10], p1[11]), cvtpk(p1[12], p1[13]), cvtpk(p1[14], p1[15])};
;                 }
.LBB0_590:
	v_add_u32_e32 v36, s48, v143
	v_add_u32_e32 v37, v144, v36
	ds_read_b128 v[52:55], v37
	ds_read_b128 v[84:87], v37 offset:4096
	v_add_u32_e32 v37, v142, v36
	ds_read_b128 v[92:95], v37
	ds_read_b128 v[100:103], v37 offset:4096
	v_add_u32_e32 v37, v141, v36
	v_add_u32_e32 v36, v140, v36
	ds_read_b128 v[108:111], v37
	ds_read_b128 v[146:149], v37 offset:4096
	ds_read_b128 v[150:153], v36
	ds_read_b128 v[154:157], v36 offset:4096
	s_waitcnt lgkmcnt(7)
	v_mfma_f32_32x32x16_bf16 v[36:51], v[52:55], v[68:71], v[18:33]
	s_waitcnt lgkmcnt(6)
	v_mfma_f32_32x32x16_bf16 v[52:67], v[84:87], v[68:71], v[18:33]
	v_lshlrev_b32_e32 v84, 2, v139
	v_add_lshl_u32 v85, v136, s43, 2
	s_waitcnt lgkmcnt(5)
	v_mfma_f32_32x32x16_bf16 v[36:51], v[92:95], v[72:75], v[36:51]
	s_waitcnt lgkmcnt(4)
	v_mfma_f32_32x32x16_bf16 v[52:67], v[100:103], v[72:75], v[52:67]
	v_add3_u32 v100, s75, v84, v85
	ds_read2_b32 v[84:85], v100 offset0:191 offset1:192
	ds_read2_b32 v[86:87], v100 offset0:189 offset1:190
	ds_read2_b32 v[92:93], v100 offset0:159 offset1:160
	ds_read2_b32 v[94:95], v100 offset0:157 offset1:158
	s_waitcnt lgkmcnt(7)
	v_mfma_f32_32x32x16_bf16 v[36:51], v[108:111], v[76:79], v[36:51]
	s_waitcnt lgkmcnt(6)
	v_mfma_f32_32x32x16_bf16 v[52:67], v[146:149], v[76:79], v[52:67]
	s_waitcnt lgkmcnt(5)
	v_mfma_f32_32x32x16_bf16 v[36:51], v[150:153], v[80:83], v[36:51]
	s_waitcnt lgkmcnt(4)
	v_mfma_f32_32x32x16_bf16 v[52:67], v[154:157], v[80:83], v[52:67]
	s_waitcnt lgkmcnt(3)
	s_nop 8
	v_add_f32_e32 v85, v36, v85
	v_add_f32_e32 v84, v37, v84
	ds_read2_b32 v[36:37], v100 offset0:183 offset1:184
	s_waitcnt lgkmcnt(3)
	v_add_f32_e32 v87, v38, v87
	v_add_f32_e32 v86, v39, v86
	ds_read2_b32 v[38:39], v100 offset0:181 offset1:182
	v_exp_f32_e32 v85, v85
	s_waitcnt lgkmcnt(3)
	v_add_f32_e32 v93, v52, v93
	v_add_f32_e32 v92, v53, v92
	ds_read2_b32 v[52:53], v100 offset0:151 offset1:152
	s_waitcnt lgkmcnt(3)
	v_add_f32_e32 v95, v54, v95
	v_add_f32_e32 v94, v55, v94
	ds_read2_b32 v[54:55], v100 offset0:149 offset1:150
	s_waitcnt lgkmcnt(3)
	v_add_f32_e32 v101, v40, v37
	s_waitcnt lgkmcnt(1)
	v_add_f32_e32 v53, v56, v53
	v_add_f32_e32 v56, v41, v36
	v_add_f32_e32 v52, v57, v52
	v_add_f32_e32 v57, v42, v39
	s_waitcnt lgkmcnt(0)
	v_add_f32_e32 v55, v58, v55
	ds_read2_b32 v[36:37], v100 offset0:175 offset1:176
	ds_read2_b32 v[40:41], v100 offset0:173 offset1:174
	v_add_f32_e32 v58, v43, v38
	ds_read2_b32 v[38:39], v100 offset0:143 offset1:144
	ds_read2_b32 v[42:43], v100 offset0:141 offset1:142
	v_add_f32_e32 v54, v59, v54
	s_waitcnt lgkmcnt(3)
	v_add_f32_e32 v59, v44, v37
	v_add_f32_e32 v102, v45, v36
	s_waitcnt lgkmcnt(1)
	v_add_f32_e32 v60, v60, v39
	v_add_f32_e32 v61, v61, v38
	ds_read2_b32 v[36:37], v100 offset0:167 offset1:168
	ds_read2_b32 v[38:39], v100 offset0:135 offset1:136
	v_add_f32_e32 v103, v46, v41
	v_add_f32_e32 v108, v47, v40
	ds_read2_b32 v[40:41], v100 offset0:165 offset1:166
	v_exp_f32_e32 v145, v93
	s_waitcnt lgkmcnt(3)
	v_add_f32_e32 v62, v62, v43
	v_add_f32_e32 v63, v63, v42
	s_waitcnt lgkmcnt(2)
	v_add_f32_e32 v109, v48, v37
	ds_read2_b32 v[42:43], v100 offset0:133 offset1:134
	s_waitcnt lgkmcnt(2)
	v_add_f32_e32 v64, v64, v39
	v_exp_f32_e32 v37, v84
	v_exp_f32_e32 v39, v92
	v_add_f32_e32 v100, v49, v36
	v_add_f32_e32 v65, v65, v38
	v_add_f32_e32 v36, v85, v145
	v_mov_b32_e32 v38, v35
	s_waitcnt lgkmcnt(1)
	v_add_f32_e32 v110, v50, v41
	v_add_f32_e32 v111, v51, v40
	v_exp_f32_e32 v87, v87
	v_exp_f32_e32 v146, v95
	v_add_f32_e32 v40, v36, v38
	v_add_f32_e32 v41, v37, v39
	v_exp_f32_e32 v36, v86
	s_waitcnt lgkmcnt(0)
	v_add_f32_e32 v66, v66, v43
	v_exp_f32_e32 v43, v94
	v_pk_add_f32 v[40:41], v[40:41], v[40:41] op_sel:[0,1] op_sel_hi:[1,0]
	v_add_f32_e32 v67, v67, v42
	v_add_f32_e32 v42, v87, v146
	v_mov_b32_e32 v41, v36
	v_exp_f32_e32 v38, v101
	v_exp_f32_e32 v147, v53
	v_add_f32_e32 v40, v40, v42
	v_add_f32_e32 v41, v41, v43
	v_exp_f32_e32 v42, v56
	v_exp_f32_e32 v45, v52
	v_pk_add_f32 v[40:41], v[40:41], v[40:41] op_sel:[0,1] op_sel_hi:[1,0]
	v_add_f32_e32 v44, v38, v147
	v_mov_b32_e32 v41, v42
	v_exp_f32_e32 v56, v57
	v_exp_f32_e32 v57, v55
	v_add_f32_e32 v40, v40, v44
	v_add_f32_e32 v41, v41, v45
	v_exp_f32_e32 v44, v58
	v_exp_f32_e32 v47, v54
	v_pk_add_f32 v[40:41], v[40:41], v[40:41] op_sel:[0,1] op_sel_hi:[1,0]
	v_add_f32_e32 v46, v56, v57
	v_mov_b32_e32 v41, v44
	v_exp_f32_e32 v58, v59
	v_exp_f32_e32 v59, v60
	v_add_f32_e32 v40, v40, v46
	v_add_f32_e32 v41, v41, v47
	v_exp_f32_e32 v46, v102
	v_exp_f32_e32 v49, v61
	v_pk_add_f32 v[40:41], v[40:41], v[40:41] op_sel:[0,1] op_sel_hi:[1,0]
	v_add_f32_e32 v48, v58, v59
	v_mov_b32_e32 v41, v46
	v_exp_f32_e32 v60, v103
	v_exp_f32_e32 v61, v62
	v_add_f32_e32 v40, v40, v48
	v_add_f32_e32 v41, v41, v49
	v_exp_f32_e32 v48, v108
	v_exp_f32_e32 v51, v63
	v_pk_add_f32 v[40:41], v[40:41], v[40:41] op_sel:[0,1] op_sel_hi:[1,0]
	v_add_f32_e32 v50, v60, v61
	v_mov_b32_e32 v41, v48
	v_exp_f32_e32 v62, v109
	v_exp_f32_e32 v63, v64
	v_add_f32_e32 v40, v40, v50
	v_add_f32_e32 v41, v41, v51
	v_exp_f32_e32 v50, v100
	v_exp_f32_e32 v53, v65
	v_pk_add_f32 v[40:41], v[40:41], v[40:41] op_sel:[0,1] op_sel_hi:[1,0]
	v_add_f32_e32 v52, v62, v63
	v_mov_b32_e32 v41, v50
	v_exp_f32_e32 v64, v110
	v_exp_f32_e32 v65, v66
	v_add_f32_e32 v40, v40, v52
	v_add_f32_e32 v41, v41, v53
	v_exp_f32_e32 v52, v111
	v_exp_f32_e32 v55, v67
	v_pk_add_f32 v[40:41], v[40:41], v[40:41] op_sel:[0,1] op_sel_hi:[1,0]
	v_add_f32_e32 v54, v64, v65
	v_mov_b32_e32 v41, v52
	v_add_f32_e32 v40, v40, v54
	v_add_f32_e32 v41, v41, v55
	v_cvt_pk_bf16_f32 v84, v85, v37
	v_add_f32_e32 v40, v40, v41
	v_add_f32_e32 v138, v138, v40
	v_cvt_pk_bf16_f32 v85, v87, v36
	v_cvt_pk_bf16_f32 v86, v38, v42
	v_cvt_pk_bf16_f32 v87, v56, v44
	v_cvt_pk_bf16_f32 v92, v58, v46
	v_cvt_pk_bf16_f32 v93, v60, v48
	v_cvt_pk_bf16_f32 v94, v62, v50
	v_cvt_pk_bf16_f32 v95, v64, v52
	v_cvt_pk_bf16_f32 v100, v145, v39
	v_cvt_pk_bf16_f32 v101, v146, v43
	v_cvt_pk_bf16_f32 v102, v147, v45
	v_cvt_pk_bf16_f32 v103, v57, v47
	v_cvt_pk_bf16_f32 v108, v59, v49
	v_cvt_pk_bf16_f32 v109, v61, v51
	v_cvt_pk_bf16_f32 v110, v63, v53
	v_cvt_pk_bf16_f32 v111, v65, v55
	s_cmp_lt_i32 s41, s54
	s_mov_b64 s[24:25], 0
	s_cbranch_scc0 .LBB0_568
	s_branch .LBB0_569

; __device__ __forceinline__ void at_dil(const Args& a, LAS unsigned char* lds, int layer) {
;     ...
;         const float l_run = other_half_sum(l_part);
;         const float oscale = 1.f / l_run, lse = ((dil_fixed ? m_dil : m_run) + __builtin_amdgcn_logf(l_run)) * LN2;
;         asm volatile("s_waitcnt lgkmcnt(0)\n\ts_barrier" ::: "memory");
;         {
;             const size_t rb = (size_t)b * S;
;             const int mw = 256 * nb2 + 32 * wid;
;             bf16_t* O = dilo + (((size_t)p * 6 + h) * NTOK + rb) * 64;
;             const size_t mw_row = (size_t)mw * dil + res;
;             store_o(o, oscale, lds, wid, lane, [&](int row) { return O + (mw_row + (size_t)row * dil) * 64; }, [&](int row) { return (const bf16_t*)nullptr; }, false);
;             if (hi == 0) dill[((size_t)p * 6 + h) * NTOK + rb + (size_t)(mw + r32) * dil + res] = lse;
;         }
.LBB0_598:
	v_mov_b32_e32 v34, v138
	s_nop 1
	v_permlane32_swap_b32_e32 v138, v34
	v_add_f32_e32 v54, v138, v34
	v_div_scale_f32 v34, s[24:25], v54, v54, 1.0
	v_rcp_f32_e32 v53, v34
	s_and_b64 s[24:25], s[20:21], exec
	s_cselect_b32 s27, 3, 15
	s_and_b64 s[24:25], s[16:17], exec
	v_fma_f32 v55, -v34, v53, 1.0
	v_fmac_f32_e32 v53, v55, v53
	v_div_scale_f32 v55, vcc, 1.0, v54, 1.0
	v_mul_f32_e32 v56, v55, v53
	v_fma_f32 v57, -v34, v56, v55
	v_fmac_f32_e32 v56, v57, v53
	s_sext_i32_i8 s26, s79
	v_fma_f32 v34, -v34, v56, v55
	s_mul_i32 s25, s94, 6
	s_cselect_b32 s24, 0, s27
	v_div_fmas_f32 v34, v34, v53, v56
	s_add_i32 s26, s25, s26
	s_and_b32 s28, s24, s78
	v_div_fixup_f32 v34, v34, v54, 1.0
	s_lshl_b32 s24, s95, 8
	s_ashr_i32 s27, s26, 31
	s_lshl_b64 s[18:19], s[18:19], 12
	s_add_i32 s24, s24, s43
	s_lshl_b64 s[26:27], s[26:27], 15
	v_mul_f32_e32 v36, v36, v34
	v_mul_f32_e32 v37, v37, v34
	v_mul_f32_e32 v38, v38, v34
	v_mul_f32_e32 v39, v39, v34
	s_add_u32 s18, s26, s18
	v_cvt_pk_bf16_f32 v36, v36, v37
	v_cvt_pk_bf16_f32 v37, v38, v39
	v_ashrrev_i32_e32 v38, 2, v135
	v_mul_f32_e32 v18, v18, v34
	v_mul_f32_e32 v19, v19, v34
	v_mul_f32_e32 v20, v20, v34
	v_mul_f32_e32 v21, v21, v34
	s_addc_u32 s19, s27, s19
	v_readlane_b32 s56, v252, 8
	v_mul_u32_u24_e32 v53, 0x90, v136
	v_and_b32_e32 v38, -8, v38
	v_cvt_pk_bf16_f32 v18, v18, v19
	v_cvt_pk_bf16_f32 v19, v20, v21
	v_mul_f32_e32 v20, v22, v34
	v_mul_f32_e32 v21, v23, v34
	v_mul_f32_e32 v22, v24, v34
	v_mul_f32_e32 v23, v25, v34
	s_lshl_b64 s[26:27], s[18:19], 7
	v_readlane_b32 s58, v252, 10
	v_add3_u32 v53, s45, v53, v38
	v_mul_f32_e32 v38, v40, v34
	v_mul_f32_e32 v39, v41, v34
	v_mul_f32_e32 v40, v42, v34
	v_mul_f32_e32 v41, v43, v34
	v_cvt_pk_bf16_f32 v20, v20, v21
	v_cvt_pk_bf16_f32 v21, v22, v23
	s_waitcnt lgkmcnt(0)
	s_barrier
	v_readlane_b32 s59, v252, 11
	s_add_u32 s26, s58, s26
	v_cvt_pk_bf16_f32 v38, v38, v39
	v_cvt_pk_bf16_f32 v39, v40, v41
	ds_write2_b64 v53, v[18:19], v[20:21] offset0:8 offset1:10
	v_mul_f32_e32 v18, v26, v34
	v_mul_f32_e32 v19, v27, v34
	v_mul_f32_e32 v20, v28, v34
	v_mul_f32_e32 v21, v29, v34
	s_addc_u32 s27, s59, s27
	s_ashr_i32 s25, s24, 31
	ds_write2_b64 v53, v[36:37], v[38:39] offset1:2
	v_mul_f32_e32 v36, v44, v34
	v_mul_f32_e32 v37, v45, v34
	v_mul_f32_e32 v38, v46, v34
	v_mul_f32_e32 v39, v47, v34
	v_cvt_pk_bf16_f32 v18, v18, v19
	v_cvt_pk_bf16_f32 v19, v20, v21
	v_mul_f32_e32 v20, v30, v34
	v_mul_f32_e32 v21, v31, v34
	v_mul_f32_e32 v22, v32, v34
	v_mul_f32_e32 v23, v33, v34
	s_and_b64 s[20:21], s[20:21], exec
	v_cvt_pk_bf16_f32 v36, v36, v37
	v_cvt_pk_bf16_f32 v37, v38, v39
	v_mul_f32_e32 v38, v48, v34
	v_mul_f32_e32 v39, v49, v34
	v_mul_f32_e32 v40, v50, v34
	v_mul_f32_e32 v41, v51, v34
	v_cvt_pk_bf16_f32 v20, v20, v21
	v_cvt_pk_bf16_f32 v21, v22, v23
	s_cselect_b32 s20, 2, 4
	s_and_b64 s[16:17], s[16:17], exec
	v_cvt_pk_bf16_f32 v38, v38, v39
	v_cvt_pk_bf16_f32 v39, v40, v41
	ds_write2_b64 v53, v[18:19], v[20:21] offset0:12 offset1:14
	v_lshlrev_b32_e32 v18, 4, v135
	s_movk_i32 s10, 0x90
	s_cselect_b32 s20, 0, s20
	ds_write2_b64 v53, v[36:37], v[38:39] offset0:4 offset1:6
	v_and_b32_e32 v34, 0x70, v18
	v_mul_lo_u32 v18, v52, s10
	s_lshl_b64 s[16:17], s[24:25], s20
	s_waitcnt lgkmcnt(0)
	v_add3_u32 v28, s45, v34, v18
	v_ashrrev_i32_e32 v53, 31, v52
	s_or_b32 s16, s16, s28
	ds_read_b128 v[18:21], v28
	v_lshlrev_b64 v[22:23], s20, v[52:53]
	v_lshl_add_u64 v[22:23], v[22:23], 0, s[16:17]
	v_lshlrev_b64 v[22:23], 7, v[22:23]
	v_lshl_add_u64 v[22:23], s[26:27], 0, v[22:23]
	v_lshl_add_u64 v[26:27], v[22:23], 0, v[34:35]
	ds_read_b128 v[22:25], v28 offset:1152
	s_waitcnt lgkmcnt(1)
	global_store_dwordx4 v[26:27], v[18:21], off
	v_cmp_gt_u32_e32 vcc, 32, v135
	v_readlane_b32 s57, v252, 9
	v_add_u32_e32 v18, 8, v52
	v_ashrrev_i32_e32 v19, 31, v18
	v_lshlrev_b64 v[18:19], s20, v[18:19]
	v_lshl_add_u64 v[18:19], v[18:19], 0, s[16:17]
	v_lshlrev_b64 v[18:19], 7, v[18:19]
	v_lshl_add_u64 v[18:19], s[26:27], 0, v[18:19]
	v_lshl_add_u64 v[18:19], v[18:19], 0, v[34:35]
	s_waitcnt lgkmcnt(0)
	global_store_dwordx4 v[18:19], v[22:25], off
	ds_read_b128 v[18:21], v28 offset:2304
	s_nop 0
	v_add_u32_e32 v22, 16, v52
	v_ashrrev_i32_e32 v23, 31, v22
	v_lshlrev_b64 v[22:23], s20, v[22:23]
	v_lshl_add_u64 v[22:23], v[22:23], 0, s[16:17]
	v_lshlrev_b64 v[22:23], 7, v[22:23]
	v_lshl_add_u64 v[22:23], s[26:27], 0, v[22:23]
	v_lshl_add_u64 v[26:27], v[22:23], 0, v[34:35]
	ds_read_b128 v[22:25], v28 offset:3456
	s_waitcnt lgkmcnt(1)
	global_store_dwordx4 v[26:27], v[18:21], off
	s_nop 1
	v_add_u32_e32 v18, 24, v52
	v_ashrrev_i32_e32 v19, 31, v18
	v_lshlrev_b64 v[18:19], s20, v[18:19]
	v_lshl_add_u64 v[18:19], v[18:19], 0, s[16:17]
	v_lshlrev_b64 v[18:19], 7, v[18:19]
	v_lshl_add_u64 v[18:19], s[26:27], 0, v[18:19]
	v_lshl_add_u64 v[18:19], v[18:19], 0, v[34:35]
	s_waitcnt lgkmcnt(0)
	global_store_dwordx4 v[18:19], v[22:25], off
	s_waitcnt lgkmcnt(0)
	s_and_saveexec_b64 s[16:17], vcc
	s_cbranch_execz .LBB0_546
	v_log_f32_e32 v18, v54
	s_lshl_b64 s[18:19], s[18:19], 2
	s_add_u32 s18, s82, s18
	s_addc_u32 s19, s83, s19
	v_add_f32_e32 v18, v137, v18
	v_mul_f32_e32 v20, 0x3f317218, v18
	v_or_b32_e32 v18, s24, v135
	v_ashrrev_i32_e32 v19, 31, v18
	v_lshlrev_b64 v[18:19], s20, v[18:19]
	v_lshl_add_u64 v[18:19], v[18:19], 2, s[18:19]
	s_lshl_b32 s66, s28, 2
	v_lshl_add_u64 v[18:19], v[18:19], 0, s[66:67]
	global_store_dword v[18:19], v20, off
	s_branch .LBB0_546
